# conv1: 3 workgroups per CU (weights of 5 k-steps resident, k5-8 loaded mid-phase), regenerated MFMA phases, hand-written epilogue; c2pvq proj preload
# baseline (speedup 1.0000x reference)
_Z11k_conv1_t14I3GeoILi64ELi16ELi3ELi2EEEvPKfPKDv8_DF16_S3_Pfiiii:
	s_load_dwordx2 s[34:35], s[0:1], 0x0
	s_load_dwordx4 s[16:19], s[0:1], 0x20
	s_lshl_b32 s5, s3, 3
	v_readfirstlane_b32 s12, v0
	s_lshl_b32 s57, s2, 6
	s_add_i32 s54, s5, -1
	s_lshr_b32 s20, s12, 6
	s_waitcnt lgkmcnt(0)
	s_mul_i32 s28, s17, s16
	s_add_i32 s24, s57, -1
	s_add_i32 s56, s16, -1
	s_lshl_b32 s55, s4, 6
	s_ashr_i32 s29, s28, 31
	s_add_i32 s10, s20, s54
	s_cmpk_gt_u32 s12, 0x23f
	s_cselect_b64 s[6:7], -1, 0
	s_and_b64 s[8:9], s[6:7], exec
	s_cselect_b32 s23, -9, 0
	s_cselect_b32 s8, 8, 0
	s_add_i32 s10, s10, s23
	s_max_i32 s9, s10, 0
	s_or_b32 s8, s8, s55
	s_min_i32 s9, s9, s56
	s_mul_i32 s8, s8, s16
	s_add_i32 s8, s9, s8
	s_mul_i32 s36, s8, s17
	s_ashr_i32 s37, s36, 31
	s_lshl_b64 s[30:31], s[28:29], 2
	s_cmpk_gt_u32 s12, 0x13f
	s_cselect_b64 s[8:9], -1, 0
	s_and_b64 s[10:11], s[8:9], exec
	s_cselect_b32 s10, -9, 0
	v_mov_b32_e32 v1, v0
	s_cselect_b32 s11, 8, 0
	s_add_i32 s22, s20, s10
	s_add_i32 s22, s22, 4
	v_and_b32_e32 v1, 63, v1
	s_add_i32 s10, s22, s54
	v_or_b32_e32 v2, s57, v1
	s_max_i32 s10, s10, 0
	s_or_b32 s11, s11, s55
	v_ashrrev_i32_e32 v3, 31, v2
	s_min_i32 s10, s10, s56
	s_mul_i32 s11, s11, s16
	v_lshl_add_u64 v[4:5], v[2:3], 2, s[34:35]
	s_add_i32 s10, s10, s11
	v_lshl_add_u64 v[6:7], s[36:37], 2, v[4:5]
	s_mul_i32 s38, s10, s17
	v_lshl_add_u64 v[8:9], v[6:7], 0, s[30:31]
	s_ashr_i32 s39, s38, 31
	v_lshl_add_u64 v[10:11], v[8:9], 0, s[30:31]
	s_cmp_lt_u32 s12, 64
	v_lshl_add_u64 v[12:13], v[10:11], 0, s[30:31]
	s_cselect_b64 s[10:11], -1, 0
	v_lshl_add_u64 v[14:15], v[12:13], 0, s[30:31]
	s_and_b64 s[14:15], s[10:11], exec
	v_lshl_add_u64 v[16:17], v[14:15], 0, s[30:31]
	s_cselect_b32 s13, 0, -9
	v_lshl_add_u64 v[18:19], v[16:17], 0, s[30:31]
	s_cselect_b32 s14, 0, 8
	s_add_i32 s21, s20, s13
	v_lshl_add_u64 v[20:21], v[18:19], 0, s[30:31]
	global_load_dword v44, v[6:7], off
	global_load_dword v43, v[8:9], off
	global_load_dword v34, v[10:11], off
	global_load_dword v35, v[12:13], off
	global_load_dword v30, v[14:15], off
	global_load_dword v31, v[16:17], off
	global_load_dword v32, v[18:19], off
	global_load_dword v33, v[20:21], off
	v_lshl_add_u64 v[6:7], s[38:39], 2, v[4:5]
	s_add_i32 s21, s21, 8
	v_lshl_add_u64 v[8:9], v[6:7], 0, s[30:31]
	s_add_i32 s13, s21, s54
	v_lshl_add_u64 v[10:11], v[8:9], 0, s[30:31]
	s_max_i32 s13, s13, 0
	s_or_b32 s14, s14, s55
	v_lshl_add_u64 v[12:13], v[10:11], 0, s[30:31]
	s_min_i32 s13, s13, s56
	s_mul_i32 s14, s14, s16
	v_lshl_add_u64 v[14:15], v[12:13], 0, s[30:31]
	s_add_i32 s13, s13, s14
	v_lshl_add_u64 v[16:17], v[14:15], 0, s[30:31]
	s_mul_i32 s40, s13, s17
	v_lshl_add_u64 v[18:19], v[16:17], 0, s[30:31]
	s_ashr_i32 s41, s40, 31
	s_add_i32 s58, s20, s5
	v_lshl_add_u64 v[20:21], v[18:19], 0, s[30:31]
	global_load_dword v42, v[6:7], off
	global_load_dword v41, v[8:9], off
	global_load_dword v28, v[10:11], off
	global_load_dword v29, v[12:13], off
	global_load_dword v24, v[14:15], off
	global_load_dword v25, v[16:17], off
	global_load_dword v26, v[18:19], off
	global_load_dword v27, v[20:21], off
	v_lshl_add_u64 v[6:7], s[40:41], 2, v[4:5]
	s_add_i32 s13, s58, 2
	v_lshl_add_u64 v[8:9], v[6:7], 0, s[30:31]
	s_max_i32 s13, s13, 0
	s_or_b32 s14, s55, 8
	v_lshl_add_u64 v[10:11], v[8:9], 0, s[30:31]
	s_min_i32 s13, s13, s56
	s_mul_i32 s59, s16, s14
	v_lshl_add_u64 v[12:13], v[10:11], 0, s[30:31]
	s_add_i32 s13, s13, s59
	v_lshl_add_u64 v[14:15], v[12:13], 0, s[30:31]
	s_mul_i32 s42, s13, s17
	v_lshl_add_u64 v[16:17], v[14:15], 0, s[30:31]
	s_ashr_i32 s43, s42, 31
	v_lshl_add_u64 v[36:37], v[16:17], 0, s[30:31]
	v_lshl_add_u64 v[4:5], s[42:43], 2, v[4:5]
	v_lshl_add_u64 v[46:47], v[36:37], 0, s[30:31]
	global_load_dword v40, v[6:7], off
	global_load_dword v39, v[8:9], off
	global_load_dword v22, v[10:11], off
	global_load_dword v23, v[12:13], off
	global_load_dword v18, v[14:15], off
	global_load_dword v19, v[16:17], off
	global_load_dword v20, v[36:37], off
	global_load_dword v21, v[46:47], off
	v_lshl_add_u64 v[6:7], v[4:5], 0, s[30:31]
	v_lshl_add_u64 v[8:9], v[6:7], 0, s[30:31]
	v_lshl_add_u64 v[10:11], v[8:9], 0, s[30:31]
	v_lshl_add_u64 v[46:47], v[10:11], 0, s[30:31]
	v_lshl_add_u64 v[48:49], v[46:47], 0, s[30:31]
	v_lshl_add_u64 v[50:51], v[48:49], 0, s[30:31]
	v_lshl_add_u64 v[52:53], v[50:51], 0, s[30:31]
	global_load_dword v38, v[4:5], off
	global_load_dword v37, v[6:7], off
	global_load_dword v16, v[8:9], off
	global_load_dword v17, v[10:11], off
	global_load_dword v12, v[46:47], off
	global_load_dword v13, v[48:49], off
	global_load_dword v14, v[50:51], off
	global_load_dword v15, v[52:53], off
	s_cmpk_gt_u32 s12, 0x7f
	s_cselect_b64 s[44:45], -1, 0
	s_and_b64 vcc, exec, s[44:45]
	s_cbranch_vccz .LBB4_2
	v_cmp_lt_u32_e32 vcc, 8, v1
	v_min_u32_e32 v3, 17, v1
	s_nop 0
	v_cndmask_b32_e64 v1, 0, -9, vcc
	v_add3_u32 v1, v3, s54, v1
	v_max_i32_e32 v1, 0, v1
	v_min_i32_e32 v4, s56, v1
	v_cndmask_b32_e64 v1, 0, 8, vcc
	v_or_b32_e32 v1, s55, v1
	v_mad_u64_u32 v[4:5], s[12:13], v1, s16, v[4:5]
	v_mul_lo_u32 v1, v4, s17
	s_max_i32 s12, s24, 0
	v_add_u32_e32 v4, s12, v1
	v_mov_b32_e32 v69, s12
	s_load_dwordx2 s[12:13], s[0:1], 0x8
	s_cbranch_execz .LBB4_3
	s_branch .LBB4_4

.LBB4_3:
	s_or_b32 s14, s5, s20
	s_or_b32 s14, s14, 6
	s_max_i32 s14, s14, 0
	s_min_i32 s14, s14, s56
	s_add_i32 s14, s14, s59
	s_mul_i32 s14, s14, s17
	v_add_u32_e32 v4, s14, v2
	s_max_i32 s14, s24, 0
	v_mov_b32_e32 v69, s14
.LBB4_4:
	v_ashrrev_i32_e32 v5, 31, v4
	v_lshl_add_u64 v[4:5], v[4:5], 2, s[34:35]
	v_lshlrev_b32_e32 v45, 5, v0
	v_lshl_add_u64 v[48:49], s[28:29], 2, v[4:5]
	v_and_b32_e32 v2, 0x7e0, v45
	v_mov_b32_e32 v3, 0
	v_lshl_add_u64 v[50:51], v[48:49], 0, s[30:31]
	s_waitcnt lgkmcnt(0)
	s_mov_b64 s[62:63], s[12:13]
	v_lshlrev_b32_e32 v96, 5, v0
	v_and_b32_e32 v96, 0x1fe0, v96
	v_lshl_add_u64 v[46:47], s[12:13], 0, v[2:3]
	v_lshl_add_u64 v[52:53], v[50:51], 0, s[30:31]
	v_and_b32_e32 v2, 0x1800, v45
	v_lshl_add_u64 v[54:55], v[52:53], 0, s[30:31]
	v_lshl_add_u64 v[138:139], v[46:47], 0, v[2:3]
	s_movk_i32 s12, 0x2000
	v_lshl_add_u64 v[56:57], v[54:55], 0, s[30:31]
	v_add_co_u32_e32 v46, vcc, s12, v138
	v_lshl_add_u64 v[58:59], v[56:57], 0, s[30:31]
	s_nop 0
	v_addc_co_u32_e32 v47, vcc, 0, v139, vcc
	s_movk_i32 s12, 0x4000
	v_lshl_add_u64 v[60:61], v[58:59], 0, s[30:31]
	global_load_dword v36, v[4:5], off
	global_load_dword v1, v[48:49], off
	global_load_dword v10, v[50:51], off
	global_load_dword v11, v[52:53], off
	global_load_dword v6, v[54:55], off
	global_load_dword v7, v[56:57], off
	global_load_dword v8, v[58:59], off
	global_load_dword v9, v[60:61], off
	global_load_dwordx4 v[130:133], v[138:139], off
	global_load_dwordx4 v[130:133], v[138:139], off
	global_load_dwordx4 v[130:133], v[138:139], off
	global_load_dwordx4 v[130:133], v[138:139], off
	global_load_dwordx4 v[130:133], v[138:139], off
	global_load_dwordx4 v[130:133], v[138:139], off
	global_load_dwordx4 v[130:133], v[138:139], off
	global_load_dwordx4 v[130:133], v[138:139], off
	global_load_dwordx4 v[130:133], v[138:139], off
	global_load_dwordx4 v[134:137], v[138:139], off offset:16
	global_load_dwordx4 v[122:125], v[46:47], off
	global_load_dwordx4 v[126:129], v[46:47], off offset:16
	v_add_co_u32_e32 v46, vcc, s12, v138
	s_movk_i32 s12, 0x6000
	s_nop 0
	v_addc_co_u32_e32 v47, vcc, 0, v139, vcc
	global_load_dwordx4 v[114:117], v[46:47], off
	global_load_dwordx4 v[118:121], v[46:47], off offset:16
	v_add_co_u32_e32 v46, vcc, s12, v138
	s_mov_b32 s12, 0x8000
	s_nop 0
	v_addc_co_u32_e32 v47, vcc, 0, v139, vcc
	global_load_dwordx4 v[106:109], v[46:47], off
	global_load_dwordx4 v[110:113], v[46:47], off offset:16
	v_add_co_u32_e32 v46, vcc, s12, v138
	s_mov_b32 s12, 0xa000
	s_nop 0
	v_addc_co_u32_e32 v47, vcc, 0, v139, vcc
	global_load_dwordx4 v[98:101], v[46:47], off
	global_load_dwordx4 v[102:105], v[46:47], off offset:16
	v_add_co_u32_e32 v46, vcc, s12, v138
	s_mov_b32 s12, 0xc000
	s_nop 0
	v_addc_co_u32_e32 v47, vcc, 0, v139, vcc
	v_add_co_u32_e32 v46, vcc, s12, v138
	s_mov_b32 s12, 0xe000
	s_nop 0
	v_addc_co_u32_e32 v47, vcc, 0, v139, vcc
	v_add_co_u32_e32 v46, vcc, s12, v138
	s_sub_i32 s15, 1, s5
	s_nop 0
	v_addc_co_u32_e32 v47, vcc, 0, v139, vcc
	v_add_co_u32_e32 v46, vcc, 0x10000, v138
	s_add_i32 s14, s23, s20
	s_nop 0
	v_addc_co_u32_e32 v47, vcc, 0, v139, vcc
	s_cmp_lt_i32 s14, s15
	s_cselect_b64 s[12:13], -1, 0
	v_mov_b32_e32 v45, v0
	s_and_b64 vcc, exec, s[12:13]
	s_cbranch_vccz .LBB4_6
	s_waitcnt vmcnt(57)
	v_mov_b32_e32 v44, 0
	s_waitcnt vmcnt(56)
	v_mov_b32_e32 v43, 0
	s_waitcnt vmcnt(55)
	v_mov_b32_e32 v34, 0
	s_waitcnt vmcnt(54)
	v_mov_b32_e32 v35, 0
	s_waitcnt vmcnt(53)
	v_mov_b32_e32 v30, 0
	s_waitcnt vmcnt(52)
	v_mov_b32_e32 v31, 0
	s_waitcnt vmcnt(51)
	v_mov_b32_e32 v32, 0
	s_waitcnt vmcnt(50)
	v_mov_b32_e32 v33, 0

.LBB4_20:
	s_or_b64 exec, exec, s[20:21]
	s_add_i32 s58, s58, 6
	s_load_dwordx2 s[20:21], s[0:1], 0x18
	s_max_i32 s0, s58, 0
	s_min_i32 s58, s0, s56
	s_lshl_b32 s0, s28, 4
	s_waitcnt vmcnt(24)
	v_mov_b32_e32 v1, v0
	s_waitcnt lgkmcnt(0)
	s_barrier
	s_ashr_i32 s1, s0, 31
	s_add_i32 s58, s58, s59
	s_lshl_b64 s[0:1], s[0:1], 2
	v_and_b32_e32 v1, 63, v1
	s_add_u32 s0, s34, s0
	s_waitcnt vmcnt(21)
	v_or_b32_e32 v6, s57, v1
	s_addc_u32 s1, s35, s1
	s_waitcnt vmcnt(20)
	v_ashrrev_i32_e32 v7, 31, v6
	s_waitcnt vmcnt(18)
	v_lshl_add_u64 v[8:9], v[6:7], 2, s[0:1]
	v_lshl_add_u64 v[10:11], s[36:37], 2, v[8:9]
	v_lshl_add_u64 v[12:13], v[10:11], 0, s[30:31]
	v_lshl_add_u64 v[14:15], v[12:13], 0, s[30:31]
	v_lshl_add_u64 v[16:17], v[14:15], 0, s[30:31]
	v_lshl_add_u64 v[18:19], v[16:17], 0, s[30:31]
	v_lshl_add_u64 v[20:21], v[18:19], 0, s[30:31]
	v_lshl_add_u64 v[22:23], v[20:21], 0, s[30:31]
	v_lshl_add_u64 v[24:25], v[22:23], 0, s[30:31]
	global_load_dword v79, v[10:11], off
	global_load_dword v78, v[12:13], off
	global_load_dword v66, v[14:15], off
	global_load_dword v67, v[16:17], off
	global_load_dword v164, v[18:19], off
	global_load_dword v165, v[20:21], off
	global_load_dword v166, v[22:23], off
	global_load_dword v167, v[24:25], off
	v_lshl_add_u64 v[10:11], s[38:39], 2, v[8:9]
	v_lshl_add_u64 v[12:13], v[10:11], 0, s[30:31]
	v_lshl_add_u64 v[14:15], v[12:13], 0, s[30:31]
	v_lshl_add_u64 v[16:17], v[14:15], 0, s[30:31]
	v_lshl_add_u64 v[18:19], v[16:17], 0, s[30:31]
	v_lshl_add_u64 v[20:21], v[18:19], 0, s[30:31]
	v_lshl_add_u64 v[22:23], v[20:21], 0, s[30:31]
	v_lshl_add_u64 v[24:25], v[22:23], 0, s[30:31]
	global_load_dword v77, v[10:11], off
	global_load_dword v76, v[12:13], off
	global_load_dword v162, v[14:15], off
	global_load_dword v163, v[16:17], off
	global_load_dword v158, v[18:19], off
	global_load_dword v159, v[20:21], off
	global_load_dword v160, v[22:23], off
	global_load_dword v161, v[24:25], off
	v_lshl_add_u64 v[10:11], s[40:41], 2, v[8:9]
	v_lshl_add_u64 v[12:13], v[10:11], 0, s[30:31]
	v_lshl_add_u64 v[14:15], v[12:13], 0, s[30:31]
	v_lshl_add_u64 v[16:17], v[14:15], 0, s[30:31]
	v_lshl_add_u64 v[18:19], v[16:17], 0, s[30:31]
	v_lshl_add_u64 v[20:21], v[18:19], 0, s[30:31]
	v_lshl_add_u64 v[22:23], v[20:21], 0, s[30:31]
	v_lshl_add_u64 v[8:9], s[42:43], 2, v[8:9]
	v_lshl_add_u64 v[24:25], v[22:23], 0, s[30:31]
	global_load_dword v75, v[10:11], off
	global_load_dword v74, v[12:13], off
	global_load_dword v156, v[14:15], off
	global_load_dword v157, v[16:17], off
	global_load_dword v152, v[18:19], off
	global_load_dword v153, v[20:21], off
	global_load_dword v154, v[22:23], off
	global_load_dword v155, v[24:25], off
	v_lshl_add_u64 v[10:11], v[8:9], 0, s[30:31]
	v_lshl_add_u64 v[12:13], v[10:11], 0, s[30:31]
	v_lshl_add_u64 v[14:15], v[12:13], 0, s[30:31]
	v_lshl_add_u64 v[16:17], v[14:15], 0, s[30:31]
	v_lshl_add_u64 v[18:19], v[16:17], 0, s[30:31]
	v_lshl_add_u64 v[20:21], v[18:19], 0, s[30:31]
	v_lshl_add_u64 v[22:23], v[20:21], 0, s[30:31]
	global_load_dword v73, v[8:9], off
	global_load_dword v72, v[10:11], off
	global_load_dword v150, v[12:13], off
	global_load_dword v151, v[14:15], off
	global_load_dword v146, v[16:17], off
	global_load_dword v147, v[18:19], off
	global_load_dword v148, v[20:21], off
	global_load_dword v149, v[22:23], off
	s_and_b64 vcc, exec, s[44:45]
	s_cbranch_vccz .LBB4_22
	v_cmp_lt_u32_e32 vcc, 8, v1
	v_min_u32_e32 v7, 17, v1
	s_nop 0
	v_cndmask_b32_e64 v1, 0, -9, vcc
	v_add3_u32 v1, v7, s54, v1
	v_max_i32_e32 v1, 0, v1
	v_min_i32_e32 v8, s56, v1
	v_cndmask_b32_e64 v1, 0, 8, vcc
	v_or_b32_e32 v1, s55, v1
	v_mad_u64_u32 v[8:9], s[46:47], v1, s16, v[8:9]
	v_mul_lo_u32 v1, v8, s17
	v_add_u32_e32 v8, v1, v69
	s_mul_i32 s58, s58, s17
	s_cbranch_execz .LBB4_23
	s_branch .LBB4_24

.LBB4_24:
	v_ashrrev_i32_e32 v9, 31, v8
	v_lshl_add_u64 v[6:7], v[8:9], 2, s[0:1]
	v_lshl_add_u64 v[8:9], s[28:29], 2, v[6:7]
	v_lshl_add_u64 v[10:11], v[8:9], 0, s[30:31]
	v_lshl_add_u64 v[12:13], v[10:11], 0, s[30:31]
	v_lshl_add_u64 v[14:15], v[12:13], 0, s[30:31]
	v_lshl_add_u64 v[16:17], v[14:15], 0, s[30:31]
	v_lshl_add_u64 v[18:19], v[16:17], 0, s[30:31]
	v_lshl_add_u64 v[20:21], v[18:19], 0, s[30:31]
	global_load_dword v71, v[6:7], off
	global_load_dword v70, v[8:9], off
	global_load_dword v144, v[10:11], off
	global_load_dword v145, v[12:13], off
	global_load_dword v140, v[14:15], off
	global_load_dword v141, v[16:17], off
	global_load_dword v142, v[18:19], off
	global_load_dword v143, v[20:21], off
	v_and_b32_e32 v68, 31, v0
	v_and_b32_e32 v1, 32, v0
	s_movk_i32 s46, 0x50
	v_mad_u32_u24 v1, v68, s46, v1
	ds_read_b128 v[80:83], v1
	ds_read_b128 v[84:87], v1 offset:16
	ds_read_b128 v[88:91], v1 offset:10400
	ds_read_b128 v[92:95], v1 offset:10416
	s_waitcnt vmcnt(48) lgkmcnt(3)
	v_mfma_f32_32x32x16_f16 v[50:65], v[134:137], v[80:83], 0
	s_waitcnt lgkmcnt(2)
	v_mfma_f32_32x32x16_f16 v[50:65], v[130:133], v[84:87], v[50:65]
	v_mfma_f32_32x32x16_f16 v[50:65], v[130:133], v[80:83], v[50:65]
	ds_read_b128 v[80:83], v1 offset:20800
	ds_read_b128 v[84:87], v1 offset:20816
	s_waitcnt lgkmcnt(3)
	v_mfma_f32_32x32x16_f16 v[34:49], v[134:137], v[88:91], 0
	s_waitcnt lgkmcnt(2)
	v_mfma_f32_32x32x16_f16 v[34:49], v[130:133], v[92:95], v[34:49]
	v_mfma_f32_32x32x16_f16 v[34:49], v[130:133], v[88:91], v[34:49]
	ds_read_b128 v[88:91], v1 offset:31200
	ds_read_b128 v[92:95], v1 offset:31216
	s_waitcnt lgkmcnt(3)
	v_mfma_f32_32x32x16_f16 v[18:33], v[134:137], v[80:83], 0
	s_waitcnt lgkmcnt(2)
	v_mfma_f32_32x32x16_f16 v[18:33], v[130:133], v[84:87], v[18:33]
	v_mfma_f32_32x32x16_f16 v[18:33], v[130:133], v[80:83], v[18:33]
	ds_read_b128 v[80:83], v1 offset:2640
	ds_read_b128 v[84:87], v1 offset:2656
	s_waitcnt lgkmcnt(3)
	v_mfma_f32_32x32x16_f16 v[2:17], v[134:137], v[88:91], 0
	s_waitcnt lgkmcnt(2)
	v_mfma_f32_32x32x16_f16 v[2:17], v[130:133], v[92:95], v[2:17]
	v_mfma_f32_32x32x16_f16 v[2:17], v[130:133], v[88:91], v[2:17]
	ds_read_b128 v[88:91], v1 offset:13040
	ds_read_b128 v[92:95], v1 offset:13056
	s_waitcnt vmcnt(46) lgkmcnt(3)
	v_mfma_f32_32x32x16_f16 v[50:65], v[126:129], v[80:83], v[50:65]
	s_waitcnt lgkmcnt(2)
	v_mfma_f32_32x32x16_f16 v[50:65], v[122:125], v[84:87], v[50:65]
	v_mfma_f32_32x32x16_f16 v[50:65], v[122:125], v[80:83], v[50:65]
	ds_read_b128 v[80:83], v1 offset:23440
	ds_read_b128 v[84:87], v1 offset:23456
	s_waitcnt lgkmcnt(3)
	v_mfma_f32_32x32x16_f16 v[34:49], v[126:129], v[88:91], v[34:49]
	s_waitcnt lgkmcnt(2)
	v_mfma_f32_32x32x16_f16 v[34:49], v[122:125], v[92:95], v[34:49]
	v_mfma_f32_32x32x16_f16 v[34:49], v[122:125], v[88:91], v[34:49]
	ds_read_b128 v[88:91], v1 offset:33840
	ds_read_b128 v[92:95], v1 offset:33856
	s_waitcnt lgkmcnt(3)
	v_mfma_f32_32x32x16_f16 v[18:33], v[126:129], v[80:83], v[18:33]
	s_waitcnt lgkmcnt(2)
	v_mfma_f32_32x32x16_f16 v[18:33], v[122:125], v[84:87], v[18:33]
	v_mfma_f32_32x32x16_f16 v[18:33], v[122:125], v[80:83], v[18:33]
	ds_read_b128 v[80:83], v1 offset:80
	ds_read_b128 v[84:87], v1 offset:96
	s_waitcnt lgkmcnt(3)
	v_mfma_f32_32x32x16_f16 v[2:17], v[126:129], v[88:91], v[2:17]
	s_waitcnt lgkmcnt(2)
	v_mfma_f32_32x32x16_f16 v[2:17], v[122:125], v[92:95], v[2:17]
	v_mfma_f32_32x32x16_f16 v[2:17], v[122:125], v[88:91], v[2:17]
	ds_read_b128 v[88:91], v1 offset:10480
	ds_read_b128 v[92:95], v1 offset:10496
	s_waitcnt vmcnt(44) lgkmcnt(3)
	v_mfma_f32_32x32x16_f16 v[50:65], v[118:121], v[80:83], v[50:65]
	s_waitcnt lgkmcnt(2)
	v_mfma_f32_32x32x16_f16 v[50:65], v[114:117], v[84:87], v[50:65]
	v_mfma_f32_32x32x16_f16 v[50:65], v[114:117], v[80:83], v[50:65]
	ds_read_b128 v[80:83], v1 offset:20880
	ds_read_b128 v[84:87], v1 offset:20896
	s_waitcnt lgkmcnt(3)
	v_mfma_f32_32x32x16_f16 v[34:49], v[118:121], v[88:91], v[34:49]
	s_waitcnt lgkmcnt(2)
	v_mfma_f32_32x32x16_f16 v[34:49], v[114:117], v[92:95], v[34:49]
	v_mfma_f32_32x32x16_f16 v[34:49], v[114:117], v[88:91], v[34:49]
	ds_read_b128 v[88:91], v1 offset:31280
	ds_read_b128 v[92:95], v1 offset:31296
	s_waitcnt lgkmcnt(3)
	v_mfma_f32_32x32x16_f16 v[18:33], v[118:121], v[80:83], v[18:33]
	s_waitcnt lgkmcnt(2)
	v_mfma_f32_32x32x16_f16 v[18:33], v[114:117], v[84:87], v[18:33]
	v_mfma_f32_32x32x16_f16 v[18:33], v[114:117], v[80:83], v[18:33]
	ds_read_b128 v[80:83], v1 offset:5200
	ds_read_b128 v[84:87], v1 offset:5216
	s_waitcnt lgkmcnt(3)
	v_mfma_f32_32x32x16_f16 v[2:17], v[118:121], v[88:91], v[2:17]
	s_waitcnt lgkmcnt(2)
	v_mfma_f32_32x32x16_f16 v[2:17], v[114:117], v[92:95], v[2:17]
	v_mfma_f32_32x32x16_f16 v[2:17], v[114:117], v[88:91], v[2:17]
	s_add_u32 s64, s62, 0xa000
	s_addc_u32 s65, s63, 0
	global_load_dwordx4 v[130:133], v96, s[64:65]
	global_load_dwordx4 v[134:137], v96, s[64:65] offset:16
	s_add_u32 s64, s62, 0xc000
	s_addc_u32 s65, s63, 0
	global_load_dwordx4 v[122:125], v96, s[64:65]
	global_load_dwordx4 v[126:129], v96, s[64:65] offset:16
	s_add_u32 s64, s62, 0xe000
	s_addc_u32 s65, s63, 0
	global_load_dwordx4 v[114:117], v96, s[64:65]
	global_load_dwordx4 v[118:121], v96, s[64:65] offset:16
	ds_read_b128 v[88:91], v1 offset:15600
	ds_read_b128 v[92:95], v1 offset:15616
	s_waitcnt vmcnt(48) lgkmcnt(3)
	v_mfma_f32_32x32x16_f16 v[50:65], v[110:113], v[80:83], v[50:65]
	s_waitcnt lgkmcnt(2)
	v_mfma_f32_32x32x16_f16 v[50:65], v[106:109], v[84:87], v[50:65]
	v_mfma_f32_32x32x16_f16 v[50:65], v[106:109], v[80:83], v[50:65]
	ds_read_b128 v[80:83], v1 offset:26000
	ds_read_b128 v[84:87], v1 offset:26016
	s_waitcnt lgkmcnt(3)
	v_mfma_f32_32x32x16_f16 v[34:49], v[110:113], v[88:91], v[34:49]
	s_waitcnt lgkmcnt(2)
	v_mfma_f32_32x32x16_f16 v[34:49], v[106:109], v[92:95], v[34:49]
	v_mfma_f32_32x32x16_f16 v[34:49], v[106:109], v[88:91], v[34:49]
	ds_read_b128 v[88:91], v1 offset:36400
	ds_read_b128 v[92:95], v1 offset:36416
	s_waitcnt lgkmcnt(3)
	v_mfma_f32_32x32x16_f16 v[18:33], v[110:113], v[80:83], v[18:33]
	s_waitcnt lgkmcnt(2)
	v_mfma_f32_32x32x16_f16 v[18:33], v[106:109], v[84:87], v[18:33]
	v_mfma_f32_32x32x16_f16 v[18:33], v[106:109], v[80:83], v[18:33]
	ds_read_b128 v[80:83], v1 offset:7840
	ds_read_b128 v[84:87], v1 offset:7856
	s_waitcnt lgkmcnt(3)
	v_mfma_f32_32x32x16_f16 v[2:17], v[110:113], v[88:91], v[2:17]
	s_waitcnt lgkmcnt(2)
	v_mfma_f32_32x32x16_f16 v[2:17], v[106:109], v[92:95], v[2:17]
	v_mfma_f32_32x32x16_f16 v[2:17], v[106:109], v[88:91], v[2:17]
	s_add_u32 s64, s62, 0x10000
	s_addc_u32 s65, s63, 0
	global_load_dwordx4 v[106:109], v96, s[64:65]
	global_load_dwordx4 v[110:113], v96, s[64:65] offset:16
	ds_read_b128 v[88:91], v1 offset:18240
	ds_read_b128 v[92:95], v1 offset:18256
	s_waitcnt vmcnt(48) lgkmcnt(3)
	v_mfma_f32_32x32x16_f16 v[50:65], v[102:105], v[80:83], v[50:65]
	s_waitcnt lgkmcnt(2)
	v_mfma_f32_32x32x16_f16 v[50:65], v[98:101], v[84:87], v[50:65]
	v_mfma_f32_32x32x16_f16 v[50:65], v[98:101], v[80:83], v[50:65]
	ds_read_b128 v[80:83], v1 offset:28640
	ds_read_b128 v[84:87], v1 offset:28656
	s_waitcnt lgkmcnt(3)
	v_mfma_f32_32x32x16_f16 v[34:49], v[102:105], v[88:91], v[34:49]
	s_waitcnt lgkmcnt(2)
	v_mfma_f32_32x32x16_f16 v[34:49], v[98:101], v[92:95], v[34:49]
	v_mfma_f32_32x32x16_f16 v[34:49], v[98:101], v[88:91], v[34:49]
	ds_read_b128 v[88:91], v1 offset:39040
	ds_read_b128 v[92:95], v1 offset:39056
	s_waitcnt lgkmcnt(3)
	v_mfma_f32_32x32x16_f16 v[18:33], v[102:105], v[80:83], v[18:33]
	s_waitcnt lgkmcnt(2)
	v_mfma_f32_32x32x16_f16 v[18:33], v[98:101], v[84:87], v[18:33]
	v_mfma_f32_32x32x16_f16 v[18:33], v[98:101], v[80:83], v[18:33]
	ds_read_b128 v[80:83], v1 offset:5280
	ds_read_b128 v[84:87], v1 offset:5296
	s_waitcnt lgkmcnt(3)
	v_mfma_f32_32x32x16_f16 v[2:17], v[102:105], v[88:91], v[2:17]
	s_waitcnt lgkmcnt(2)
	v_mfma_f32_32x32x16_f16 v[2:17], v[98:101], v[92:95], v[2:17]
	v_mfma_f32_32x32x16_f16 v[2:17], v[98:101], v[88:91], v[2:17]
	ds_read_b128 v[88:91], v1 offset:15680
	ds_read_b128 v[92:95], v1 offset:15696
	s_waitcnt vmcnt(6) lgkmcnt(3)
	v_mfma_f32_32x32x16_f16 v[50:65], v[134:137], v[80:83], v[50:65]
	s_waitcnt lgkmcnt(2)
	v_mfma_f32_32x32x16_f16 v[50:65], v[130:133], v[84:87], v[50:65]
	v_mfma_f32_32x32x16_f16 v[50:65], v[130:133], v[80:83], v[50:65]
	ds_read_b128 v[80:83], v1 offset:26080
	ds_read_b128 v[84:87], v1 offset:26096
	s_waitcnt lgkmcnt(3)
	v_mfma_f32_32x32x16_f16 v[34:49], v[134:137], v[88:91], v[34:49]
	s_waitcnt lgkmcnt(2)
	v_mfma_f32_32x32x16_f16 v[34:49], v[130:133], v[92:95], v[34:49]
	v_mfma_f32_32x32x16_f16 v[34:49], v[130:133], v[88:91], v[34:49]
	ds_read_b128 v[88:91], v1 offset:36480
	ds_read_b128 v[92:95], v1 offset:36496
	s_waitcnt lgkmcnt(3)
	v_mfma_f32_32x32x16_f16 v[18:33], v[134:137], v[80:83], v[18:33]
	s_waitcnt lgkmcnt(2)
	v_mfma_f32_32x32x16_f16 v[18:33], v[130:133], v[84:87], v[18:33]
	v_mfma_f32_32x32x16_f16 v[18:33], v[130:133], v[80:83], v[18:33]
	ds_read_b128 v[80:83], v1 offset:10400
	ds_read_b128 v[84:87], v1 offset:10416
	s_waitcnt lgkmcnt(3)
	v_mfma_f32_32x32x16_f16 v[2:17], v[134:137], v[88:91], v[2:17]
	s_waitcnt lgkmcnt(2)
	v_mfma_f32_32x32x16_f16 v[2:17], v[130:133], v[92:95], v[2:17]
	v_mfma_f32_32x32x16_f16 v[2:17], v[130:133], v[88:91], v[2:17]
	ds_read_b128 v[88:91], v1 offset:20800
	ds_read_b128 v[92:95], v1 offset:20816
	s_waitcnt vmcnt(4) lgkmcnt(3)
	v_mfma_f32_32x32x16_f16 v[50:65], v[126:129], v[80:83], v[50:65]
	s_waitcnt lgkmcnt(2)
	v_mfma_f32_32x32x16_f16 v[50:65], v[122:125], v[84:87], v[50:65]
	v_mfma_f32_32x32x16_f16 v[50:65], v[122:125], v[80:83], v[50:65]
	ds_read_b128 v[80:83], v1 offset:31200
	ds_read_b128 v[84:87], v1 offset:31216
	s_waitcnt lgkmcnt(3)
	v_mfma_f32_32x32x16_f16 v[34:49], v[126:129], v[88:91], v[34:49]
	s_waitcnt lgkmcnt(2)
	v_mfma_f32_32x32x16_f16 v[34:49], v[122:125], v[92:95], v[34:49]
	v_mfma_f32_32x32x16_f16 v[34:49], v[122:125], v[88:91], v[34:49]
	ds_read_b128 v[88:91], v1 offset:41600
	ds_read_b128 v[92:95], v1 offset:41616
	s_waitcnt lgkmcnt(3)
	v_mfma_f32_32x32x16_f16 v[18:33], v[126:129], v[80:83], v[18:33]
	s_waitcnt lgkmcnt(2)
	v_mfma_f32_32x32x16_f16 v[18:33], v[122:125], v[84:87], v[18:33]
	v_mfma_f32_32x32x16_f16 v[18:33], v[122:125], v[80:83], v[18:33]
	ds_read_b128 v[80:83], v1 offset:13040
	ds_read_b128 v[84:87], v1 offset:13056
	s_waitcnt lgkmcnt(3)
	v_mfma_f32_32x32x16_f16 v[2:17], v[126:129], v[88:91], v[2:17]
	s_waitcnt lgkmcnt(2)
	v_mfma_f32_32x32x16_f16 v[2:17], v[122:125], v[92:95], v[2:17]
	v_mfma_f32_32x32x16_f16 v[2:17], v[122:125], v[88:91], v[2:17]
	ds_read_b128 v[88:91], v1 offset:23440
	ds_read_b128 v[92:95], v1 offset:23456
	s_waitcnt vmcnt(2) lgkmcnt(3)
	v_mfma_f32_32x32x16_f16 v[50:65], v[118:121], v[80:83], v[50:65]
	s_waitcnt lgkmcnt(2)
	v_mfma_f32_32x32x16_f16 v[50:65], v[114:117], v[84:87], v[50:65]
	v_mfma_f32_32x32x16_f16 v[50:65], v[114:117], v[80:83], v[50:65]
	ds_read_b128 v[80:83], v1 offset:33840
	ds_read_b128 v[84:87], v1 offset:33856
	s_waitcnt lgkmcnt(3)
	v_mfma_f32_32x32x16_f16 v[34:49], v[118:121], v[88:91], v[34:49]
	s_waitcnt lgkmcnt(2)
	v_mfma_f32_32x32x16_f16 v[34:49], v[114:117], v[92:95], v[34:49]
	v_mfma_f32_32x32x16_f16 v[34:49], v[114:117], v[88:91], v[34:49]
	ds_read_b128 v[88:91], v1 offset:44240
	ds_read_b128 v[92:95], v1 offset:44256
	s_waitcnt lgkmcnt(3)
	v_mfma_f32_32x32x16_f16 v[18:33], v[118:121], v[80:83], v[18:33]
	s_waitcnt lgkmcnt(2)
	v_mfma_f32_32x32x16_f16 v[18:33], v[114:117], v[84:87], v[18:33]
	v_mfma_f32_32x32x16_f16 v[18:33], v[114:117], v[80:83], v[18:33]
	ds_read_b128 v[80:83], v1 offset:10480
	ds_read_b128 v[84:87], v1 offset:10496
	s_waitcnt lgkmcnt(3)
	v_mfma_f32_32x32x16_f16 v[2:17], v[118:121], v[88:91], v[2:17]
	s_waitcnt lgkmcnt(2)
	v_mfma_f32_32x32x16_f16 v[2:17], v[114:117], v[92:95], v[2:17]
	v_mfma_f32_32x32x16_f16 v[2:17], v[114:117], v[88:91], v[2:17]
	ds_read_b128 v[88:91], v1 offset:20880
	ds_read_b128 v[92:95], v1 offset:20896
	s_waitcnt vmcnt(0) lgkmcnt(3)
	v_mfma_f32_32x32x16_f16 v[50:65], v[110:113], v[80:83], v[50:65]
	s_waitcnt lgkmcnt(2)
	v_mfma_f32_32x32x16_f16 v[50:65], v[106:109], v[84:87], v[50:65]
	v_mfma_f32_32x32x16_f16 v[50:65], v[106:109], v[80:83], v[50:65]
	ds_read_b128 v[80:83], v1 offset:31280
	ds_read_b128 v[84:87], v1 offset:31296
	s_waitcnt lgkmcnt(3)
	v_mfma_f32_32x32x16_f16 v[34:49], v[110:113], v[88:91], v[34:49]
	s_waitcnt lgkmcnt(2)
	v_mfma_f32_32x32x16_f16 v[34:49], v[106:109], v[92:95], v[34:49]
	v_mfma_f32_32x32x16_f16 v[34:49], v[106:109], v[88:91], v[34:49]
	ds_read_b128 v[88:91], v1 offset:41680
	ds_read_b128 v[92:95], v1 offset:41696
	s_waitcnt lgkmcnt(3)
	v_mfma_f32_32x32x16_f16 v[18:33], v[110:113], v[80:83], v[18:33]
	s_waitcnt lgkmcnt(2)
	v_mfma_f32_32x32x16_f16 v[18:33], v[106:109], v[84:87], v[18:33]
	v_mfma_f32_32x32x16_f16 v[18:33], v[106:109], v[80:83], v[18:33]
	s_waitcnt lgkmcnt(1)
	v_mfma_f32_32x32x16_f16 v[2:17], v[110:113], v[88:91], v[2:17]
	s_waitcnt lgkmcnt(0)
	v_mfma_f32_32x32x16_f16 v[2:17], v[106:109], v[92:95], v[2:17]
	v_mfma_f32_32x32x16_f16 v[2:17], v[106:109], v[88:91], v[2:17]
	s_add_u32 s64, s62, 0x12000
	s_addc_u32 s65, s63, 0
	global_load_dwordx4 v[130:133], v96, s[64:65]
	global_load_dwordx4 v[134:137], v96, s[64:65] offset:16
	s_add_u32 s64, s62, 0x14000
	s_addc_u32 s65, s63, 0
	global_load_dwordx4 v[122:125], v96, s[64:65]
	global_load_dwordx4 v[126:129], v96, s[64:65] offset:16
	s_add_u32 s64, s62, 0x16000
	s_addc_u32 s65, s63, 0
	global_load_dwordx4 v[114:117], v96, s[64:65]
	global_load_dwordx4 v[118:121], v96, s[64:65] offset:16
	s_add_u32 s64, s62, 0x18000
	s_addc_u32 s65, s63, 0
	global_load_dwordx4 v[106:109], v96, s[64:65]
	global_load_dwordx4 v[110:113], v96, s[64:65] offset:16
	s_add_u32 s64, s62, 0x1a000
	s_addc_u32 s65, s63, 0
	global_load_dwordx4 v[98:101], v96, s[64:65]
	global_load_dwordx4 v[102:105], v96, s[64:65] offset:16
	v_cndmask_b32_e64 v81, 0, 1, s[12:13]
	v_mov_b32_e32 v80, v0
	v_cmp_ne_u32_e64 s[0:1], 1, v81
	s_andn2_b64 vcc, exec, s[12:13]
	s_barrier
	s_cbranch_vccnz .LBB4_26
	s_waitcnt vmcnt(57)
	v_mov_b32_e32 v79, 0
	s_waitcnt vmcnt(56)
	v_mov_b32_e32 v78, 0
	s_waitcnt vmcnt(55)
	v_mov_b32_e32 v66, 0
	s_waitcnt vmcnt(54)
	v_mov_b32_e32 v67, v79
	s_waitcnt vmcnt(53)
	v_mov_b32_e32 v164, 0
	s_waitcnt vmcnt(52)
	v_mov_b32_e32 v165, v79
	s_waitcnt vmcnt(51)
	v_mov_b32_e32 v166, 0
	s_waitcnt vmcnt(50)
	v_mov_b32_e32 v167, v79
.LBB4_26:
	v_and_b32_e32 v81, 63, v80
	v_add_u32_e32 v82, 1, v81
	v_and_b32_e32 v80, 1, v80
	v_lshrrev_b32_e32 v82, 1, v82
	v_add_u32_e32 v83, 33, v82
	v_cmp_eq_u32_e32 vcc, 0, v80
	s_nop 1
	v_cndmask_b32_e32 v82, v82, v83, vcc
	v_mov_b32_e32 v83, s33
	v_mad_u32_u24 v92, v82, s46, v83
	s_mov_b32 s46, 0x41800000
	s_waitcnt vmcnt(54)
	v_pk_mul_f32 v[84:85], v[66:67], s[46:47] op_sel_hi:[1,0]
	v_mul_u32_u24_e32 v80, 0x50, v82
	v_cvt_pk_f16_f32 v87, v84, v85
	v_cvt_f32_f16_e32 v84, v87
	v_cvt_f32_f16_sdwa v85, v87 dst_sel:DWORD dst_unused:UNUSED_PAD src0_sel:WORD_1
	v_fma_mixlo_f16 v82, v79, s46, 0
	v_mul_f32_e32 v83, 0x41800000, v79
	v_fma_mixlo_f16 v82, v79, s46, -v82 op_sel_hi:[0,0,1]
	v_mul_f32_e32 v79, 0x41800000, v78
	v_fma_mixlo_f16 v88, v78, s46, 0
	v_cvt_pk_f16_f32 v86, v83, v79
	v_fma_mixhi_f16 v82, v78, s46, -v88 op_sel_hi:[0,0,1]
	s_waitcnt vmcnt(52)
	v_pk_mul_f32 v[78:79], v[164:165], s[46:47] op_sel_hi:[1,0]
	v_pk_fma_f32 v[66:67], v[66:67], s[46:47], v[84:85] op_sel_hi:[1,0,1] neg_lo:[0,0,1] neg_hi:[0,0,1]
	v_cvt_pk_f16_f32 v88, v78, v79
	s_waitcnt vmcnt(50)
	v_pk_mul_f32 v[84:85], v[166:167], s[46:47] op_sel_hi:[1,0]
	v_cvt_f32_f16_e32 v78, v88
	v_cvt_f32_f16_sdwa v79, v88 dst_sel:DWORD dst_unused:UNUSED_PAD src0_sel:WORD_1
	v_cvt_pk_f16_f32 v89, v84, v85
	v_cvt_f32_f16_e32 v90, v89
	v_cvt_f32_f16_sdwa v91, v89 dst_sel:DWORD dst_unused:UNUSED_PAD src0_sel:WORD_1
	v_pk_fma_f32 v[164:165], v[164:165], s[46:47], v[78:79] op_sel_hi:[1,0,1] neg_lo:[0,0,1] neg_hi:[0,0,1]
	v_cvt_pk_f16_f32 v83, v66, v67
	v_cvt_pk_f16_f32 v84, v164, v165
	v_pk_fma_f32 v[164:165], v[166:167], s[46:47], v[90:91] op_sel_hi:[1,0,1] neg_lo:[0,0,1] neg_hi:[0,0,1]
	s_andn2_b64 vcc, exec, s[6:7]
	v_cvt_pk_f16_f32 v85, v164, v165
	v_cndmask_b32_e64 v164, 0, 1, s[6:7]
	v_cmp_ne_u32_e64 s[12:13], 1, v164
	ds_write_b128 v92, v[86:89]
	ds_write_b128 v92, v[82:85] offset:16
	s_cbranch_vccnz .LBB4_28
	s_waitcnt vmcnt(49)
	v_mov_b32_e32 v77, 0
	s_waitcnt vmcnt(48)
	v_mov_b32_e32 v76, 0
	s_waitcnt vmcnt(47)
	v_mov_b32_e32 v162, 0
	s_waitcnt vmcnt(46)
	v_mov_b32_e32 v163, v77
	s_waitcnt vmcnt(45)
	v_mov_b32_e32 v158, 0
	s_waitcnt vmcnt(44)
	v_mov_b32_e32 v159, v77
	s_waitcnt vmcnt(43)
	v_mov_b32_e32 v160, 0
	s_waitcnt vmcnt(42)
	v_mov_b32_e32 v161, v77
.LBB4_28:
	s_waitcnt vmcnt(46)
	v_pk_mul_f32 v[166:167], v[162:163], s[46:47] op_sel_hi:[1,0]
	v_fma_mixlo_f16 v164, v77, s46, 0
	v_cvt_pk_f16_f32 v83, v166, v167
	v_cvt_f32_f16_e32 v166, v83
	v_cvt_f32_f16_sdwa v167, v83 dst_sel:DWORD dst_unused:UNUSED_PAD src0_sel:WORD_1
	v_mul_f32_e32 v165, 0x41800000, v77
	v_fma_mixlo_f16 v164, v77, s46, -v164 op_sel_hi:[0,0,1]
	v_mul_f32_e32 v66, 0x41800000, v76
	v_fma_mixlo_f16 v67, v76, s46, 0
	v_pk_fma_f32 v[162:163], v[162:163], s[46:47], v[166:167] op_sel_hi:[1,0,1] neg_lo:[0,0,1] neg_hi:[0,0,1]
	s_waitcnt vmcnt(44)
	v_pk_mul_f32 v[166:167], v[158:159], s[46:47] op_sel_hi:[1,0]
	v_cvt_pk_f16_f32 v82, v165, v66
	v_fma_mixhi_f16 v164, v76, s46, -v67 op_sel_hi:[0,0,1]
	v_cvt_pk_f16_f32 v84, v166, v167
	s_waitcnt vmcnt(42)
	v_pk_mul_f32 v[66:67], v[160:161], s[46:47] op_sel_hi:[1,0]
	v_cvt_f32_f16_e32 v166, v84
	v_cvt_f32_f16_sdwa v167, v84 dst_sel:DWORD dst_unused:UNUSED_PAD src0_sel:WORD_1
	v_cvt_pk_f16_f32 v85, v66, v67
	v_cvt_f32_f16_e32 v66, v85
	v_cvt_f32_f16_sdwa v67, v85 dst_sel:DWORD dst_unused:UNUSED_PAD src0_sel:WORD_1
	v_pk_fma_f32 v[158:159], v[158:159], s[46:47], v[166:167] op_sel_hi:[1,0,1] neg_lo:[0,0,1] neg_hi:[0,0,1]
	v_add_u32_e32 v78, s50, v80
	v_cvt_pk_f16_f32 v166, v158, v159
	v_pk_fma_f32 v[158:159], v[160:161], s[46:47], v[66:67] op_sel_hi:[1,0,1] neg_lo:[0,0,1] neg_hi:[0,0,1]
	v_cvt_pk_f16_f32 v165, v162, v163
	v_cvt_pk_f16_f32 v167, v158, v159
	v_cndmask_b32_e64 v158, 0, 1, s[8:9]
	v_cmp_ne_u32_e64 s[6:7], 1, v158
	s_andn2_b64 vcc, exec, s[8:9]
	ds_write_b128 v78, v[82:85]
	ds_write_b128 v78, v[164:167] offset:16
	s_cbranch_vccnz .LBB4_30
	s_waitcnt vmcnt(41)
	v_mov_b32_e32 v75, 0
	s_waitcnt vmcnt(40)
	v_mov_b32_e32 v74, 0
	s_waitcnt vmcnt(39)
	v_mov_b32_e32 v156, 0
	s_waitcnt vmcnt(38)
	v_mov_b32_e32 v157, v75
	s_waitcnt vmcnt(37)
	v_mov_b32_e32 v152, 0
	s_waitcnt vmcnt(36)
	v_mov_b32_e32 v153, v75
	s_waitcnt vmcnt(35)
	v_mov_b32_e32 v154, 0
	s_waitcnt vmcnt(34)
	v_mov_b32_e32 v155, v75
.LBB4_30:
	s_waitcnt vmcnt(38)
	v_pk_mul_f32 v[160:161], v[156:157], s[46:47] op_sel_hi:[1,0]
	v_fma_mixlo_f16 v158, v75, s46, 0
	v_cvt_pk_f16_f32 v163, v160, v161
	v_cvt_f32_f16_e32 v160, v163
	v_cvt_f32_f16_sdwa v161, v163 dst_sel:DWORD dst_unused:UNUSED_PAD src0_sel:WORD_1
	v_fma_mixlo_f16 v158, v75, s46, -v158 op_sel_hi:[0,0,1]
	v_fma_mixlo_f16 v164, v74, s46, 0
	v_fma_mixhi_f16 v158, v74, s46, -v164 op_sel_hi:[0,0,1]
	v_pk_fma_f32 v[156:157], v[156:157], s[46:47], v[160:161] op_sel_hi:[1,0,1] neg_lo:[0,0,1] neg_hi:[0,0,1]
	s_waitcnt vmcnt(36)
	v_pk_mul_f32 v[160:161], v[152:153], s[46:47] op_sel_hi:[1,0]
	s_waitcnt vmcnt(34)
	v_pk_mul_f32 v[166:167], v[154:155], s[46:47] op_sel_hi:[1,0]
	v_cvt_pk_f16_f32 v164, v160, v161
	v_cvt_f32_f16_e32 v160, v164
	v_cvt_f32_f16_sdwa v161, v164 dst_sel:DWORD dst_unused:UNUSED_PAD src0_sel:WORD_1
	v_cvt_pk_f16_f32 v165, v166, v167
	v_cvt_f32_f16_e32 v166, v165
	v_cvt_f32_f16_sdwa v167, v165 dst_sel:DWORD dst_unused:UNUSED_PAD src0_sel:WORD_1
	v_pk_fma_f32 v[152:153], v[152:153], s[46:47], v[160:161] op_sel_hi:[1,0,1] neg_lo:[0,0,1] neg_hi:[0,0,1]
	v_mul_f32_e32 v159, 0x41800000, v75
	v_cvt_pk_f16_f32 v160, v152, v153
	v_pk_fma_f32 v[152:153], v[154:155], s[46:47], v[166:167] op_sel_hi:[1,0,1] neg_lo:[0,0,1] neg_hi:[0,0,1]
	v_mul_f32_e32 v162, 0x41800000, v74
	v_cvt_pk_f16_f32 v161, v152, v153
	v_cndmask_b32_e64 v152, 0, 1, s[10:11]
	v_add_u32_e32 v66, s51, v80
	v_cvt_pk_f16_f32 v162, v159, v162
	v_cvt_pk_f16_f32 v159, v156, v157
	v_cmp_ne_u32_e64 s[8:9], 1, v152
	s_andn2_b64 vcc, exec, s[10:11]
	ds_write_b128 v66, v[162:165]
	ds_write_b128 v66, v[158:161] offset:16
	s_cbranch_vccnz .LBB4_32
	s_waitcnt vmcnt(33)
	v_mov_b32_e32 v73, 0
	s_waitcnt vmcnt(32)
	v_mov_b32_e32 v72, 0
	s_waitcnt vmcnt(31)
	v_mov_b32_e32 v150, 0
	s_waitcnt vmcnt(30)
	v_mov_b32_e32 v151, v73
	s_waitcnt vmcnt(29)
	v_mov_b32_e32 v146, 0
	s_waitcnt vmcnt(28)
	v_mov_b32_e32 v147, v73
	s_waitcnt vmcnt(27)
	v_mov_b32_e32 v148, 0
	s_waitcnt vmcnt(26)
	v_mov_b32_e32 v149, v73
.LBB4_32:
	s_waitcnt vmcnt(30)
	v_pk_mul_f32 v[154:155], v[150:151], s[46:47] op_sel_hi:[1,0]
	v_fma_mixlo_f16 v152, v73, s46, 0
	v_cvt_pk_f16_f32 v157, v154, v155
	v_cvt_f32_f16_e32 v154, v157
	v_cvt_f32_f16_sdwa v155, v157 dst_sel:DWORD dst_unused:UNUSED_PAD src0_sel:WORD_1
	v_fma_mixlo_f16 v152, v73, s46, -v152 op_sel_hi:[0,0,1]
	v_fma_mixlo_f16 v158, v72, s46, 0
	v_fma_mixhi_f16 v152, v72, s46, -v158 op_sel_hi:[0,0,1]
	v_pk_fma_f32 v[150:151], v[150:151], s[46:47], v[154:155] op_sel_hi:[1,0,1] neg_lo:[0,0,1] neg_hi:[0,0,1]
	s_waitcnt vmcnt(28)
	v_pk_mul_f32 v[154:155], v[146:147], s[46:47] op_sel_hi:[1,0]
	s_waitcnt vmcnt(26)
	v_pk_mul_f32 v[160:161], v[148:149], s[46:47] op_sel_hi:[1,0]
	v_cvt_pk_f16_f32 v158, v154, v155
	v_cvt_f32_f16_e32 v154, v158
	v_cvt_f32_f16_sdwa v155, v158 dst_sel:DWORD dst_unused:UNUSED_PAD src0_sel:WORD_1
	v_cvt_pk_f16_f32 v159, v160, v161
	v_cvt_f32_f16_e32 v160, v159
	v_cvt_f32_f16_sdwa v161, v159 dst_sel:DWORD dst_unused:UNUSED_PAD src0_sel:WORD_1
	v_pk_fma_f32 v[146:147], v[146:147], s[46:47], v[154:155] op_sel_hi:[1,0,1] neg_lo:[0,0,1] neg_hi:[0,0,1]
	v_mul_f32_e32 v153, 0x41800000, v73
	v_cvt_pk_f16_f32 v154, v146, v147
	v_pk_fma_f32 v[146:147], v[148:149], s[46:47], v[160:161] op_sel_hi:[1,0,1] neg_lo:[0,0,1] neg_hi:[0,0,1]
	v_mul_f32_e32 v156, 0x41800000, v72
	v_cvt_pk_f16_f32 v155, v146, v147
	v_cndmask_b32_e64 v146, 0, 1, s[44:45]
	v_add_u32_e32 v162, s52, v80
	v_cvt_pk_f16_f32 v156, v153, v156
	v_cvt_pk_f16_f32 v153, v150, v151
	v_cmp_ne_u32_e64 s[10:11], 1, v146
	s_andn2_b64 vcc, exec, s[44:45]
	ds_write_b128 v162, v[156:159] offset:32
	ds_write_b128 v162, v[152:155] offset:48
	s_cbranch_vccnz .LBB4_34
	v_cmp_lt_u32_e32 vcc, 8, v81
	v_min_u32_e32 v146, 17, v81
	s_movk_i32 s44, 0x1450
	v_cndmask_b32_e64 v147, 0, -9, vcc
	v_add_u32_e32 v147, v147, v146
	v_cndmask_b32_e64 v146, 0, 32, vcc
	v_cmp_lt_i32_e32 vcc, s5, v147
	s_and_b64 s[46:47], s[24:25], vcc
	v_cmp_gt_u32_e32 vcc, 18, v81
	v_mad_i32_i24 v146, v147, s44, v146
	s_and_b64 s[48:49], s[26:27], vcc
	s_cbranch_execz .LBB4_35
	s_branch .LBB4_36
.LBB4_34:
.LBB4_35:
	s_andn2_b64 s[44:45], s[46:47], exec
	s_and_b64 s[46:47], s[22:23], exec
	v_add_u32_e32 v146, s53, v80
	s_or_b64 s[46:47], s[44:45], s[46:47]
	s_or_b64 s[48:49], s[48:49], exec
.LBB4_36:
	s_and_saveexec_b64 s[44:45], s[48:49]
	s_cbranch_execz .LBB4_40
	s_xor_b64 s[48:49], s[46:47], -1
	s_and_saveexec_b64 s[46:47], s[48:49]
	s_cbranch_execz .LBB4_39
	s_waitcnt vmcnt(24)
	v_mov_b32_e32 v70, 0
	v_mov_b32_e32 v71, 0
	s_waitcnt vmcnt(23)
	v_mov_b32_e32 v144, 0
	s_waitcnt vmcnt(22)
	v_mov_b32_e32 v145, v70
	s_waitcnt vmcnt(21)
	v_mov_b32_e32 v140, 0
	s_waitcnt vmcnt(20)
	v_mov_b32_e32 v141, v70
	s_waitcnt vmcnt(19)
	v_mov_b32_e32 v142, 0
	s_waitcnt vmcnt(18)
	v_mov_b32_e32 v143, v70
.LBB4_39:
	s_or_b64 exec, exec, s[46:47]
	s_mov_b32 s46, 0x41800000
	s_waitcnt vmcnt(22)
	v_pk_mul_f32 v[150:151], v[144:145], s[46:47] op_sel_hi:[1,0]
	v_fma_mixlo_f16 v148, v71, s46, 0
	v_cvt_pk_f16_f32 v153, v150, v151
	v_cvt_f32_f16_e32 v150, v153
	v_cvt_f32_f16_sdwa v151, v153 dst_sel:DWORD dst_unused:UNUSED_PAD src0_sel:WORD_1
	v_fma_mixlo_f16 v148, v71, s46, -v148 op_sel_hi:[0,0,1]
	v_fma_mixlo_f16 v154, v70, s46, 0
	v_fma_mixhi_f16 v148, v70, s46, -v154 op_sel_hi:[0,0,1]
	v_pk_fma_f32 v[144:145], v[144:145], s[46:47], v[150:151] op_sel_hi:[1,0,1] neg_lo:[0,0,1] neg_hi:[0,0,1]
	s_waitcnt vmcnt(20)
	v_pk_mul_f32 v[150:151], v[140:141], s[46:47] op_sel_hi:[1,0]
	s_waitcnt vmcnt(18)
	v_pk_mul_f32 v[156:157], v[142:143], s[46:47] op_sel_hi:[1,0]
	v_cvt_pk_f16_f32 v154, v150, v151
	v_cvt_f32_f16_e32 v150, v154
	v_cvt_f32_f16_sdwa v151, v154 dst_sel:DWORD dst_unused:UNUSED_PAD src0_sel:WORD_1
	v_cvt_pk_f16_f32 v155, v156, v157
	v_cvt_f32_f16_e32 v156, v155
	v_cvt_f32_f16_sdwa v157, v155 dst_sel:DWORD dst_unused:UNUSED_PAD src0_sel:WORD_1
	v_mul_f32_e32 v147, 0x41800000, v71
	v_mul_f32_e32 v149, 0x41800000, v70
	v_pk_fma_f32 v[140:141], v[140:141], s[46:47], v[150:151] op_sel_hi:[1,0,1] neg_lo:[0,0,1] neg_hi:[0,0,1]
	v_cvt_pk_f16_f32 v152, v147, v149
	v_cvt_pk_f16_f32 v150, v140, v141
	v_pk_fma_f32 v[140:141], v[142:143], s[46:47], v[156:157] op_sel_hi:[1,0,1] neg_lo:[0,0,1] neg_hi:[0,0,1]
	v_cvt_pk_f16_f32 v149, v144, v145
	v_cvt_pk_f16_f32 v151, v140, v141
	ds_write_b128 v146, v[152:155]
	ds_write_b128 v146, v[148:151] offset:16
.LBB4_40:
	s_or_b64 exec, exec, s[44:45]
	s_lshl_b32 s44, s28, 5
	s_waitcnt vmcnt(21)
	v_mov_b32_e32 v140, v0
	s_ashr_i32 s45, s44, 31
	s_waitcnt lgkmcnt(0)
	s_barrier
	s_lshl_b64 s[44:45], s[44:45], 2
	s_waitcnt vmcnt(19)
	v_and_b32_e32 v142, 63, v140
	s_add_u32 s44, s34, s44
	v_or_b32_e32 v140, s57, v142
	s_addc_u32 s45, s35, s45
	v_ashrrev_i32_e32 v141, 31, v140
	v_lshl_add_u64 v[144:145], v[140:141], 2, s[44:45]
	v_lshl_add_u64 v[146:147], s[36:37], 2, v[144:145]
	v_lshl_add_u64 v[148:149], v[146:147], 0, s[30:31]
	v_lshl_add_u64 v[150:151], v[148:149], 0, s[30:31]
	v_lshl_add_u64 v[152:153], v[150:151], 0, s[30:31]
	v_lshl_add_u64 v[154:155], v[152:153], 0, s[30:31]
	v_lshl_add_u64 v[156:157], v[154:155], 0, s[30:31]
	v_lshl_add_u64 v[158:159], v[156:157], 0, s[30:31]
	v_lshl_add_u64 v[160:161], v[158:159], 0, s[30:31]
	global_load_dword v79, v[146:147], off
	global_load_dword v78, v[148:149], off
	global_load_dword v66, v[150:151], off
	global_load_dword v67, v[152:153], off
	global_load_dword v164, v[154:155], off
	global_load_dword v165, v[156:157], off
	global_load_dword v166, v[158:159], off
	global_load_dword v167, v[160:161], off
	v_lshl_add_u64 v[146:147], s[38:39], 2, v[144:145]
	v_lshl_add_u64 v[148:149], v[146:147], 0, s[30:31]
	v_lshl_add_u64 v[150:151], v[148:149], 0, s[30:31]
	v_lshl_add_u64 v[152:153], v[150:151], 0, s[30:31]
	v_lshl_add_u64 v[154:155], v[152:153], 0, s[30:31]
	v_lshl_add_u64 v[156:157], v[154:155], 0, s[30:31]
	v_lshl_add_u64 v[160:161], v[156:157], 0, s[30:31]
	v_lshl_add_u64 v[70:71], v[160:161], 0, s[30:31]
	global_load_dword v77, v[146:147], off
	global_load_dword v76, v[148:149], off
	global_load_dword v162, v[150:151], off
	global_load_dword v163, v[152:153], off
	global_load_dword v158, v[154:155], off
	global_load_dword v159, v[156:157], off
	s_nop 0
	global_load_dword v160, v[160:161], off
	s_nop 0
	global_load_dword v161, v[70:71], off
	v_lshl_add_u64 v[146:147], s[40:41], 2, v[144:145]
	v_lshl_add_u64 v[148:149], v[146:147], 0, s[30:31]
	v_lshl_add_u64 v[150:151], v[148:149], 0, s[30:31]
	v_lshl_add_u64 v[152:153], v[150:151], 0, s[30:31]
	v_lshl_add_u64 v[154:155], v[152:153], 0, s[30:31]
	v_lshl_add_u64 v[70:71], v[154:155], 0, s[30:31]
	v_lshl_add_u64 v[72:73], v[70:71], 0, s[30:31]
	v_lshl_add_u64 v[144:145], s[42:43], 2, v[144:145]
	v_lshl_add_u64 v[80:81], v[72:73], 0, s[30:31]
	global_load_dword v75, v[146:147], off
	global_load_dword v74, v[148:149], off
	global_load_dword v156, v[150:151], off
	global_load_dword v157, v[152:153], off
	s_nop 0
	global_load_dword v152, v[154:155], off
	global_load_dword v153, v[70:71], off
	s_nop 0
	global_load_dword v154, v[72:73], off
	global_load_dword v155, v[80:81], off
	v_lshl_add_u64 v[146:147], v[144:145], 0, s[30:31]
	v_lshl_add_u64 v[148:149], v[146:147], 0, s[30:31]
	v_lshl_add_u64 v[70:71], v[148:149], 0, s[30:31]
	v_lshl_add_u64 v[80:81], v[70:71], 0, s[30:31]
	v_lshl_add_u64 v[82:83], v[80:81], 0, s[30:31]
	v_lshl_add_u64 v[84:85], v[82:83], 0, s[30:31]
	v_lshl_add_u64 v[86:87], v[84:85], 0, s[30:31]
	global_load_dword v73, v[144:145], off
	global_load_dword v72, v[146:147], off
	global_load_dword v150, v[148:149], off
	global_load_dword v151, v[70:71], off
	s_nop 0
	global_load_dword v146, v[80:81], off
	global_load_dword v147, v[82:83], off
	global_load_dword v148, v[84:85], off
	global_load_dword v149, v[86:87], off
	s_and_b64 vcc, exec, s[10:11]
	s_cbranch_vccnz .LBB4_42
	v_cmp_lt_u32_e32 vcc, 8, v142
	v_min_u32_e32 v141, 17, v142
	s_nop 0
	v_cndmask_b32_e64 v142, 0, -9, vcc
	v_add3_u32 v141, v141, s54, v142
	v_max_i32_e32 v141, 0, v141
	v_min_i32_e32 v142, s56, v141
	v_cndmask_b32_e64 v141, 0, 8, vcc
	v_or_b32_e32 v141, s55, v141
	s_waitcnt vmcnt(50)
	v_mad_u64_u32 v[142:143], s[46:47], v141, s16, v[142:143]
	v_mul_lo_u32 v141, v142, s17
	v_add_u32_e32 v142, v141, v69
	s_cbranch_execz .LBB4_43
	s_branch .LBB4_44

.LBB4_44:
	s_waitcnt vmcnt(50)
	v_ashrrev_i32_e32 v143, 31, v142
	v_lshl_add_u64 v[140:141], v[142:143], 2, s[44:45]
	v_lshl_add_u64 v[142:143], s[28:29], 2, v[140:141]
	v_lshl_add_u64 v[144:145], v[142:143], 0, s[30:31]
	v_lshl_add_u64 v[80:81], v[144:145], 0, s[30:31]
	v_lshl_add_u64 v[82:83], v[80:81], 0, s[30:31]
	v_lshl_add_u64 v[84:85], v[82:83], 0, s[30:31]
	v_lshl_add_u64 v[86:87], v[84:85], 0, s[30:31]
	v_lshl_add_u64 v[88:89], v[86:87], 0, s[30:31]
	global_load_dword v71, v[140:141], off
	global_load_dword v70, v[142:143], off
	s_nop 0
	global_load_dword v144, v[144:145], off
	s_nop 0
	global_load_dword v145, v[80:81], off
	global_load_dword v140, v[82:83], off
	global_load_dword v141, v[84:85], off
	global_load_dword v142, v[86:87], off
	global_load_dword v143, v[88:89], off
	ds_read_b128 v[80:83], v1
	ds_read_b128 v[84:87], v1 offset:16
	ds_read_b128 v[88:91], v1 offset:10400
	ds_read_b128 v[92:95], v1 offset:10416
	s_waitcnt vmcnt(48) lgkmcnt(3)
	v_mfma_f32_32x32x16_f16 v[50:65], v[134:137], v[80:83], v[50:65]
	s_waitcnt lgkmcnt(2)
	v_mfma_f32_32x32x16_f16 v[50:65], v[130:133], v[84:87], v[50:65]
	v_mfma_f32_32x32x16_f16 v[50:65], v[130:133], v[80:83], v[50:65]
	ds_read_b128 v[80:83], v1 offset:20800
	ds_read_b128 v[84:87], v1 offset:20816
	s_waitcnt lgkmcnt(3)
	v_mfma_f32_32x32x16_f16 v[34:49], v[134:137], v[88:91], v[34:49]
	s_waitcnt lgkmcnt(2)
	v_mfma_f32_32x32x16_f16 v[34:49], v[130:133], v[92:95], v[34:49]
	v_mfma_f32_32x32x16_f16 v[34:49], v[130:133], v[88:91], v[34:49]
	ds_read_b128 v[88:91], v1 offset:31200
	ds_read_b128 v[92:95], v1 offset:31216
	s_waitcnt lgkmcnt(3)
	v_mfma_f32_32x32x16_f16 v[18:33], v[134:137], v[80:83], v[18:33]
	s_waitcnt lgkmcnt(2)
	v_mfma_f32_32x32x16_f16 v[18:33], v[130:133], v[84:87], v[18:33]
	v_mfma_f32_32x32x16_f16 v[18:33], v[130:133], v[80:83], v[18:33]
	ds_read_b128 v[80:83], v1 offset:2640
	ds_read_b128 v[84:87], v1 offset:2656
	s_waitcnt lgkmcnt(3)
	v_mfma_f32_32x32x16_f16 v[2:17], v[134:137], v[88:91], v[2:17]
	s_waitcnt lgkmcnt(2)
	v_mfma_f32_32x32x16_f16 v[2:17], v[130:133], v[92:95], v[2:17]
	v_mfma_f32_32x32x16_f16 v[2:17], v[130:133], v[88:91], v[2:17]
	ds_read_b128 v[88:91], v1 offset:13040
	ds_read_b128 v[92:95], v1 offset:13056
	s_waitcnt vmcnt(46) lgkmcnt(3)
	v_mfma_f32_32x32x16_f16 v[50:65], v[126:129], v[80:83], v[50:65]
	s_waitcnt lgkmcnt(2)
	v_mfma_f32_32x32x16_f16 v[50:65], v[122:125], v[84:87], v[50:65]
	v_mfma_f32_32x32x16_f16 v[50:65], v[122:125], v[80:83], v[50:65]
	ds_read_b128 v[80:83], v1 offset:23440
	ds_read_b128 v[84:87], v1 offset:23456
	s_waitcnt lgkmcnt(3)
	v_mfma_f32_32x32x16_f16 v[34:49], v[126:129], v[88:91], v[34:49]
	s_waitcnt lgkmcnt(2)
	v_mfma_f32_32x32x16_f16 v[34:49], v[122:125], v[92:95], v[34:49]
	v_mfma_f32_32x32x16_f16 v[34:49], v[122:125], v[88:91], v[34:49]
	ds_read_b128 v[88:91], v1 offset:33840
	ds_read_b128 v[92:95], v1 offset:33856
	s_waitcnt lgkmcnt(3)
	v_mfma_f32_32x32x16_f16 v[18:33], v[126:129], v[80:83], v[18:33]
	s_waitcnt lgkmcnt(2)
	v_mfma_f32_32x32x16_f16 v[18:33], v[122:125], v[84:87], v[18:33]
	v_mfma_f32_32x32x16_f16 v[18:33], v[122:125], v[80:83], v[18:33]
	ds_read_b128 v[80:83], v1 offset:80
	ds_read_b128 v[84:87], v1 offset:96
	s_waitcnt lgkmcnt(3)
	v_mfma_f32_32x32x16_f16 v[2:17], v[126:129], v[88:91], v[2:17]
	s_waitcnt lgkmcnt(2)
	v_mfma_f32_32x32x16_f16 v[2:17], v[122:125], v[92:95], v[2:17]
	v_mfma_f32_32x32x16_f16 v[2:17], v[122:125], v[88:91], v[2:17]
	ds_read_b128 v[88:91], v1 offset:10480
	ds_read_b128 v[92:95], v1 offset:10496
	s_waitcnt vmcnt(44) lgkmcnt(3)
	v_mfma_f32_32x32x16_f16 v[50:65], v[118:121], v[80:83], v[50:65]
	s_waitcnt lgkmcnt(2)
	v_mfma_f32_32x32x16_f16 v[50:65], v[114:117], v[84:87], v[50:65]
	v_mfma_f32_32x32x16_f16 v[50:65], v[114:117], v[80:83], v[50:65]
	ds_read_b128 v[80:83], v1 offset:20880
	ds_read_b128 v[84:87], v1 offset:20896
	s_waitcnt lgkmcnt(3)
	v_mfma_f32_32x32x16_f16 v[34:49], v[118:121], v[88:91], v[34:49]
	s_waitcnt lgkmcnt(2)
	v_mfma_f32_32x32x16_f16 v[34:49], v[114:117], v[92:95], v[34:49]
	v_mfma_f32_32x32x16_f16 v[34:49], v[114:117], v[88:91], v[34:49]
	ds_read_b128 v[88:91], v1 offset:31280
	ds_read_b128 v[92:95], v1 offset:31296
	s_waitcnt lgkmcnt(3)
	v_mfma_f32_32x32x16_f16 v[18:33], v[118:121], v[80:83], v[18:33]
	s_waitcnt lgkmcnt(2)
	v_mfma_f32_32x32x16_f16 v[18:33], v[114:117], v[84:87], v[18:33]
	v_mfma_f32_32x32x16_f16 v[18:33], v[114:117], v[80:83], v[18:33]
	ds_read_b128 v[80:83], v1 offset:5200
	ds_read_b128 v[84:87], v1 offset:5216
	s_waitcnt lgkmcnt(3)
	v_mfma_f32_32x32x16_f16 v[2:17], v[118:121], v[88:91], v[2:17]
	s_waitcnt lgkmcnt(2)
	v_mfma_f32_32x32x16_f16 v[2:17], v[114:117], v[92:95], v[2:17]
	v_mfma_f32_32x32x16_f16 v[2:17], v[114:117], v[88:91], v[2:17]
	s_add_u32 s64, s62, 0x1c000
	s_addc_u32 s65, s63, 0
	global_load_dwordx4 v[130:133], v96, s[64:65]
	global_load_dwordx4 v[134:137], v96, s[64:65] offset:16
	s_add_u32 s64, s62, 0x1e000
	s_addc_u32 s65, s63, 0
	global_load_dwordx4 v[122:125], v96, s[64:65]
	global_load_dwordx4 v[126:129], v96, s[64:65] offset:16
	s_add_u32 s64, s62, 0x20000
	s_addc_u32 s65, s63, 0
	global_load_dwordx4 v[114:117], v96, s[64:65]
	global_load_dwordx4 v[118:121], v96, s[64:65] offset:16
	ds_read_b128 v[88:91], v1 offset:15600
	ds_read_b128 v[92:95], v1 offset:15616
	s_waitcnt vmcnt(48) lgkmcnt(3)
	v_mfma_f32_32x32x16_f16 v[50:65], v[110:113], v[80:83], v[50:65]
	s_waitcnt lgkmcnt(2)
	v_mfma_f32_32x32x16_f16 v[50:65], v[106:109], v[84:87], v[50:65]
	v_mfma_f32_32x32x16_f16 v[50:65], v[106:109], v[80:83], v[50:65]
	ds_read_b128 v[80:83], v1 offset:26000
	ds_read_b128 v[84:87], v1 offset:26016
	s_waitcnt lgkmcnt(3)
	v_mfma_f32_32x32x16_f16 v[34:49], v[110:113], v[88:91], v[34:49]
	s_waitcnt lgkmcnt(2)
	v_mfma_f32_32x32x16_f16 v[34:49], v[106:109], v[92:95], v[34:49]
	v_mfma_f32_32x32x16_f16 v[34:49], v[106:109], v[88:91], v[34:49]
	ds_read_b128 v[88:91], v1 offset:36400
	ds_read_b128 v[92:95], v1 offset:36416
	s_waitcnt lgkmcnt(3)
	v_mfma_f32_32x32x16_f16 v[18:33], v[110:113], v[80:83], v[18:33]
	s_waitcnt lgkmcnt(2)
	v_mfma_f32_32x32x16_f16 v[18:33], v[106:109], v[84:87], v[18:33]
	v_mfma_f32_32x32x16_f16 v[18:33], v[106:109], v[80:83], v[18:33]
	ds_read_b128 v[80:83], v1 offset:7840
	ds_read_b128 v[84:87], v1 offset:7856
	s_waitcnt lgkmcnt(3)
	v_mfma_f32_32x32x16_f16 v[2:17], v[110:113], v[88:91], v[2:17]
	s_waitcnt lgkmcnt(2)
	v_mfma_f32_32x32x16_f16 v[2:17], v[106:109], v[92:95], v[2:17]
	v_mfma_f32_32x32x16_f16 v[2:17], v[106:109], v[88:91], v[2:17]
	s_add_u32 s64, s62, 0x22000
	s_addc_u32 s65, s63, 0
	global_load_dwordx4 v[106:109], v96, s[64:65]
	global_load_dwordx4 v[110:113], v96, s[64:65] offset:16
	ds_read_b128 v[88:91], v1 offset:18240
	ds_read_b128 v[92:95], v1 offset:18256
	s_waitcnt vmcnt(48) lgkmcnt(3)
	v_mfma_f32_32x32x16_f16 v[50:65], v[102:105], v[80:83], v[50:65]
	s_waitcnt lgkmcnt(2)
	v_mfma_f32_32x32x16_f16 v[50:65], v[98:101], v[84:87], v[50:65]
	v_mfma_f32_32x32x16_f16 v[50:65], v[98:101], v[80:83], v[50:65]
	ds_read_b128 v[80:83], v1 offset:28640
	ds_read_b128 v[84:87], v1 offset:28656
	s_waitcnt lgkmcnt(3)
	v_mfma_f32_32x32x16_f16 v[34:49], v[102:105], v[88:91], v[34:49]
	s_waitcnt lgkmcnt(2)
	v_mfma_f32_32x32x16_f16 v[34:49], v[98:101], v[92:95], v[34:49]
	v_mfma_f32_32x32x16_f16 v[34:49], v[98:101], v[88:91], v[34:49]
	ds_read_b128 v[88:91], v1 offset:39040
	ds_read_b128 v[92:95], v1 offset:39056
	s_waitcnt lgkmcnt(3)
	v_mfma_f32_32x32x16_f16 v[18:33], v[102:105], v[80:83], v[18:33]
	s_waitcnt lgkmcnt(2)
	v_mfma_f32_32x32x16_f16 v[18:33], v[98:101], v[84:87], v[18:33]
	v_mfma_f32_32x32x16_f16 v[18:33], v[98:101], v[80:83], v[18:33]
	ds_read_b128 v[80:83], v1 offset:5280
	ds_read_b128 v[84:87], v1 offset:5296
	s_waitcnt lgkmcnt(3)
	v_mfma_f32_32x32x16_f16 v[2:17], v[102:105], v[88:91], v[2:17]
	s_waitcnt lgkmcnt(2)
	v_mfma_f32_32x32x16_f16 v[2:17], v[98:101], v[92:95], v[2:17]
	v_mfma_f32_32x32x16_f16 v[2:17], v[98:101], v[88:91], v[2:17]
	ds_read_b128 v[88:91], v1 offset:15680
	ds_read_b128 v[92:95], v1 offset:15696
	s_waitcnt vmcnt(6) lgkmcnt(3)
	v_mfma_f32_32x32x16_f16 v[50:65], v[134:137], v[80:83], v[50:65]
	s_waitcnt lgkmcnt(2)
	v_mfma_f32_32x32x16_f16 v[50:65], v[130:133], v[84:87], v[50:65]
	v_mfma_f32_32x32x16_f16 v[50:65], v[130:133], v[80:83], v[50:65]
	ds_read_b128 v[80:83], v1 offset:26080
	ds_read_b128 v[84:87], v1 offset:26096
	s_waitcnt lgkmcnt(3)
	v_mfma_f32_32x32x16_f16 v[34:49], v[134:137], v[88:91], v[34:49]
	s_waitcnt lgkmcnt(2)
	v_mfma_f32_32x32x16_f16 v[34:49], v[130:133], v[92:95], v[34:49]
	v_mfma_f32_32x32x16_f16 v[34:49], v[130:133], v[88:91], v[34:49]
	ds_read_b128 v[88:91], v1 offset:36480
	ds_read_b128 v[92:95], v1 offset:36496
	s_waitcnt lgkmcnt(3)
	v_mfma_f32_32x32x16_f16 v[18:33], v[134:137], v[80:83], v[18:33]
	s_waitcnt lgkmcnt(2)
	v_mfma_f32_32x32x16_f16 v[18:33], v[130:133], v[84:87], v[18:33]
	v_mfma_f32_32x32x16_f16 v[18:33], v[130:133], v[80:83], v[18:33]
	ds_read_b128 v[80:83], v1 offset:10400
	ds_read_b128 v[84:87], v1 offset:10416
	s_waitcnt lgkmcnt(3)
	v_mfma_f32_32x32x16_f16 v[2:17], v[134:137], v[88:91], v[2:17]
	s_waitcnt lgkmcnt(2)
	v_mfma_f32_32x32x16_f16 v[2:17], v[130:133], v[92:95], v[2:17]
	v_mfma_f32_32x32x16_f16 v[2:17], v[130:133], v[88:91], v[2:17]
	ds_read_b128 v[88:91], v1 offset:20800
	ds_read_b128 v[92:95], v1 offset:20816
	s_waitcnt vmcnt(4) lgkmcnt(3)
	v_mfma_f32_32x32x16_f16 v[50:65], v[126:129], v[80:83], v[50:65]
	s_waitcnt lgkmcnt(2)
	v_mfma_f32_32x32x16_f16 v[50:65], v[122:125], v[84:87], v[50:65]
	v_mfma_f32_32x32x16_f16 v[50:65], v[122:125], v[80:83], v[50:65]
	ds_read_b128 v[80:83], v1 offset:31200
	ds_read_b128 v[84:87], v1 offset:31216
	s_waitcnt lgkmcnt(3)
	v_mfma_f32_32x32x16_f16 v[34:49], v[126:129], v[88:91], v[34:49]
	s_waitcnt lgkmcnt(2)
	v_mfma_f32_32x32x16_f16 v[34:49], v[122:125], v[92:95], v[34:49]
	v_mfma_f32_32x32x16_f16 v[34:49], v[122:125], v[88:91], v[34:49]
	ds_read_b128 v[88:91], v1 offset:41600
	ds_read_b128 v[92:95], v1 offset:41616
	s_waitcnt lgkmcnt(3)
	v_mfma_f32_32x32x16_f16 v[18:33], v[126:129], v[80:83], v[18:33]
	s_waitcnt lgkmcnt(2)
	v_mfma_f32_32x32x16_f16 v[18:33], v[122:125], v[84:87], v[18:33]
	v_mfma_f32_32x32x16_f16 v[18:33], v[122:125], v[80:83], v[18:33]
	ds_read_b128 v[80:83], v1 offset:13040
	ds_read_b128 v[84:87], v1 offset:13056
	s_waitcnt lgkmcnt(3)
	v_mfma_f32_32x32x16_f16 v[2:17], v[126:129], v[88:91], v[2:17]
	s_waitcnt lgkmcnt(2)
	v_mfma_f32_32x32x16_f16 v[2:17], v[122:125], v[92:95], v[2:17]
	v_mfma_f32_32x32x16_f16 v[2:17], v[122:125], v[88:91], v[2:17]
	ds_read_b128 v[88:91], v1 offset:23440
	ds_read_b128 v[92:95], v1 offset:23456
	s_waitcnt vmcnt(2) lgkmcnt(3)
	v_mfma_f32_32x32x16_f16 v[50:65], v[118:121], v[80:83], v[50:65]
	s_waitcnt lgkmcnt(2)
	v_mfma_f32_32x32x16_f16 v[50:65], v[114:117], v[84:87], v[50:65]
	v_mfma_f32_32x32x16_f16 v[50:65], v[114:117], v[80:83], v[50:65]
	ds_read_b128 v[80:83], v1 offset:33840
	ds_read_b128 v[84:87], v1 offset:33856
	s_waitcnt lgkmcnt(3)
	v_mfma_f32_32x32x16_f16 v[34:49], v[118:121], v[88:91], v[34:49]
	s_waitcnt lgkmcnt(2)
	v_mfma_f32_32x32x16_f16 v[34:49], v[114:117], v[92:95], v[34:49]
	v_mfma_f32_32x32x16_f16 v[34:49], v[114:117], v[88:91], v[34:49]
	ds_read_b128 v[88:91], v1 offset:44240
	ds_read_b128 v[92:95], v1 offset:44256
	s_waitcnt lgkmcnt(3)
	v_mfma_f32_32x32x16_f16 v[18:33], v[118:121], v[80:83], v[18:33]
	s_waitcnt lgkmcnt(2)
	v_mfma_f32_32x32x16_f16 v[18:33], v[114:117], v[84:87], v[18:33]
	v_mfma_f32_32x32x16_f16 v[18:33], v[114:117], v[80:83], v[18:33]
	ds_read_b128 v[80:83], v1 offset:10480
	ds_read_b128 v[84:87], v1 offset:10496
	s_waitcnt lgkmcnt(3)
	v_mfma_f32_32x32x16_f16 v[2:17], v[118:121], v[88:91], v[2:17]
	s_waitcnt lgkmcnt(2)
	v_mfma_f32_32x32x16_f16 v[2:17], v[114:117], v[92:95], v[2:17]
	v_mfma_f32_32x32x16_f16 v[2:17], v[114:117], v[88:91], v[2:17]
	ds_read_b128 v[88:91], v1 offset:20880
	ds_read_b128 v[92:95], v1 offset:20896
	s_waitcnt vmcnt(0) lgkmcnt(3)
	v_mfma_f32_32x32x16_f16 v[50:65], v[110:113], v[80:83], v[50:65]
	s_waitcnt lgkmcnt(2)
	v_mfma_f32_32x32x16_f16 v[50:65], v[106:109], v[84:87], v[50:65]
	v_mfma_f32_32x32x16_f16 v[50:65], v[106:109], v[80:83], v[50:65]
	ds_read_b128 v[80:83], v1 offset:31280
	ds_read_b128 v[84:87], v1 offset:31296
	s_waitcnt lgkmcnt(3)
	v_mfma_f32_32x32x16_f16 v[34:49], v[110:113], v[88:91], v[34:49]
	s_waitcnt lgkmcnt(2)
	v_mfma_f32_32x32x16_f16 v[34:49], v[106:109], v[92:95], v[34:49]
	v_mfma_f32_32x32x16_f16 v[34:49], v[106:109], v[88:91], v[34:49]
	ds_read_b128 v[88:91], v1 offset:41680
	ds_read_b128 v[92:95], v1 offset:41696
	s_waitcnt lgkmcnt(3)
	v_mfma_f32_32x32x16_f16 v[18:33], v[110:113], v[80:83], v[18:33]
	s_waitcnt lgkmcnt(2)
	v_mfma_f32_32x32x16_f16 v[18:33], v[106:109], v[84:87], v[18:33]
	v_mfma_f32_32x32x16_f16 v[18:33], v[106:109], v[80:83], v[18:33]
	s_waitcnt lgkmcnt(1)
	v_mfma_f32_32x32x16_f16 v[2:17], v[110:113], v[88:91], v[2:17]
	s_waitcnt lgkmcnt(0)
	v_mfma_f32_32x32x16_f16 v[2:17], v[106:109], v[92:95], v[2:17]
	v_mfma_f32_32x32x16_f16 v[2:17], v[106:109], v[88:91], v[2:17]
	s_add_u32 s64, s62, 0x24000
	s_addc_u32 s65, s63, 0
	global_load_dwordx4 v[130:133], v96, s[64:65]
	global_load_dwordx4 v[134:137], v96, s[64:65] offset:16
	s_add_u32 s64, s62, 0x26000
	s_addc_u32 s65, s63, 0
	global_load_dwordx4 v[122:125], v96, s[64:65]
	global_load_dwordx4 v[126:129], v96, s[64:65] offset:16
	s_add_u32 s64, s62, 0x28000
	s_addc_u32 s65, s63, 0
	global_load_dwordx4 v[114:117], v96, s[64:65]
	global_load_dwordx4 v[118:121], v96, s[64:65] offset:16
	s_add_u32 s64, s62, 0x2a000
	s_addc_u32 s65, s63, 0
	global_load_dwordx4 v[106:109], v96, s[64:65]
	global_load_dwordx4 v[110:113], v96, s[64:65] offset:16
	s_add_u32 s64, s62, 0x2c000
	s_addc_u32 s65, s63, 0
	global_load_dwordx4 v[98:101], v96, s[64:65]
	global_load_dwordx4 v[102:105], v96, s[64:65] offset:16
	v_mov_b32_e32 v80, v0
	s_and_b64 vcc, exec, s[0:1]
	s_barrier
	s_cbranch_vccnz .LBB4_46
	s_waitcnt vmcnt(57)
	v_mov_b32_e32 v79, 0
	s_waitcnt vmcnt(56)
	v_mov_b32_e32 v78, 0
	s_waitcnt vmcnt(55)
	v_mov_b32_e32 v66, 0
	s_waitcnt vmcnt(54)
	v_mov_b32_e32 v67, v79
	s_waitcnt vmcnt(53)
	v_mov_b32_e32 v164, 0
	s_waitcnt vmcnt(52)
	v_mov_b32_e32 v165, v79
	s_waitcnt vmcnt(51)
	v_mov_b32_e32 v166, 0
	s_waitcnt vmcnt(50)
	v_mov_b32_e32 v167, v79
.LBB4_46:
	v_and_b32_e32 v81, 63, v80
	v_add_u32_e32 v82, 1, v81
	v_and_b32_e32 v80, 1, v80
	v_lshrrev_b32_e32 v82, 1, v82
	v_add_u32_e32 v83, 33, v82
	v_cmp_eq_u32_e32 vcc, 0, v80
	s_movk_i32 s44, 0x50
	s_nop 0
	v_cndmask_b32_e32 v82, v82, v83, vcc
	v_mov_b32_e32 v83, s33
	v_mad_u32_u24 v92, v82, s44, v83
	s_mov_b32 s44, 0x41800000
	s_waitcnt vmcnt(54)
	v_pk_mul_f32 v[84:85], v[66:67], s[44:45] op_sel_hi:[1,0]
	v_mul_u32_u24_e32 v80, 0x50, v82
	v_cvt_pk_f16_f32 v87, v84, v85
	v_cvt_f32_f16_e32 v84, v87
	v_cvt_f32_f16_sdwa v85, v87 dst_sel:DWORD dst_unused:UNUSED_PAD src0_sel:WORD_1
	v_fma_mixlo_f16 v82, v79, s44, 0
	v_mul_f32_e32 v83, 0x41800000, v79
	v_fma_mixlo_f16 v82, v79, s44, -v82 op_sel_hi:[0,0,1]
	v_mul_f32_e32 v79, 0x41800000, v78
	v_fma_mixlo_f16 v88, v78, s44, 0
	v_cvt_pk_f16_f32 v86, v83, v79
	v_fma_mixhi_f16 v82, v78, s44, -v88 op_sel_hi:[0,0,1]
	s_waitcnt vmcnt(52)
	v_pk_mul_f32 v[78:79], v[164:165], s[44:45] op_sel_hi:[1,0]
	v_pk_fma_f32 v[66:67], v[66:67], s[44:45], v[84:85] op_sel_hi:[1,0,1] neg_lo:[0,0,1] neg_hi:[0,0,1]
	v_cvt_pk_f16_f32 v88, v78, v79
	s_waitcnt vmcnt(50)
	v_pk_mul_f32 v[84:85], v[166:167], s[44:45] op_sel_hi:[1,0]
	v_cvt_f32_f16_e32 v78, v88
	v_cvt_f32_f16_sdwa v79, v88 dst_sel:DWORD dst_unused:UNUSED_PAD src0_sel:WORD_1
	v_cvt_pk_f16_f32 v89, v84, v85
	v_cvt_f32_f16_e32 v90, v89
	v_cvt_f32_f16_sdwa v91, v89 dst_sel:DWORD dst_unused:UNUSED_PAD src0_sel:WORD_1
	v_pk_fma_f32 v[164:165], v[164:165], s[44:45], v[78:79] op_sel_hi:[1,0,1] neg_lo:[0,0,1] neg_hi:[0,0,1]
	v_cvt_pk_f16_f32 v83, v66, v67
	v_cvt_pk_f16_f32 v84, v164, v165
	v_pk_fma_f32 v[164:165], v[166:167], s[44:45], v[90:91] op_sel_hi:[1,0,1] neg_lo:[0,0,1] neg_hi:[0,0,1]
	s_and_b64 vcc, exec, s[12:13]
	v_cvt_pk_f16_f32 v85, v164, v165
	ds_write_b128 v92, v[86:89]
	ds_write_b128 v92, v[82:85] offset:16
	s_cbranch_vccnz .LBB4_48
	s_waitcnt vmcnt(49)
	v_mov_b32_e32 v77, 0
	s_waitcnt vmcnt(48)
	v_mov_b32_e32 v76, 0
	s_waitcnt vmcnt(47)
	v_mov_b32_e32 v162, 0
	s_waitcnt vmcnt(46)
	v_mov_b32_e32 v163, v77
	s_waitcnt vmcnt(45)
	v_mov_b32_e32 v158, 0
	s_waitcnt vmcnt(44)
	v_mov_b32_e32 v159, v77
	s_waitcnt vmcnt(43)
	v_mov_b32_e32 v160, 0
	s_waitcnt vmcnt(42)
	v_mov_b32_e32 v161, v77
.LBB4_48:
	s_waitcnt vmcnt(46)
	v_pk_mul_f32 v[166:167], v[162:163], s[44:45] op_sel_hi:[1,0]
	v_fma_mixlo_f16 v164, v77, s44, 0
	v_cvt_pk_f16_f32 v83, v166, v167
	v_cvt_f32_f16_e32 v166, v83
	v_cvt_f32_f16_sdwa v167, v83 dst_sel:DWORD dst_unused:UNUSED_PAD src0_sel:WORD_1
	v_mul_f32_e32 v165, 0x41800000, v77
	v_fma_mixlo_f16 v164, v77, s44, -v164 op_sel_hi:[0,0,1]
	v_mul_f32_e32 v66, 0x41800000, v76
	v_fma_mixlo_f16 v67, v76, s44, 0
	v_pk_fma_f32 v[162:163], v[162:163], s[44:45], v[166:167] op_sel_hi:[1,0,1] neg_lo:[0,0,1] neg_hi:[0,0,1]
	s_waitcnt vmcnt(44)
	v_pk_mul_f32 v[166:167], v[158:159], s[44:45] op_sel_hi:[1,0]
	v_cvt_pk_f16_f32 v82, v165, v66
	v_fma_mixhi_f16 v164, v76, s44, -v67 op_sel_hi:[0,0,1]
	v_cvt_pk_f16_f32 v84, v166, v167
	s_waitcnt vmcnt(42)
	v_pk_mul_f32 v[66:67], v[160:161], s[44:45] op_sel_hi:[1,0]
	v_cvt_f32_f16_e32 v166, v84
	v_cvt_f32_f16_sdwa v167, v84 dst_sel:DWORD dst_unused:UNUSED_PAD src0_sel:WORD_1
	v_cvt_pk_f16_f32 v85, v66, v67
	v_cvt_f32_f16_e32 v66, v85
	v_cvt_f32_f16_sdwa v67, v85 dst_sel:DWORD dst_unused:UNUSED_PAD src0_sel:WORD_1
	v_pk_fma_f32 v[158:159], v[158:159], s[44:45], v[166:167] op_sel_hi:[1,0,1] neg_lo:[0,0,1] neg_hi:[0,0,1]
	v_add_u32_e32 v78, s50, v80
	v_cvt_pk_f16_f32 v166, v158, v159
	v_pk_fma_f32 v[158:159], v[160:161], s[44:45], v[66:67] op_sel_hi:[1,0,1] neg_lo:[0,0,1] neg_hi:[0,0,1]
	v_cvt_pk_f16_f32 v165, v162, v163
	v_cvt_pk_f16_f32 v167, v158, v159
	s_and_b64 vcc, exec, s[6:7]
	ds_write_b128 v78, v[82:85]
	ds_write_b128 v78, v[164:167] offset:16
	s_cbranch_vccnz .LBB4_50
	s_waitcnt vmcnt(41)
	v_mov_b32_e32 v75, 0
	s_waitcnt vmcnt(40)
	v_mov_b32_e32 v74, 0
	s_waitcnt vmcnt(39)
	v_mov_b32_e32 v156, 0
	s_waitcnt vmcnt(38)
	v_mov_b32_e32 v157, v75
	s_waitcnt vmcnt(37)
	v_mov_b32_e32 v152, 0
	s_waitcnt vmcnt(36)
	v_mov_b32_e32 v153, v75
	s_waitcnt vmcnt(35)
	v_mov_b32_e32 v154, 0
	s_waitcnt vmcnt(34)
	v_mov_b32_e32 v155, v75
.LBB4_50:
	s_waitcnt vmcnt(38)
	v_pk_mul_f32 v[160:161], v[156:157], s[44:45] op_sel_hi:[1,0]
	v_fma_mixlo_f16 v158, v75, s44, 0
	v_cvt_pk_f16_f32 v163, v160, v161
	v_cvt_f32_f16_e32 v160, v163
	v_cvt_f32_f16_sdwa v161, v163 dst_sel:DWORD dst_unused:UNUSED_PAD src0_sel:WORD_1
	v_fma_mixlo_f16 v158, v75, s44, -v158 op_sel_hi:[0,0,1]
	v_fma_mixlo_f16 v164, v74, s44, 0
	v_fma_mixhi_f16 v158, v74, s44, -v164 op_sel_hi:[0,0,1]
	v_pk_fma_f32 v[156:157], v[156:157], s[44:45], v[160:161] op_sel_hi:[1,0,1] neg_lo:[0,0,1] neg_hi:[0,0,1]
	s_waitcnt vmcnt(36)
	v_pk_mul_f32 v[160:161], v[152:153], s[44:45] op_sel_hi:[1,0]
	s_waitcnt vmcnt(34)
	v_pk_mul_f32 v[166:167], v[154:155], s[44:45] op_sel_hi:[1,0]
	v_cvt_pk_f16_f32 v164, v160, v161
	v_cvt_f32_f16_e32 v160, v164
	v_cvt_f32_f16_sdwa v161, v164 dst_sel:DWORD dst_unused:UNUSED_PAD src0_sel:WORD_1
	v_cvt_pk_f16_f32 v165, v166, v167
	v_cvt_f32_f16_e32 v166, v165
	v_cvt_f32_f16_sdwa v167, v165 dst_sel:DWORD dst_unused:UNUSED_PAD src0_sel:WORD_1
	v_pk_fma_f32 v[152:153], v[152:153], s[44:45], v[160:161] op_sel_hi:[1,0,1] neg_lo:[0,0,1] neg_hi:[0,0,1]
	v_mul_f32_e32 v159, 0x41800000, v75
	v_mul_f32_e32 v162, 0x41800000, v74
	v_cvt_pk_f16_f32 v160, v152, v153
	v_pk_fma_f32 v[152:153], v[154:155], s[44:45], v[166:167] op_sel_hi:[1,0,1] neg_lo:[0,0,1] neg_hi:[0,0,1]
	v_add_u32_e32 v66, s51, v80
	v_cvt_pk_f16_f32 v162, v159, v162
	v_cvt_pk_f16_f32 v159, v156, v157
	v_cvt_pk_f16_f32 v161, v152, v153
	s_and_b64 vcc, exec, s[8:9]
	ds_write_b128 v66, v[162:165]
	ds_write_b128 v66, v[158:161] offset:16
	s_cbranch_vccnz .LBB4_52
	s_waitcnt vmcnt(33)
	v_mov_b32_e32 v73, 0
	s_waitcnt vmcnt(32)
	v_mov_b32_e32 v72, 0
	s_waitcnt vmcnt(31)
	v_mov_b32_e32 v150, 0
	s_waitcnt vmcnt(30)
	v_mov_b32_e32 v151, v73
	s_waitcnt vmcnt(29)
	v_mov_b32_e32 v146, 0
	s_waitcnt vmcnt(28)
	v_mov_b32_e32 v147, v73
	s_waitcnt vmcnt(27)
	v_mov_b32_e32 v148, 0
	s_waitcnt vmcnt(26)
	v_mov_b32_e32 v149, v73
.LBB4_52:
	s_waitcnt vmcnt(30)
	v_pk_mul_f32 v[154:155], v[150:151], s[44:45] op_sel_hi:[1,0]
	v_fma_mixlo_f16 v152, v73, s44, 0
	v_cvt_pk_f16_f32 v157, v154, v155
	v_cvt_f32_f16_e32 v154, v157
	v_cvt_f32_f16_sdwa v155, v157 dst_sel:DWORD dst_unused:UNUSED_PAD src0_sel:WORD_1
	v_fma_mixlo_f16 v152, v73, s44, -v152 op_sel_hi:[0,0,1]
	v_fma_mixlo_f16 v158, v72, s44, 0
	v_fma_mixhi_f16 v152, v72, s44, -v158 op_sel_hi:[0,0,1]
	v_pk_fma_f32 v[150:151], v[150:151], s[44:45], v[154:155] op_sel_hi:[1,0,1] neg_lo:[0,0,1] neg_hi:[0,0,1]
	s_waitcnt vmcnt(28)
	v_pk_mul_f32 v[154:155], v[146:147], s[44:45] op_sel_hi:[1,0]
	s_waitcnt vmcnt(26)
	v_pk_mul_f32 v[160:161], v[148:149], s[44:45] op_sel_hi:[1,0]
	v_cvt_pk_f16_f32 v158, v154, v155
	v_cvt_f32_f16_e32 v154, v158
	v_cvt_f32_f16_sdwa v155, v158 dst_sel:DWORD dst_unused:UNUSED_PAD src0_sel:WORD_1
	v_cvt_pk_f16_f32 v159, v160, v161
	v_cvt_f32_f16_e32 v160, v159
	v_cvt_f32_f16_sdwa v161, v159 dst_sel:DWORD dst_unused:UNUSED_PAD src0_sel:WORD_1
	v_pk_fma_f32 v[146:147], v[146:147], s[44:45], v[154:155] op_sel_hi:[1,0,1] neg_lo:[0,0,1] neg_hi:[0,0,1]
	v_mul_f32_e32 v153, 0x41800000, v73
	v_mul_f32_e32 v156, 0x41800000, v72
	v_cvt_pk_f16_f32 v154, v146, v147
	v_pk_fma_f32 v[146:147], v[148:149], s[44:45], v[160:161] op_sel_hi:[1,0,1] neg_lo:[0,0,1] neg_hi:[0,0,1]
	v_add_u32_e32 v162, s52, v80
	v_cvt_pk_f16_f32 v156, v153, v156
	v_cvt_pk_f16_f32 v153, v150, v151
	v_cvt_pk_f16_f32 v155, v146, v147
	s_and_b64 vcc, exec, s[10:11]
	ds_write_b128 v162, v[156:159] offset:32
	ds_write_b128 v162, v[152:155] offset:48
	s_cbranch_vccnz .LBB4_54
	v_cmp_lt_u32_e32 vcc, 8, v81
	v_min_u32_e32 v146, 17, v81
	s_movk_i32 s44, 0x1450
	v_cndmask_b32_e64 v147, 0, -9, vcc
	v_add_u32_e32 v147, v147, v146
	v_cndmask_b32_e64 v146, 0, 32, vcc
	v_cmp_lt_i32_e32 vcc, s5, v147
	s_and_b64 s[46:47], s[24:25], vcc
	v_cmp_gt_u32_e32 vcc, 18, v81
	v_mad_i32_i24 v146, v147, s44, v146
	s_and_b64 s[48:49], s[26:27], vcc
	s_cbranch_execz .LBB4_55
	s_branch .LBB4_56

.LBB4_60:
	s_or_b64 exec, exec, s[44:45]
	s_mul_i32 s44, s28, 48
	s_waitcnt vmcnt(21)
	v_mov_b32_e32 v140, v0
	s_ashr_i32 s45, s44, 31
	s_waitcnt lgkmcnt(0)
	s_barrier
	s_lshl_b64 s[44:45], s[44:45], 2
	s_waitcnt vmcnt(19)
	v_and_b32_e32 v142, 63, v140
	s_add_u32 s34, s34, s44
	v_or_b32_e32 v140, s57, v142
	s_addc_u32 s35, s35, s45
	v_ashrrev_i32_e32 v141, 31, v140
	v_lshl_add_u64 v[144:145], v[140:141], 2, s[34:35]
	v_lshl_add_u64 v[146:147], s[36:37], 2, v[144:145]
	v_lshl_add_u64 v[148:149], v[146:147], 0, s[30:31]
	v_lshl_add_u64 v[150:151], v[148:149], 0, s[30:31]
	v_lshl_add_u64 v[152:153], v[150:151], 0, s[30:31]
	v_lshl_add_u64 v[154:155], v[152:153], 0, s[30:31]
	v_lshl_add_u64 v[156:157], v[154:155], 0, s[30:31]
	v_lshl_add_u64 v[158:159], v[156:157], 0, s[30:31]
	v_lshl_add_u64 v[160:161], v[158:159], 0, s[30:31]
	global_load_dword v78, v[146:147], off
	global_load_dword v77, v[148:149], off
	global_load_dword v66, v[150:151], off
	global_load_dword v67, v[152:153], off
	global_load_dword v164, v[154:155], off
	global_load_dword v165, v[156:157], off
	global_load_dword v166, v[158:159], off
	global_load_dword v167, v[160:161], off
	v_lshl_add_u64 v[146:147], s[38:39], 2, v[144:145]
	v_lshl_add_u64 v[148:149], v[146:147], 0, s[30:31]
	v_lshl_add_u64 v[150:151], v[148:149], 0, s[30:31]
	v_lshl_add_u64 v[152:153], v[150:151], 0, s[30:31]
	v_lshl_add_u64 v[154:155], v[152:153], 0, s[30:31]
	v_lshl_add_u64 v[156:157], v[154:155], 0, s[30:31]
	v_lshl_add_u64 v[160:161], v[156:157], 0, s[30:31]
	v_lshl_add_u64 v[70:71], v[160:161], 0, s[30:31]
	global_load_dword v76, v[146:147], off
	global_load_dword v75, v[148:149], off
	global_load_dword v162, v[150:151], off
	global_load_dword v163, v[152:153], off
	global_load_dword v158, v[154:155], off
	global_load_dword v159, v[156:157], off
	s_nop 0
	global_load_dword v160, v[160:161], off
	s_nop 0
	global_load_dword v161, v[70:71], off
	v_lshl_add_u64 v[146:147], s[40:41], 2, v[144:145]
	v_lshl_add_u64 v[148:149], v[146:147], 0, s[30:31]
	v_lshl_add_u64 v[150:151], v[148:149], 0, s[30:31]
	v_lshl_add_u64 v[152:153], v[150:151], 0, s[30:31]
	v_lshl_add_u64 v[154:155], v[152:153], 0, s[30:31]
	v_lshl_add_u64 v[70:71], v[154:155], 0, s[30:31]
	v_lshl_add_u64 v[80:81], v[70:71], 0, s[30:31]
	v_lshl_add_u64 v[144:145], s[42:43], 2, v[144:145]
	v_lshl_add_u64 v[82:83], v[80:81], 0, s[30:31]
	global_load_dword v74, v[146:147], off
	global_load_dword v73, v[148:149], off
	global_load_dword v156, v[150:151], off
	global_load_dword v157, v[152:153], off
	s_nop 0
	global_load_dword v152, v[154:155], off
	global_load_dword v153, v[70:71], off
	s_nop 0
	global_load_dword v154, v[80:81], off
	global_load_dword v155, v[82:83], off
	v_lshl_add_u64 v[146:147], v[144:145], 0, s[30:31]
	v_lshl_add_u64 v[148:149], v[146:147], 0, s[30:31]
	v_lshl_add_u64 v[80:81], v[148:149], 0, s[30:31]
	v_lshl_add_u64 v[82:83], v[80:81], 0, s[30:31]
	v_lshl_add_u64 v[84:85], v[82:83], 0, s[30:31]
	v_lshl_add_u64 v[86:87], v[84:85], 0, s[30:31]
	v_lshl_add_u64 v[88:89], v[86:87], 0, s[30:31]
	global_load_dword v72, v[144:145], off
	global_load_dword v71, v[146:147], off
	global_load_dword v150, v[148:149], off
	global_load_dword v151, v[80:81], off
	s_nop 0
	global_load_dword v146, v[82:83], off
	global_load_dword v147, v[84:85], off
	global_load_dword v148, v[86:87], off
	global_load_dword v149, v[88:89], off
	s_and_b64 vcc, exec, s[10:11]
	s_cbranch_vccnz .LBB4_62
	v_cmp_lt_u32_e32 vcc, 8, v142
	v_min_u32_e32 v141, 17, v142
	s_nop 0
	v_cndmask_b32_e64 v142, 0, -9, vcc
	v_add3_u32 v141, v141, s54, v142
	v_max_i32_e32 v141, 0, v141
	v_min_i32_e32 v142, s56, v141
	v_cndmask_b32_e64 v141, 0, 8, vcc
	v_or_b32_e32 v141, s55, v141
	s_waitcnt vmcnt(50)
	v_mad_u64_u32 v[142:143], s[36:37], v141, s16, v[142:143]
	v_mul_lo_u32 v141, v142, s17
	v_add_u32_e32 v142, v141, v69
	s_cbranch_execz .LBB4_63
	s_branch .LBB4_64

.LBB4_64:
	s_waitcnt vmcnt(50)
	v_ashrrev_i32_e32 v143, 31, v142
	v_lshl_add_u64 v[140:141], v[142:143], 2, s[34:35]
	v_lshl_add_u64 v[142:143], s[28:29], 2, v[140:141]
	v_lshl_add_u64 v[144:145], v[142:143], 0, s[30:31]
	v_lshl_add_u64 v[80:81], v[144:145], 0, s[30:31]
	v_lshl_add_u64 v[82:83], v[80:81], 0, s[30:31]
	v_lshl_add_u64 v[84:85], v[82:83], 0, s[30:31]
	v_lshl_add_u64 v[86:87], v[84:85], 0, s[30:31]
	v_lshl_add_u64 v[88:89], v[86:87], 0, s[30:31]
	global_load_dword v70, v[140:141], off
	global_load_dword v69, v[142:143], off
	s_nop 0
	global_load_dword v144, v[144:145], off
	s_nop 0
	global_load_dword v145, v[80:81], off
	global_load_dword v140, v[82:83], off
	global_load_dword v141, v[84:85], off
	global_load_dword v142, v[86:87], off
	global_load_dword v143, v[88:89], off
	ds_read_b128 v[80:83], v1
	ds_read_b128 v[84:87], v1 offset:16
	ds_read_b128 v[88:91], v1 offset:10400
	ds_read_b128 v[92:95], v1 offset:10416
	s_waitcnt vmcnt(48) lgkmcnt(3)
	v_mfma_f32_32x32x16_f16 v[50:65], v[134:137], v[80:83], v[50:65]
	s_waitcnt lgkmcnt(2)
	v_mfma_f32_32x32x16_f16 v[50:65], v[130:133], v[84:87], v[50:65]
	v_mfma_f32_32x32x16_f16 v[50:65], v[130:133], v[80:83], v[50:65]
	ds_read_b128 v[80:83], v1 offset:20800
	ds_read_b128 v[84:87], v1 offset:20816
	s_waitcnt lgkmcnt(3)
	v_mfma_f32_32x32x16_f16 v[34:49], v[134:137], v[88:91], v[34:49]
	s_waitcnt lgkmcnt(2)
	v_mfma_f32_32x32x16_f16 v[34:49], v[130:133], v[92:95], v[34:49]
	v_mfma_f32_32x32x16_f16 v[34:49], v[130:133], v[88:91], v[34:49]
	ds_read_b128 v[88:91], v1 offset:31200
	ds_read_b128 v[92:95], v1 offset:31216
	s_waitcnt lgkmcnt(3)
	v_mfma_f32_32x32x16_f16 v[18:33], v[134:137], v[80:83], v[18:33]
	s_waitcnt lgkmcnt(2)
	v_mfma_f32_32x32x16_f16 v[18:33], v[130:133], v[84:87], v[18:33]
	v_mfma_f32_32x32x16_f16 v[18:33], v[130:133], v[80:83], v[18:33]
	ds_read_b128 v[80:83], v1 offset:2640
	ds_read_b128 v[84:87], v1 offset:2656
	s_waitcnt lgkmcnt(3)
	v_mfma_f32_32x32x16_f16 v[2:17], v[134:137], v[88:91], v[2:17]
	s_waitcnt lgkmcnt(2)
	v_mfma_f32_32x32x16_f16 v[2:17], v[130:133], v[92:95], v[2:17]
	v_mfma_f32_32x32x16_f16 v[2:17], v[130:133], v[88:91], v[2:17]
	ds_read_b128 v[88:91], v1 offset:13040
	ds_read_b128 v[92:95], v1 offset:13056
	s_waitcnt vmcnt(46) lgkmcnt(3)
	v_mfma_f32_32x32x16_f16 v[50:65], v[126:129], v[80:83], v[50:65]
	s_waitcnt lgkmcnt(2)
	v_mfma_f32_32x32x16_f16 v[50:65], v[122:125], v[84:87], v[50:65]
	v_mfma_f32_32x32x16_f16 v[50:65], v[122:125], v[80:83], v[50:65]
	ds_read_b128 v[80:83], v1 offset:23440
	ds_read_b128 v[84:87], v1 offset:23456
	s_waitcnt lgkmcnt(3)
	v_mfma_f32_32x32x16_f16 v[34:49], v[126:129], v[88:91], v[34:49]
	s_waitcnt lgkmcnt(2)
	v_mfma_f32_32x32x16_f16 v[34:49], v[122:125], v[92:95], v[34:49]
	v_mfma_f32_32x32x16_f16 v[34:49], v[122:125], v[88:91], v[34:49]
	ds_read_b128 v[88:91], v1 offset:33840
	ds_read_b128 v[92:95], v1 offset:33856
	s_waitcnt lgkmcnt(3)
	v_mfma_f32_32x32x16_f16 v[18:33], v[126:129], v[80:83], v[18:33]
	s_waitcnt lgkmcnt(2)
	v_mfma_f32_32x32x16_f16 v[18:33], v[122:125], v[84:87], v[18:33]
	v_mfma_f32_32x32x16_f16 v[18:33], v[122:125], v[80:83], v[18:33]
	ds_read_b128 v[80:83], v1 offset:80
	ds_read_b128 v[84:87], v1 offset:96
	s_waitcnt lgkmcnt(3)
	v_mfma_f32_32x32x16_f16 v[2:17], v[126:129], v[88:91], v[2:17]
	s_waitcnt lgkmcnt(2)
	v_mfma_f32_32x32x16_f16 v[2:17], v[122:125], v[92:95], v[2:17]
	v_mfma_f32_32x32x16_f16 v[2:17], v[122:125], v[88:91], v[2:17]
	ds_read_b128 v[88:91], v1 offset:10480
	ds_read_b128 v[92:95], v1 offset:10496
	s_waitcnt vmcnt(44) lgkmcnt(3)
	v_mfma_f32_32x32x16_f16 v[50:65], v[118:121], v[80:83], v[50:65]
	s_waitcnt lgkmcnt(2)
	v_mfma_f32_32x32x16_f16 v[50:65], v[114:117], v[84:87], v[50:65]
	v_mfma_f32_32x32x16_f16 v[50:65], v[114:117], v[80:83], v[50:65]
	ds_read_b128 v[80:83], v1 offset:20880
	ds_read_b128 v[84:87], v1 offset:20896
	s_waitcnt lgkmcnt(3)
	v_mfma_f32_32x32x16_f16 v[34:49], v[118:121], v[88:91], v[34:49]
	s_waitcnt lgkmcnt(2)
	v_mfma_f32_32x32x16_f16 v[34:49], v[114:117], v[92:95], v[34:49]
	v_mfma_f32_32x32x16_f16 v[34:49], v[114:117], v[88:91], v[34:49]
	ds_read_b128 v[88:91], v1 offset:31280
	ds_read_b128 v[92:95], v1 offset:31296
	s_waitcnt lgkmcnt(3)
	v_mfma_f32_32x32x16_f16 v[18:33], v[118:121], v[80:83], v[18:33]
	s_waitcnt lgkmcnt(2)
	v_mfma_f32_32x32x16_f16 v[18:33], v[114:117], v[84:87], v[18:33]
	v_mfma_f32_32x32x16_f16 v[18:33], v[114:117], v[80:83], v[18:33]
	ds_read_b128 v[80:83], v1 offset:5200
	ds_read_b128 v[84:87], v1 offset:5216
	s_waitcnt lgkmcnt(3)
	v_mfma_f32_32x32x16_f16 v[2:17], v[118:121], v[88:91], v[2:17]
	s_waitcnt lgkmcnt(2)
	v_mfma_f32_32x32x16_f16 v[2:17], v[114:117], v[92:95], v[2:17]
	v_mfma_f32_32x32x16_f16 v[2:17], v[114:117], v[88:91], v[2:17]
	s_add_u32 s64, s62, 0x2e000
	s_addc_u32 s65, s63, 0
	global_load_dwordx4 v[130:133], v96, s[64:65]
	global_load_dwordx4 v[134:137], v96, s[64:65] offset:16
	s_add_u32 s64, s62, 0x30000
	s_addc_u32 s65, s63, 0
	global_load_dwordx4 v[122:125], v96, s[64:65]
	global_load_dwordx4 v[126:129], v96, s[64:65] offset:16
	s_add_u32 s64, s62, 0x32000
	s_addc_u32 s65, s63, 0
	global_load_dwordx4 v[114:117], v96, s[64:65]
	global_load_dwordx4 v[118:121], v96, s[64:65] offset:16
	ds_read_b128 v[88:91], v1 offset:15600
	ds_read_b128 v[92:95], v1 offset:15616
	s_waitcnt vmcnt(48) lgkmcnt(3)
	v_mfma_f32_32x32x16_f16 v[50:65], v[110:113], v[80:83], v[50:65]
	s_waitcnt lgkmcnt(2)
	v_mfma_f32_32x32x16_f16 v[50:65], v[106:109], v[84:87], v[50:65]
	v_mfma_f32_32x32x16_f16 v[50:65], v[106:109], v[80:83], v[50:65]
	ds_read_b128 v[80:83], v1 offset:26000
	ds_read_b128 v[84:87], v1 offset:26016
	s_waitcnt lgkmcnt(3)
	v_mfma_f32_32x32x16_f16 v[34:49], v[110:113], v[88:91], v[34:49]
	s_waitcnt lgkmcnt(2)
	v_mfma_f32_32x32x16_f16 v[34:49], v[106:109], v[92:95], v[34:49]
	v_mfma_f32_32x32x16_f16 v[34:49], v[106:109], v[88:91], v[34:49]
	ds_read_b128 v[88:91], v1 offset:36400
	ds_read_b128 v[92:95], v1 offset:36416
	s_waitcnt lgkmcnt(3)
	v_mfma_f32_32x32x16_f16 v[18:33], v[110:113], v[80:83], v[18:33]
	s_waitcnt lgkmcnt(2)
	v_mfma_f32_32x32x16_f16 v[18:33], v[106:109], v[84:87], v[18:33]
	v_mfma_f32_32x32x16_f16 v[18:33], v[106:109], v[80:83], v[18:33]
	ds_read_b128 v[80:83], v1 offset:7840
	ds_read_b128 v[84:87], v1 offset:7856
	s_waitcnt lgkmcnt(3)
	v_mfma_f32_32x32x16_f16 v[2:17], v[110:113], v[88:91], v[2:17]
	s_waitcnt lgkmcnt(2)
	v_mfma_f32_32x32x16_f16 v[2:17], v[106:109], v[92:95], v[2:17]
	v_mfma_f32_32x32x16_f16 v[2:17], v[106:109], v[88:91], v[2:17]
	s_add_u32 s64, s62, 0x34000
	s_addc_u32 s65, s63, 0
	global_load_dwordx4 v[106:109], v96, s[64:65]
	global_load_dwordx4 v[110:113], v96, s[64:65] offset:16
	ds_read_b128 v[88:91], v1 offset:18240
	ds_read_b128 v[92:95], v1 offset:18256
	s_waitcnt vmcnt(48) lgkmcnt(3)
	v_mfma_f32_32x32x16_f16 v[50:65], v[102:105], v[80:83], v[50:65]
	s_waitcnt lgkmcnt(2)
	v_mfma_f32_32x32x16_f16 v[50:65], v[98:101], v[84:87], v[50:65]
	v_mfma_f32_32x32x16_f16 v[50:65], v[98:101], v[80:83], v[50:65]
	ds_read_b128 v[80:83], v1 offset:28640
	ds_read_b128 v[84:87], v1 offset:28656
	s_waitcnt lgkmcnt(3)
	v_mfma_f32_32x32x16_f16 v[34:49], v[102:105], v[88:91], v[34:49]
	s_waitcnt lgkmcnt(2)
	v_mfma_f32_32x32x16_f16 v[34:49], v[98:101], v[92:95], v[34:49]
	v_mfma_f32_32x32x16_f16 v[34:49], v[98:101], v[88:91], v[34:49]
	ds_read_b128 v[88:91], v1 offset:39040
	ds_read_b128 v[92:95], v1 offset:39056
	s_waitcnt lgkmcnt(3)
	v_mfma_f32_32x32x16_f16 v[18:33], v[102:105], v[80:83], v[18:33]
	s_waitcnt lgkmcnt(2)
	v_mfma_f32_32x32x16_f16 v[18:33], v[98:101], v[84:87], v[18:33]
	v_mfma_f32_32x32x16_f16 v[18:33], v[98:101], v[80:83], v[18:33]
	ds_read_b128 v[80:83], v1 offset:5280
	ds_read_b128 v[84:87], v1 offset:5296
	s_waitcnt lgkmcnt(3)
	v_mfma_f32_32x32x16_f16 v[2:17], v[102:105], v[88:91], v[2:17]
	s_waitcnt lgkmcnt(2)
	v_mfma_f32_32x32x16_f16 v[2:17], v[98:101], v[92:95], v[2:17]
	v_mfma_f32_32x32x16_f16 v[2:17], v[98:101], v[88:91], v[2:17]
	ds_read_b128 v[88:91], v1 offset:15680
	ds_read_b128 v[92:95], v1 offset:15696
	s_waitcnt vmcnt(6) lgkmcnt(3)
	v_mfma_f32_32x32x16_f16 v[50:65], v[134:137], v[80:83], v[50:65]
	s_waitcnt lgkmcnt(2)
	v_mfma_f32_32x32x16_f16 v[50:65], v[130:133], v[84:87], v[50:65]
	v_mfma_f32_32x32x16_f16 v[50:65], v[130:133], v[80:83], v[50:65]
	ds_read_b128 v[80:83], v1 offset:26080
	ds_read_b128 v[84:87], v1 offset:26096
	s_waitcnt lgkmcnt(3)
	v_mfma_f32_32x32x16_f16 v[34:49], v[134:137], v[88:91], v[34:49]
	s_waitcnt lgkmcnt(2)
	v_mfma_f32_32x32x16_f16 v[34:49], v[130:133], v[92:95], v[34:49]
	v_mfma_f32_32x32x16_f16 v[34:49], v[130:133], v[88:91], v[34:49]
	ds_read_b128 v[88:91], v1 offset:36480
	ds_read_b128 v[92:95], v1 offset:36496
	s_waitcnt lgkmcnt(3)
	v_mfma_f32_32x32x16_f16 v[18:33], v[134:137], v[80:83], v[18:33]
	s_waitcnt lgkmcnt(2)
	v_mfma_f32_32x32x16_f16 v[18:33], v[130:133], v[84:87], v[18:33]
	v_mfma_f32_32x32x16_f16 v[18:33], v[130:133], v[80:83], v[18:33]
	ds_read_b128 v[80:83], v1 offset:10400
	ds_read_b128 v[84:87], v1 offset:10416
	s_waitcnt lgkmcnt(3)
	v_mfma_f32_32x32x16_f16 v[2:17], v[134:137], v[88:91], v[2:17]
	s_waitcnt lgkmcnt(2)
	v_mfma_f32_32x32x16_f16 v[2:17], v[130:133], v[92:95], v[2:17]
	v_mfma_f32_32x32x16_f16 v[2:17], v[130:133], v[88:91], v[2:17]
	ds_read_b128 v[88:91], v1 offset:20800
	ds_read_b128 v[92:95], v1 offset:20816
	s_waitcnt vmcnt(4) lgkmcnt(3)
	v_mfma_f32_32x32x16_f16 v[50:65], v[126:129], v[80:83], v[50:65]
	s_waitcnt lgkmcnt(2)
	v_mfma_f32_32x32x16_f16 v[50:65], v[122:125], v[84:87], v[50:65]
	v_mfma_f32_32x32x16_f16 v[50:65], v[122:125], v[80:83], v[50:65]
	ds_read_b128 v[80:83], v1 offset:31200
	ds_read_b128 v[84:87], v1 offset:31216
	s_waitcnt lgkmcnt(3)
	v_mfma_f32_32x32x16_f16 v[34:49], v[126:129], v[88:91], v[34:49]
	s_waitcnt lgkmcnt(2)
	v_mfma_f32_32x32x16_f16 v[34:49], v[122:125], v[92:95], v[34:49]
	v_mfma_f32_32x32x16_f16 v[34:49], v[122:125], v[88:91], v[34:49]
	ds_read_b128 v[88:91], v1 offset:41600
	ds_read_b128 v[92:95], v1 offset:41616
	s_waitcnt lgkmcnt(3)
	v_mfma_f32_32x32x16_f16 v[18:33], v[126:129], v[80:83], v[18:33]
	s_waitcnt lgkmcnt(2)
	v_mfma_f32_32x32x16_f16 v[18:33], v[122:125], v[84:87], v[18:33]
	v_mfma_f32_32x32x16_f16 v[18:33], v[122:125], v[80:83], v[18:33]
	ds_read_b128 v[80:83], v1 offset:13040
	ds_read_b128 v[84:87], v1 offset:13056
	s_waitcnt lgkmcnt(3)
	v_mfma_f32_32x32x16_f16 v[2:17], v[126:129], v[88:91], v[2:17]
	s_waitcnt lgkmcnt(2)
	v_mfma_f32_32x32x16_f16 v[2:17], v[122:125], v[92:95], v[2:17]
	v_mfma_f32_32x32x16_f16 v[2:17], v[122:125], v[88:91], v[2:17]
	ds_read_b128 v[88:91], v1 offset:23440
	ds_read_b128 v[92:95], v1 offset:23456
	s_waitcnt vmcnt(2) lgkmcnt(3)
	v_mfma_f32_32x32x16_f16 v[50:65], v[118:121], v[80:83], v[50:65]
	s_waitcnt lgkmcnt(2)
	v_mfma_f32_32x32x16_f16 v[50:65], v[114:117], v[84:87], v[50:65]
	v_mfma_f32_32x32x16_f16 v[50:65], v[114:117], v[80:83], v[50:65]
	ds_read_b128 v[80:83], v1 offset:33840
	ds_read_b128 v[84:87], v1 offset:33856
	s_waitcnt lgkmcnt(3)
	v_mfma_f32_32x32x16_f16 v[34:49], v[118:121], v[88:91], v[34:49]
	s_waitcnt lgkmcnt(2)
	v_mfma_f32_32x32x16_f16 v[34:49], v[114:117], v[92:95], v[34:49]
	v_mfma_f32_32x32x16_f16 v[34:49], v[114:117], v[88:91], v[34:49]
	ds_read_b128 v[88:91], v1 offset:44240
	ds_read_b128 v[92:95], v1 offset:44256
	s_waitcnt lgkmcnt(3)
	v_mfma_f32_32x32x16_f16 v[18:33], v[118:121], v[80:83], v[18:33]
	s_waitcnt lgkmcnt(2)
	v_mfma_f32_32x32x16_f16 v[18:33], v[114:117], v[84:87], v[18:33]
	v_mfma_f32_32x32x16_f16 v[18:33], v[114:117], v[80:83], v[18:33]
	ds_read_b128 v[80:83], v1 offset:10480
	ds_read_b128 v[84:87], v1 offset:10496
	s_waitcnt lgkmcnt(3)
	v_mfma_f32_32x32x16_f16 v[2:17], v[118:121], v[88:91], v[2:17]
	s_waitcnt lgkmcnt(2)
	v_mfma_f32_32x32x16_f16 v[2:17], v[114:117], v[92:95], v[2:17]
	v_mfma_f32_32x32x16_f16 v[2:17], v[114:117], v[88:91], v[2:17]
	ds_read_b128 v[88:91], v1 offset:20880
	ds_read_b128 v[92:95], v1 offset:20896
	s_waitcnt vmcnt(0) lgkmcnt(3)
	v_mfma_f32_32x32x16_f16 v[50:65], v[110:113], v[80:83], v[50:65]
	s_waitcnt lgkmcnt(2)
	v_mfma_f32_32x32x16_f16 v[50:65], v[106:109], v[84:87], v[50:65]
	v_mfma_f32_32x32x16_f16 v[50:65], v[106:109], v[80:83], v[50:65]
	ds_read_b128 v[80:83], v1 offset:31280
	ds_read_b128 v[84:87], v1 offset:31296
	s_waitcnt lgkmcnt(3)
	v_mfma_f32_32x32x16_f16 v[34:49], v[110:113], v[88:91], v[34:49]
	s_waitcnt lgkmcnt(2)
	v_mfma_f32_32x32x16_f16 v[34:49], v[106:109], v[92:95], v[34:49]
	v_mfma_f32_32x32x16_f16 v[34:49], v[106:109], v[88:91], v[34:49]
	ds_read_b128 v[88:91], v1 offset:41680
	ds_read_b128 v[92:95], v1 offset:41696
	s_waitcnt lgkmcnt(3)
	v_mfma_f32_32x32x16_f16 v[18:33], v[110:113], v[80:83], v[18:33]
	s_waitcnt lgkmcnt(2)
	v_mfma_f32_32x32x16_f16 v[18:33], v[106:109], v[84:87], v[18:33]
	v_mfma_f32_32x32x16_f16 v[18:33], v[106:109], v[80:83], v[18:33]
	s_waitcnt lgkmcnt(1)
	v_mfma_f32_32x32x16_f16 v[2:17], v[110:113], v[88:91], v[2:17]
	s_waitcnt lgkmcnt(0)
	v_mfma_f32_32x32x16_f16 v[2:17], v[106:109], v[92:95], v[2:17]
	v_mfma_f32_32x32x16_f16 v[2:17], v[106:109], v[88:91], v[2:17]
	s_add_u32 s64, s62, 0x36000
	s_addc_u32 s65, s63, 0
	global_load_dwordx4 v[130:133], v96, s[64:65]
	global_load_dwordx4 v[134:137], v96, s[64:65] offset:16
	s_add_u32 s64, s62, 0x38000
	s_addc_u32 s65, s63, 0
	global_load_dwordx4 v[122:125], v96, s[64:65]
	global_load_dwordx4 v[126:129], v96, s[64:65] offset:16
	s_add_u32 s64, s62, 0x3a000
	s_addc_u32 s65, s63, 0
	global_load_dwordx4 v[114:117], v96, s[64:65]
	global_load_dwordx4 v[118:121], v96, s[64:65] offset:16
	s_add_u32 s64, s62, 0x3c000
	s_addc_u32 s65, s63, 0
	global_load_dwordx4 v[106:109], v96, s[64:65]
	global_load_dwordx4 v[110:113], v96, s[64:65] offset:16
	s_add_u32 s64, s62, 0x3e000
	s_addc_u32 s65, s63, 0
	global_load_dwordx4 v[98:101], v96, s[64:65]
	global_load_dwordx4 v[102:105], v96, s[64:65] offset:16
	v_mov_b32_e32 v138, v0
	s_and_b64 vcc, exec, s[0:1]
	s_barrier
	s_cbranch_vccnz .LBB4_66
	s_waitcnt vmcnt(57)
	v_mov_b32_e32 v78, 0
	s_waitcnt vmcnt(56)
	v_mov_b32_e32 v77, 0
	s_waitcnt vmcnt(55)
	v_mov_b32_e32 v66, 0
	s_waitcnt vmcnt(54)
	v_mov_b32_e32 v67, v78
	s_waitcnt vmcnt(53)
	v_mov_b32_e32 v164, 0
	s_waitcnt vmcnt(52)
	v_mov_b32_e32 v165, v78
	s_waitcnt vmcnt(51)
	v_mov_b32_e32 v166, 0
	s_waitcnt vmcnt(50)
	v_mov_b32_e32 v167, v78
.LBB4_66:
	v_and_b32_e32 v139, 63, v138
	v_add_u32_e32 v79, 1, v139
	v_and_b32_e32 v138, 1, v138
	v_lshrrev_b32_e32 v79, 1, v79
	v_add_u32_e32 v80, 33, v79
	v_cmp_eq_u32_e32 vcc, 0, v138
	s_movk_i32 s0, 0x50
	s_waitcnt vmcnt(56)
	v_mul_f32_e32 v82, 0x41800000, v77
	v_cndmask_b32_e32 v79, v79, v80, vcc
	v_mov_b32_e32 v80, s33
	v_mad_u32_u24 v88, v79, s0, v80
	s_mov_b32 s0, 0x41800000
	v_fma_mixlo_f16 v80, v78, s0, 0
	v_mul_u32_u24_e32 v138, 0x50, v79
	v_mul_f32_e32 v79, 0x41800000, v78
	v_fma_mixlo_f16 v78, v78, s0, -v80 op_sel_hi:[0,0,1]
	s_waitcnt vmcnt(54)
	v_pk_mul_f32 v[80:81], v[66:67], s[0:1] op_sel_hi:[1,0]
	v_fma_mixlo_f16 v84, v77, s0, 0
	v_cvt_pk_f16_f32 v83, v80, v81
	v_cvt_f32_f16_e32 v80, v83
	v_cvt_f32_f16_sdwa v81, v83 dst_sel:DWORD dst_unused:UNUSED_PAD src0_sel:WORD_1
	v_fma_mixhi_f16 v78, v77, s0, -v84 op_sel_hi:[0,0,1]
	s_waitcnt vmcnt(50)
	v_pk_mul_f32 v[86:87], v[166:167], s[0:1] op_sel_hi:[1,0]
	v_cvt_pk_f16_f32 v82, v79, v82
	v_pk_fma_f32 v[66:67], v[66:67], s[0:1], v[80:81] op_sel_hi:[1,0,1] neg_lo:[0,0,1] neg_hi:[0,0,1]
	v_pk_mul_f32 v[80:81], v[164:165], s[0:1] op_sel_hi:[1,0]
	v_cvt_pk_f16_f32 v85, v86, v87
	v_cvt_pk_f16_f32 v84, v80, v81
	v_cvt_f32_f16_e32 v80, v84
	v_cvt_f32_f16_sdwa v81, v84 dst_sel:DWORD dst_unused:UNUSED_PAD src0_sel:WORD_1
	v_cvt_f32_f16_e32 v86, v85
	v_cvt_f32_f16_sdwa v87, v85 dst_sel:DWORD dst_unused:UNUSED_PAD src0_sel:WORD_1
	v_cvt_pk_f16_f32 v79, v66, v67
	v_pk_fma_f32 v[164:165], v[164:165], s[0:1], v[80:81] op_sel_hi:[1,0,1] neg_lo:[0,0,1] neg_hi:[0,0,1]
	s_and_b64 vcc, exec, s[12:13]
	v_cvt_pk_f16_f32 v80, v164, v165
	v_pk_fma_f32 v[164:165], v[166:167], s[0:1], v[86:87] op_sel_hi:[1,0,1] neg_lo:[0,0,1] neg_hi:[0,0,1]
	ds_write_b128 v88, v[82:85]
	v_cvt_pk_f16_f32 v81, v164, v165
	ds_write_b128 v88, v[78:81] offset:16
	s_cbranch_vccnz .LBB4_68
	s_waitcnt vmcnt(49)
	v_mov_b32_e32 v76, 0
	s_waitcnt vmcnt(48)
	v_mov_b32_e32 v75, 0
	s_waitcnt vmcnt(47)
	v_mov_b32_e32 v162, 0
	s_waitcnt vmcnt(46)
	v_mov_b32_e32 v163, v76
	s_waitcnt vmcnt(45)
	v_mov_b32_e32 v158, 0
	s_waitcnt vmcnt(44)
	v_mov_b32_e32 v159, v76
	s_waitcnt vmcnt(43)
	v_mov_b32_e32 v160, 0
	s_waitcnt vmcnt(42)
	v_mov_b32_e32 v161, v76
.LBB4_68:
	s_waitcnt vmcnt(46)
	v_pk_mul_f32 v[166:167], v[162:163], s[0:1] op_sel_hi:[1,0]
	v_fma_mixlo_f16 v164, v76, s0, 0
	v_cvt_pk_f16_f32 v77, v166, v167
	v_cvt_f32_f16_e32 v166, v77
	v_cvt_f32_f16_sdwa v167, v77 dst_sel:DWORD dst_unused:UNUSED_PAD src0_sel:WORD_1
	v_mul_f32_e32 v165, 0x41800000, v76
	v_fma_mixlo_f16 v164, v76, s0, -v164 op_sel_hi:[0,0,1]
	v_mul_f32_e32 v66, 0x41800000, v75
	v_fma_mixlo_f16 v67, v75, s0, 0
	v_pk_fma_f32 v[162:163], v[162:163], s[0:1], v[166:167] op_sel_hi:[1,0,1] neg_lo:[0,0,1] neg_hi:[0,0,1]
	s_waitcnt vmcnt(44)
	v_pk_mul_f32 v[166:167], v[158:159], s[0:1] op_sel_hi:[1,0]
	v_cvt_pk_f16_f32 v76, v165, v66
	v_fma_mixhi_f16 v164, v75, s0, -v67 op_sel_hi:[0,0,1]
	v_cvt_pk_f16_f32 v78, v166, v167
	s_waitcnt vmcnt(42)
	v_pk_mul_f32 v[66:67], v[160:161], s[0:1] op_sel_hi:[1,0]
	v_cvt_f32_f16_e32 v166, v78
	v_cvt_f32_f16_sdwa v167, v78 dst_sel:DWORD dst_unused:UNUSED_PAD src0_sel:WORD_1
	v_cvt_pk_f16_f32 v79, v66, v67
	v_cvt_f32_f16_e32 v66, v79
	v_cvt_f32_f16_sdwa v67, v79 dst_sel:DWORD dst_unused:UNUSED_PAD src0_sel:WORD_1
	v_pk_fma_f32 v[158:159], v[158:159], s[0:1], v[166:167] op_sel_hi:[1,0,1] neg_lo:[0,0,1] neg_hi:[0,0,1]
	v_add_u32_e32 v80, s50, v138
	v_cvt_pk_f16_f32 v166, v158, v159
	v_pk_fma_f32 v[158:159], v[160:161], s[0:1], v[66:67] op_sel_hi:[1,0,1] neg_lo:[0,0,1] neg_hi:[0,0,1]
	v_cvt_pk_f16_f32 v165, v162, v163
	v_cvt_pk_f16_f32 v167, v158, v159
	s_and_b64 vcc, exec, s[6:7]
	ds_write_b128 v80, v[76:79]
	ds_write_b128 v80, v[164:167] offset:16
	s_cbranch_vccnz .LBB4_70
	s_waitcnt vmcnt(41)
	v_mov_b32_e32 v74, 0
	s_waitcnt vmcnt(40)
	v_mov_b32_e32 v73, 0
	s_waitcnt vmcnt(39)
	v_mov_b32_e32 v156, 0
	s_waitcnt vmcnt(38)
	v_mov_b32_e32 v157, v74
	s_waitcnt vmcnt(37)
	v_mov_b32_e32 v152, 0
	s_waitcnt vmcnt(36)
	v_mov_b32_e32 v153, v74
	s_waitcnt vmcnt(35)
	v_mov_b32_e32 v154, 0
	s_waitcnt vmcnt(34)
	v_mov_b32_e32 v155, v74
.LBB4_70:
	s_waitcnt vmcnt(38)
	v_pk_mul_f32 v[160:161], v[156:157], s[0:1] op_sel_hi:[1,0]
	v_fma_mixlo_f16 v158, v74, s0, 0
	v_cvt_pk_f16_f32 v163, v160, v161
	v_cvt_f32_f16_e32 v160, v163
	v_cvt_f32_f16_sdwa v161, v163 dst_sel:DWORD dst_unused:UNUSED_PAD src0_sel:WORD_1
	v_fma_mixlo_f16 v158, v74, s0, -v158 op_sel_hi:[0,0,1]
	v_fma_mixlo_f16 v164, v73, s0, 0
	v_fma_mixhi_f16 v158, v73, s0, -v164 op_sel_hi:[0,0,1]
	v_pk_fma_f32 v[156:157], v[156:157], s[0:1], v[160:161] op_sel_hi:[1,0,1] neg_lo:[0,0,1] neg_hi:[0,0,1]
	s_waitcnt vmcnt(36)
	v_pk_mul_f32 v[160:161], v[152:153], s[0:1] op_sel_hi:[1,0]
	s_waitcnt vmcnt(34)
	v_pk_mul_f32 v[166:167], v[154:155], s[0:1] op_sel_hi:[1,0]
	v_cvt_pk_f16_f32 v164, v160, v161
	v_cvt_f32_f16_e32 v160, v164
	v_cvt_f32_f16_sdwa v161, v164 dst_sel:DWORD dst_unused:UNUSED_PAD src0_sel:WORD_1
	v_cvt_pk_f16_f32 v165, v166, v167
	v_cvt_f32_f16_e32 v166, v165
	v_cvt_f32_f16_sdwa v167, v165 dst_sel:DWORD dst_unused:UNUSED_PAD src0_sel:WORD_1
	v_pk_fma_f32 v[152:153], v[152:153], s[0:1], v[160:161] op_sel_hi:[1,0,1] neg_lo:[0,0,1] neg_hi:[0,0,1]
	v_mul_f32_e32 v159, 0x41800000, v74
	v_mul_f32_e32 v162, 0x41800000, v73
	v_cvt_pk_f16_f32 v160, v152, v153
	v_pk_fma_f32 v[152:153], v[154:155], s[0:1], v[166:167] op_sel_hi:[1,0,1] neg_lo:[0,0,1] neg_hi:[0,0,1]
	v_add_u32_e32 v66, s51, v138
	v_cvt_pk_f16_f32 v162, v159, v162
	v_cvt_pk_f16_f32 v159, v156, v157
	v_cvt_pk_f16_f32 v161, v152, v153
	s_and_b64 vcc, exec, s[8:9]
	ds_write_b128 v66, v[162:165]
	ds_write_b128 v66, v[158:161] offset:16
	s_cbranch_vccnz .LBB4_72
	s_waitcnt vmcnt(33)
	v_mov_b32_e32 v72, 0
	s_waitcnt vmcnt(32)
	v_mov_b32_e32 v71, 0
	s_waitcnt vmcnt(31)
	v_mov_b32_e32 v150, 0
	s_waitcnt vmcnt(30)
	v_mov_b32_e32 v151, v72
	s_waitcnt vmcnt(29)
	v_mov_b32_e32 v146, 0
	s_waitcnt vmcnt(28)
	v_mov_b32_e32 v147, v72
	s_waitcnt vmcnt(27)
	v_mov_b32_e32 v148, 0
	s_waitcnt vmcnt(26)
	v_mov_b32_e32 v149, v72
.LBB4_72:
	s_waitcnt vmcnt(30)
	v_pk_mul_f32 v[154:155], v[150:151], s[0:1] op_sel_hi:[1,0]
	v_fma_mixlo_f16 v152, v72, s0, 0
	v_cvt_pk_f16_f32 v157, v154, v155
	v_cvt_f32_f16_e32 v154, v157
	v_cvt_f32_f16_sdwa v155, v157 dst_sel:DWORD dst_unused:UNUSED_PAD src0_sel:WORD_1
	v_fma_mixlo_f16 v152, v72, s0, -v152 op_sel_hi:[0,0,1]
	v_fma_mixlo_f16 v158, v71, s0, 0
	v_fma_mixhi_f16 v152, v71, s0, -v158 op_sel_hi:[0,0,1]
	v_pk_fma_f32 v[150:151], v[150:151], s[0:1], v[154:155] op_sel_hi:[1,0,1] neg_lo:[0,0,1] neg_hi:[0,0,1]
	s_waitcnt vmcnt(28)
	v_pk_mul_f32 v[154:155], v[146:147], s[0:1] op_sel_hi:[1,0]
	s_waitcnt vmcnt(26)
	v_pk_mul_f32 v[160:161], v[148:149], s[0:1] op_sel_hi:[1,0]
	v_cvt_pk_f16_f32 v158, v154, v155
	v_cvt_f32_f16_e32 v154, v158
	v_cvt_f32_f16_sdwa v155, v158 dst_sel:DWORD dst_unused:UNUSED_PAD src0_sel:WORD_1
	v_cvt_pk_f16_f32 v159, v160, v161
	v_cvt_f32_f16_e32 v160, v159
	v_cvt_f32_f16_sdwa v161, v159 dst_sel:DWORD dst_unused:UNUSED_PAD src0_sel:WORD_1
	v_pk_fma_f32 v[146:147], v[146:147], s[0:1], v[154:155] op_sel_hi:[1,0,1] neg_lo:[0,0,1] neg_hi:[0,0,1]
	v_mul_f32_e32 v153, 0x41800000, v72
	v_mul_f32_e32 v156, 0x41800000, v71
	v_cvt_pk_f16_f32 v154, v146, v147
	v_pk_fma_f32 v[146:147], v[148:149], s[0:1], v[160:161] op_sel_hi:[1,0,1] neg_lo:[0,0,1] neg_hi:[0,0,1]
	v_add_u32_e32 v162, s52, v138
	v_cvt_pk_f16_f32 v156, v153, v156
	v_cvt_pk_f16_f32 v153, v150, v151
	v_cvt_pk_f16_f32 v155, v146, v147
	s_and_b64 vcc, exec, s[10:11]
	ds_write_b128 v162, v[156:159] offset:32
	ds_write_b128 v162, v[152:155] offset:48
	s_cbranch_vccnz .LBB4_74
	v_cmp_lt_u32_e32 vcc, 8, v139
	v_min_u32_e32 v146, 17, v139
	s_movk_i32 s0, 0x1450
	v_cndmask_b32_e64 v147, 0, -9, vcc
	v_add_u32_e32 v147, v147, v146
	v_cndmask_b32_e64 v146, 0, 32, vcc
	v_cmp_lt_i32_e32 vcc, s5, v147
	s_and_b64 s[6:7], s[24:25], vcc
	v_cmp_gt_u32_e32 vcc, 18, v139
	v_mad_i32_i24 v146, v147, s0, v146
	s_and_b64 s[8:9], s[26:27], vcc
	s_cbranch_execz .LBB4_75
	s_branch .LBB4_76

.LBB4_76:
	s_and_saveexec_b64 s[0:1], s[8:9]
	s_cbranch_execz .LBB4_80
	s_xor_b64 s[8:9], s[6:7], -1
	s_and_saveexec_b64 s[6:7], s[8:9]
	s_cbranch_execz .LBB4_79
	s_waitcnt vmcnt(24)
	v_mov_b32_e32 v69, 0
	v_mov_b32_e32 v70, 0
	s_waitcnt vmcnt(23)
	v_mov_b32_e32 v144, 0
	s_waitcnt vmcnt(22)
	v_mov_b32_e32 v145, v69
	s_waitcnt vmcnt(21)
	v_mov_b32_e32 v140, 0
	s_waitcnt vmcnt(20)
	v_mov_b32_e32 v141, v69
	s_waitcnt vmcnt(19)
	v_mov_b32_e32 v142, 0
	s_waitcnt vmcnt(18)
	v_mov_b32_e32 v143, v69
.LBB4_79:
	s_or_b64 exec, exec, s[6:7]
	s_mov_b32 s6, 0x41800000
	s_waitcnt vmcnt(22)
	v_pk_mul_f32 v[148:149], v[144:145], s[6:7] op_sel_hi:[1,0]
	v_fma_mixlo_f16 v138, v70, s6, 0
	v_cvt_pk_f16_f32 v149, v148, v149
	v_cvt_f32_f16_e32 v150, v149
	v_cvt_f32_f16_sdwa v151, v149 dst_sel:DWORD dst_unused:UNUSED_PAD src0_sel:WORD_1
	s_waitcnt vmcnt(18)
	v_pk_mul_f32 v[154:155], v[142:143], s[6:7] op_sel_hi:[1,0]
	v_fma_mixlo_f16 v138, v70, s6, -v138 op_sel_hi:[0,0,1]
	v_fma_mixlo_f16 v152, v69, s6, 0
	v_pk_fma_f32 v[144:145], v[144:145], s[6:7], v[150:151] op_sel_hi:[1,0,1] neg_lo:[0,0,1] neg_hi:[0,0,1]
	v_pk_mul_f32 v[150:151], v[140:141], s[6:7] op_sel_hi:[1,0]
	v_fma_mixhi_f16 v138, v69, s6, -v152 op_sel_hi:[0,0,1]
	v_cvt_pk_f16_f32 v150, v150, v151
	v_cvt_pk_f16_f32 v151, v154, v155
	v_cvt_f32_f16_e32 v152, v150
	v_cvt_f32_f16_sdwa v153, v150 dst_sel:DWORD dst_unused:UNUSED_PAD src0_sel:WORD_1
	v_cvt_f32_f16_e32 v154, v151
	v_cvt_f32_f16_sdwa v155, v151 dst_sel:DWORD dst_unused:UNUSED_PAD src0_sel:WORD_1
	v_mul_f32_e32 v139, 0x41800000, v70
	v_mul_f32_e32 v147, 0x41800000, v69
	v_cvt_pk_f16_f32 v148, v139, v147
	v_pk_fma_f32 v[140:141], v[140:141], s[6:7], v[152:153] op_sel_hi:[1,0,1] neg_lo:[0,0,1] neg_hi:[0,0,1]
	v_pk_fma_f32 v[142:143], v[142:143], s[6:7], v[154:155] op_sel_hi:[1,0,1] neg_lo:[0,0,1] neg_hi:[0,0,1]
	v_cvt_pk_f16_f32 v139, v144, v145
	v_cvt_pk_f16_f32 v140, v140, v141
	v_cvt_pk_f16_f32 v141, v142, v143
	ds_write_b128 v146, v[148:151]
	ds_write_b128 v146, v[138:141] offset:16
.LBB4_80:
	s_or_b64 exec, exec, s[0:1]
	s_lshl_b32 s6, s3, 2
	s_waitcnt lgkmcnt(0)
	s_barrier
	s_waitcnt vmcnt(20)
	ds_read_b128 v[80:83], v1
	ds_read_b128 v[84:87], v1 offset:16
	ds_read_b128 v[88:91], v1 offset:10400
	ds_read_b128 v[92:95], v1 offset:10416
	s_waitcnt vmcnt(8) lgkmcnt(3)
	v_mfma_f32_32x32x16_f16 v[50:65], v[134:137], v[80:83], v[50:65]
	s_waitcnt lgkmcnt(2)
	v_mfma_f32_32x32x16_f16 v[50:65], v[130:133], v[84:87], v[50:65]
	v_mfma_f32_32x32x16_f16 v[50:65], v[130:133], v[80:83], v[50:65]
	ds_read_b128 v[80:83], v1 offset:20800
	ds_read_b128 v[84:87], v1 offset:20816
	s_waitcnt lgkmcnt(3)
	v_mfma_f32_32x32x16_f16 v[34:49], v[134:137], v[88:91], v[34:49]
	s_waitcnt lgkmcnt(2)
	v_mfma_f32_32x32x16_f16 v[34:49], v[130:133], v[92:95], v[34:49]
	v_mfma_f32_32x32x16_f16 v[34:49], v[130:133], v[88:91], v[34:49]
	ds_read_b128 v[88:91], v1 offset:31200
	ds_read_b128 v[92:95], v1 offset:31216
	s_waitcnt lgkmcnt(3)
	v_mfma_f32_32x32x16_f16 v[18:33], v[134:137], v[80:83], v[18:33]
	s_waitcnt lgkmcnt(2)
	v_mfma_f32_32x32x16_f16 v[18:33], v[130:133], v[84:87], v[18:33]
	v_mfma_f32_32x32x16_f16 v[18:33], v[130:133], v[80:83], v[18:33]
	ds_read_b128 v[80:83], v1 offset:2640
	ds_read_b128 v[84:87], v1 offset:2656
	s_waitcnt lgkmcnt(3)
	v_mfma_f32_32x32x16_f16 v[2:17], v[134:137], v[88:91], v[2:17]
	s_waitcnt lgkmcnt(2)
	v_mfma_f32_32x32x16_f16 v[2:17], v[130:133], v[92:95], v[2:17]
	v_mfma_f32_32x32x16_f16 v[2:17], v[130:133], v[88:91], v[2:17]
	ds_read_b128 v[88:91], v1 offset:13040
	ds_read_b128 v[92:95], v1 offset:13056
	s_waitcnt vmcnt(6) lgkmcnt(3)
	v_mfma_f32_32x32x16_f16 v[50:65], v[126:129], v[80:83], v[50:65]
	s_waitcnt lgkmcnt(2)
	v_mfma_f32_32x32x16_f16 v[50:65], v[122:125], v[84:87], v[50:65]
	v_mfma_f32_32x32x16_f16 v[50:65], v[122:125], v[80:83], v[50:65]
	ds_read_b128 v[80:83], v1 offset:23440
	ds_read_b128 v[84:87], v1 offset:23456
	s_waitcnt lgkmcnt(3)
	v_mfma_f32_32x32x16_f16 v[34:49], v[126:129], v[88:91], v[34:49]
	s_waitcnt lgkmcnt(2)
	v_mfma_f32_32x32x16_f16 v[34:49], v[122:125], v[92:95], v[34:49]
	v_mfma_f32_32x32x16_f16 v[34:49], v[122:125], v[88:91], v[34:49]
	ds_read_b128 v[88:91], v1 offset:33840
	ds_read_b128 v[92:95], v1 offset:33856
	s_waitcnt lgkmcnt(3)
	v_mfma_f32_32x32x16_f16 v[18:33], v[126:129], v[80:83], v[18:33]
	s_waitcnt lgkmcnt(2)
	v_mfma_f32_32x32x16_f16 v[18:33], v[122:125], v[84:87], v[18:33]
	v_mfma_f32_32x32x16_f16 v[18:33], v[122:125], v[80:83], v[18:33]
	ds_read_b128 v[80:83], v1 offset:80
	ds_read_b128 v[84:87], v1 offset:96
	s_waitcnt lgkmcnt(3)
	v_mfma_f32_32x32x16_f16 v[2:17], v[126:129], v[88:91], v[2:17]
	s_waitcnt lgkmcnt(2)
	v_mfma_f32_32x32x16_f16 v[2:17], v[122:125], v[92:95], v[2:17]
	v_mfma_f32_32x32x16_f16 v[2:17], v[122:125], v[88:91], v[2:17]
	ds_read_b128 v[88:91], v1 offset:10480
	ds_read_b128 v[92:95], v1 offset:10496
	s_waitcnt vmcnt(4) lgkmcnt(3)
	v_mfma_f32_32x32x16_f16 v[50:65], v[118:121], v[80:83], v[50:65]
	s_waitcnt lgkmcnt(2)
	v_mfma_f32_32x32x16_f16 v[50:65], v[114:117], v[84:87], v[50:65]
	v_mfma_f32_32x32x16_f16 v[50:65], v[114:117], v[80:83], v[50:65]
	ds_read_b128 v[80:83], v1 offset:20880
	ds_read_b128 v[84:87], v1 offset:20896
	s_waitcnt lgkmcnt(3)
	v_mfma_f32_32x32x16_f16 v[34:49], v[118:121], v[88:91], v[34:49]
	s_waitcnt lgkmcnt(2)
	v_mfma_f32_32x32x16_f16 v[34:49], v[114:117], v[92:95], v[34:49]
	v_mfma_f32_32x32x16_f16 v[34:49], v[114:117], v[88:91], v[34:49]
	ds_read_b128 v[88:91], v1 offset:31280
	ds_read_b128 v[92:95], v1 offset:31296
	s_waitcnt lgkmcnt(3)
	v_mfma_f32_32x32x16_f16 v[18:33], v[118:121], v[80:83], v[18:33]
	s_waitcnt lgkmcnt(2)
	v_mfma_f32_32x32x16_f16 v[18:33], v[114:117], v[84:87], v[18:33]
	v_mfma_f32_32x32x16_f16 v[18:33], v[114:117], v[80:83], v[18:33]
	ds_read_b128 v[80:83], v1 offset:5200
	ds_read_b128 v[84:87], v1 offset:5216
	s_waitcnt lgkmcnt(3)
	v_mfma_f32_32x32x16_f16 v[2:17], v[118:121], v[88:91], v[2:17]
	s_waitcnt lgkmcnt(2)
	v_mfma_f32_32x32x16_f16 v[2:17], v[114:117], v[92:95], v[2:17]
	v_mfma_f32_32x32x16_f16 v[2:17], v[114:117], v[88:91], v[2:17]
	s_add_u32 s64, s62, 0x40000
	s_addc_u32 s65, s63, 0
	global_load_dwordx4 v[130:133], v96, s[64:65]
	global_load_dwordx4 v[134:137], v96, s[64:65] offset:16
	s_add_u32 s64, s62, 0x42000
	s_addc_u32 s65, s63, 0
	global_load_dwordx4 v[122:125], v96, s[64:65]
	global_load_dwordx4 v[126:129], v96, s[64:65] offset:16
	s_add_u32 s64, s62, 0x44000
	s_addc_u32 s65, s63, 0
	global_load_dwordx4 v[114:117], v96, s[64:65]
	global_load_dwordx4 v[118:121], v96, s[64:65] offset:16
	ds_read_b128 v[88:91], v1 offset:15600
	ds_read_b128 v[92:95], v1 offset:15616
	s_waitcnt vmcnt(8) lgkmcnt(3)
	v_mfma_f32_32x32x16_f16 v[50:65], v[110:113], v[80:83], v[50:65]
	s_waitcnt lgkmcnt(2)
	v_mfma_f32_32x32x16_f16 v[50:65], v[106:109], v[84:87], v[50:65]
	v_mfma_f32_32x32x16_f16 v[50:65], v[106:109], v[80:83], v[50:65]
	ds_read_b128 v[80:83], v1 offset:26000
	ds_read_b128 v[84:87], v1 offset:26016
	s_waitcnt lgkmcnt(3)
	v_mfma_f32_32x32x16_f16 v[34:49], v[110:113], v[88:91], v[34:49]
	s_waitcnt lgkmcnt(2)
	v_mfma_f32_32x32x16_f16 v[34:49], v[106:109], v[92:95], v[34:49]
	v_mfma_f32_32x32x16_f16 v[34:49], v[106:109], v[88:91], v[34:49]
	ds_read_b128 v[88:91], v1 offset:36400
	ds_read_b128 v[92:95], v1 offset:36416
	s_waitcnt lgkmcnt(3)
	v_mfma_f32_32x32x16_f16 v[18:33], v[110:113], v[80:83], v[18:33]
	s_waitcnt lgkmcnt(2)
	v_mfma_f32_32x32x16_f16 v[18:33], v[106:109], v[84:87], v[18:33]
	v_mfma_f32_32x32x16_f16 v[18:33], v[106:109], v[80:83], v[18:33]
	ds_read_b128 v[80:83], v1 offset:7840
	ds_read_b128 v[84:87], v1 offset:7856
	s_waitcnt lgkmcnt(3)
	v_mfma_f32_32x32x16_f16 v[2:17], v[110:113], v[88:91], v[2:17]
	s_waitcnt lgkmcnt(2)
	v_mfma_f32_32x32x16_f16 v[2:17], v[106:109], v[92:95], v[2:17]
	v_mfma_f32_32x32x16_f16 v[2:17], v[106:109], v[88:91], v[2:17]
	s_add_u32 s64, s62, 0x46000
	s_addc_u32 s65, s63, 0
	global_load_dwordx4 v[106:109], v96, s[64:65]
	global_load_dwordx4 v[110:113], v96, s[64:65] offset:16
	ds_read_b128 v[88:91], v1 offset:18240
	ds_read_b128 v[92:95], v1 offset:18256
	s_waitcnt vmcnt(8) lgkmcnt(3)
	v_mfma_f32_32x32x16_f16 v[50:65], v[102:105], v[80:83], v[50:65]
	s_waitcnt lgkmcnt(2)
	v_mfma_f32_32x32x16_f16 v[50:65], v[98:101], v[84:87], v[50:65]
	v_mfma_f32_32x32x16_f16 v[50:65], v[98:101], v[80:83], v[50:65]
	ds_read_b128 v[80:83], v1 offset:28640
	ds_read_b128 v[84:87], v1 offset:28656
	s_waitcnt lgkmcnt(3)
	v_mfma_f32_32x32x16_f16 v[34:49], v[102:105], v[88:91], v[34:49]
	s_waitcnt lgkmcnt(2)
	v_mfma_f32_32x32x16_f16 v[34:49], v[98:101], v[92:95], v[34:49]
	v_mfma_f32_32x32x16_f16 v[34:49], v[98:101], v[88:91], v[34:49]
	ds_read_b128 v[88:91], v1 offset:39040
	ds_read_b128 v[92:95], v1 offset:39056
	s_waitcnt lgkmcnt(3)
	v_mfma_f32_32x32x16_f16 v[18:33], v[102:105], v[80:83], v[18:33]
	s_waitcnt lgkmcnt(2)
	v_mfma_f32_32x32x16_f16 v[18:33], v[98:101], v[84:87], v[18:33]
	v_mfma_f32_32x32x16_f16 v[18:33], v[98:101], v[80:83], v[18:33]
	ds_read_b128 v[80:83], v1 offset:5280
	ds_read_b128 v[84:87], v1 offset:5296
	s_waitcnt lgkmcnt(3)
	v_mfma_f32_32x32x16_f16 v[2:17], v[102:105], v[88:91], v[2:17]
	s_waitcnt lgkmcnt(2)
	v_mfma_f32_32x32x16_f16 v[2:17], v[98:101], v[92:95], v[2:17]
	v_mfma_f32_32x32x16_f16 v[2:17], v[98:101], v[88:91], v[2:17]
	ds_read_b128 v[88:91], v1 offset:15680
	ds_read_b128 v[92:95], v1 offset:15696
	s_waitcnt vmcnt(6) lgkmcnt(3)
	v_mfma_f32_32x32x16_f16 v[50:65], v[134:137], v[80:83], v[50:65]
	s_waitcnt lgkmcnt(2)
	v_mfma_f32_32x32x16_f16 v[50:65], v[130:133], v[84:87], v[50:65]
	v_mfma_f32_32x32x16_f16 v[50:65], v[130:133], v[80:83], v[50:65]
	ds_read_b128 v[80:83], v1 offset:26080
	ds_read_b128 v[84:87], v1 offset:26096
	s_waitcnt lgkmcnt(3)
	v_mfma_f32_32x32x16_f16 v[34:49], v[134:137], v[88:91], v[34:49]
	s_waitcnt lgkmcnt(2)
	v_mfma_f32_32x32x16_f16 v[34:49], v[130:133], v[92:95], v[34:49]
	v_mfma_f32_32x32x16_f16 v[34:49], v[130:133], v[88:91], v[34:49]
	ds_read_b128 v[88:91], v1 offset:36480
	ds_read_b128 v[92:95], v1 offset:36496
	s_waitcnt lgkmcnt(3)
	v_mfma_f32_32x32x16_f16 v[18:33], v[134:137], v[80:83], v[18:33]
	s_waitcnt lgkmcnt(2)
	v_mfma_f32_32x32x16_f16 v[18:33], v[130:133], v[84:87], v[18:33]
	v_mfma_f32_32x32x16_f16 v[18:33], v[130:133], v[80:83], v[18:33]
	ds_read_b128 v[80:83], v1 offset:10400
	ds_read_b128 v[84:87], v1 offset:10416
	s_waitcnt lgkmcnt(3)
	v_mfma_f32_32x32x16_f16 v[2:17], v[134:137], v[88:91], v[2:17]
	s_waitcnt lgkmcnt(2)
	v_mfma_f32_32x32x16_f16 v[2:17], v[130:133], v[92:95], v[2:17]
	v_mfma_f32_32x32x16_f16 v[2:17], v[130:133], v[88:91], v[2:17]
	ds_read_b128 v[88:91], v1 offset:20800
	ds_read_b128 v[92:95], v1 offset:20816
	s_waitcnt vmcnt(4) lgkmcnt(3)
	v_mfma_f32_32x32x16_f16 v[50:65], v[126:129], v[80:83], v[50:65]
	s_waitcnt lgkmcnt(2)
	v_mfma_f32_32x32x16_f16 v[50:65], v[122:125], v[84:87], v[50:65]
	v_mfma_f32_32x32x16_f16 v[50:65], v[122:125], v[80:83], v[50:65]
	ds_read_b128 v[80:83], v1 offset:31200
	ds_read_b128 v[84:87], v1 offset:31216
	s_waitcnt lgkmcnt(3)
	v_mfma_f32_32x32x16_f16 v[34:49], v[126:129], v[88:91], v[34:49]
	s_waitcnt lgkmcnt(2)
	v_mfma_f32_32x32x16_f16 v[34:49], v[122:125], v[92:95], v[34:49]
	v_mfma_f32_32x32x16_f16 v[34:49], v[122:125], v[88:91], v[34:49]
	ds_read_b128 v[88:91], v1 offset:41600
	ds_read_b128 v[92:95], v1 offset:41616
	s_waitcnt lgkmcnt(3)
	v_mfma_f32_32x32x16_f16 v[18:33], v[126:129], v[80:83], v[18:33]
	s_waitcnt lgkmcnt(2)
	v_mfma_f32_32x32x16_f16 v[18:33], v[122:125], v[84:87], v[18:33]
	v_mfma_f32_32x32x16_f16 v[18:33], v[122:125], v[80:83], v[18:33]
	ds_read_b128 v[80:83], v1 offset:13040
	ds_read_b128 v[84:87], v1 offset:13056
	s_waitcnt lgkmcnt(3)
	v_mfma_f32_32x32x16_f16 v[2:17], v[126:129], v[88:91], v[2:17]
	s_waitcnt lgkmcnt(2)
	v_mfma_f32_32x32x16_f16 v[2:17], v[122:125], v[92:95], v[2:17]
	v_mfma_f32_32x32x16_f16 v[2:17], v[122:125], v[88:91], v[2:17]
	ds_read_b128 v[88:91], v1 offset:23440
	ds_read_b128 v[92:95], v1 offset:23456
	s_waitcnt vmcnt(2) lgkmcnt(3)
	v_mfma_f32_32x32x16_f16 v[50:65], v[118:121], v[80:83], v[50:65]
	s_waitcnt lgkmcnt(2)
	v_mfma_f32_32x32x16_f16 v[50:65], v[114:117], v[84:87], v[50:65]
	v_mfma_f32_32x32x16_f16 v[50:65], v[114:117], v[80:83], v[50:65]
	ds_read_b128 v[80:83], v1 offset:33840
	ds_read_b128 v[84:87], v1 offset:33856
	s_waitcnt lgkmcnt(3)
	v_mfma_f32_32x32x16_f16 v[34:49], v[118:121], v[88:91], v[34:49]
	s_waitcnt lgkmcnt(2)
	v_mfma_f32_32x32x16_f16 v[34:49], v[114:117], v[92:95], v[34:49]
	v_mfma_f32_32x32x16_f16 v[34:49], v[114:117], v[88:91], v[34:49]
	ds_read_b128 v[88:91], v1 offset:44240
	ds_read_b128 v[92:95], v1 offset:44256
	s_waitcnt lgkmcnt(3)
	v_mfma_f32_32x32x16_f16 v[18:33], v[118:121], v[80:83], v[18:33]
	s_waitcnt lgkmcnt(2)
	v_mfma_f32_32x32x16_f16 v[18:33], v[114:117], v[84:87], v[18:33]
	v_mfma_f32_32x32x16_f16 v[18:33], v[114:117], v[80:83], v[18:33]
	ds_read_b128 v[80:83], v1 offset:10480
	ds_read_b128 v[84:87], v1 offset:10496
	s_waitcnt lgkmcnt(3)
	v_mfma_f32_32x32x16_f16 v[2:17], v[118:121], v[88:91], v[2:17]
	s_waitcnt lgkmcnt(2)
	v_mfma_f32_32x32x16_f16 v[2:17], v[114:117], v[92:95], v[2:17]
	v_mfma_f32_32x32x16_f16 v[2:17], v[114:117], v[88:91], v[2:17]
	ds_read_b128 v[88:91], v1 offset:20880
	ds_read_b128 v[92:95], v1 offset:20896
	s_waitcnt vmcnt(0) lgkmcnt(3)
	v_mfma_f32_32x32x16_f16 v[50:65], v[110:113], v[80:83], v[50:65]
	s_waitcnt lgkmcnt(2)
	v_mfma_f32_32x32x16_f16 v[50:65], v[106:109], v[84:87], v[50:65]
	v_mfma_f32_32x32x16_f16 v[50:65], v[106:109], v[80:83], v[50:65]
	ds_read_b128 v[80:83], v1 offset:31280
	ds_read_b128 v[84:87], v1 offset:31296
	s_waitcnt lgkmcnt(3)
	v_mfma_f32_32x32x16_f16 v[34:49], v[110:113], v[88:91], v[34:49]
	s_waitcnt lgkmcnt(2)
	v_mfma_f32_32x32x16_f16 v[34:49], v[106:109], v[92:95], v[34:49]
	v_mfma_f32_32x32x16_f16 v[34:49], v[106:109], v[88:91], v[34:49]
	ds_read_b128 v[88:91], v1 offset:41680
	ds_read_b128 v[92:95], v1 offset:41696
	s_waitcnt lgkmcnt(3)
	v_mfma_f32_32x32x16_f16 v[18:33], v[110:113], v[80:83], v[18:33]
	s_waitcnt lgkmcnt(2)
	v_mfma_f32_32x32x16_f16 v[18:33], v[106:109], v[84:87], v[18:33]
	v_mfma_f32_32x32x16_f16 v[18:33], v[106:109], v[80:83], v[18:33]
	s_waitcnt lgkmcnt(1)
	v_mfma_f32_32x32x16_f16 v[2:17], v[110:113], v[88:91], v[2:17]
	s_waitcnt lgkmcnt(0)
	v_mfma_f32_32x32x16_f16 v[2:17], v[106:109], v[92:95], v[2:17]
	v_mfma_f32_32x32x16_f16 v[2:17], v[106:109], v[88:91], v[2:17]
	v_and_b32_e32 v151, 31, v0
	v_lshrrev_b32_e32 v66, 1, v0
	v_lshrrev_b32_e32 v67, 3, v0
	v_and_b32_e32 v66, 0x60, v66
	v_and_b32_e32 v67, 4, v67
	v_or_b32_e32 v66, v66, v67
	v_lshlrev_b32_e32 v66, 2, v66
	global_load_dwordx4 v[68:71], v66, s[14:15]
	global_load_dwordx4 v[72:75], v66, s[14:15] offset:32
	global_load_dwordx4 v[76:79], v66, s[14:15] offset:64
	global_load_dwordx4 v[80:83], v66, s[14:15] offset:96
	global_load_dwordx4 v[84:87], v66, s[14:15] offset:1024
	global_load_dwordx4 v[88:91], v66, s[14:15] offset:1056
	global_load_dwordx4 v[92:95], v66, s[14:15] offset:1088
	global_load_dwordx4 v[96:99], v66, s[14:15] offset:1120
	v_readfirstlane_b32 s24, v0
	v_lshlrev_b32_e32 v100, 5, v151
	v_lshl_add_u32 v100, v67, 2, v100
	v_lshl_or_b32 v101, s2, 5, v151
	v_cmp_eq_u32_e64 s[26:27], 0, v101
	s_lshr_b32 s24, s24, 6
	s_lshl_b32 s25, s4, 23
	s_lshl_b32 s24, s24, 21
	s_add_u32 s25, s25, s24
	s_lshl_b32 s24, s3, 14
	s_add_u32 s25, s25, s24
	s_lshl_b32 s24, s2, 10
	s_add_u32 s25, s25, s24
	s_add_u32 s22, s20, s25
	s_addc_u32 s23, s21, 0
	s_cmp_lg_u32 s3, 0
	s_cbranch_scc1 .Lc1e_inner
	global_load_dwordx4 v[118:121], v66, s[14:15] offset:512
	global_load_dwordx4 v[122:125], v66, s[14:15] offset:544
	global_load_dwordx4 v[126:129], v66, s[14:15] offset:576
	global_load_dwordx4 v[130:133], v66, s[14:15] offset:608
	global_load_dwordx4 v[134:137], v66, s[14:15] offset:1536
	global_load_dwordx4 v[138:141], v66, s[14:15] offset:1568
	global_load_dwordx4 v[142:145], v66, s[14:15] offset:1600
	global_load_dwordx4 v[146:149], v66, s[14:15] offset:1632
	s_waitcnt vmcnt(0)
	v_sub_f32_e32 v118, v68, v118
	v_sub_f32_e32 v150, v118, v84
	v_add_f32_e32 v150, v150, v134
	v_cndmask_b32_e64 v102, v118, v150, s[26:27]
	v_sub_f32_e32 v119, v69, v119
	v_sub_f32_e32 v150, v119, v85
	v_add_f32_e32 v150, v150, v135
	v_cndmask_b32_e64 v103, v119, v150, s[26:27]
	v_sub_f32_e32 v120, v70, v120
	v_sub_f32_e32 v150, v120, v86
	v_add_f32_e32 v150, v150, v136
	v_cndmask_b32_e64 v104, v120, v150, s[26:27]
	v_sub_f32_e32 v121, v71, v121
	v_sub_f32_e32 v150, v121, v87
	v_add_f32_e32 v150, v150, v137
	v_cndmask_b32_e64 v105, v121, v150, s[26:27]
	v_sub_f32_e32 v122, v72, v122
	v_sub_f32_e32 v150, v122, v88
	v_add_f32_e32 v150, v150, v138
	v_cndmask_b32_e64 v106, v122, v150, s[26:27]
	v_sub_f32_e32 v123, v73, v123
	v_sub_f32_e32 v150, v123, v89
	v_add_f32_e32 v150, v150, v139
	v_cndmask_b32_e64 v107, v123, v150, s[26:27]
	v_sub_f32_e32 v124, v74, v124
	v_sub_f32_e32 v150, v124, v90
	v_add_f32_e32 v150, v150, v140
	v_cndmask_b32_e64 v108, v124, v150, s[26:27]
	v_sub_f32_e32 v125, v75, v125
	v_sub_f32_e32 v150, v125, v91
	v_add_f32_e32 v150, v150, v141
	v_cndmask_b32_e64 v109, v125, v150, s[26:27]
	v_sub_f32_e32 v126, v76, v126
	v_sub_f32_e32 v150, v126, v92
	v_add_f32_e32 v150, v150, v142
	v_cndmask_b32_e64 v110, v126, v150, s[26:27]
	v_sub_f32_e32 v127, v77, v127
	v_sub_f32_e32 v150, v127, v93
	v_add_f32_e32 v150, v150, v143
	v_cndmask_b32_e64 v111, v127, v150, s[26:27]
	v_sub_f32_e32 v128, v78, v128
	v_sub_f32_e32 v150, v128, v94
	v_add_f32_e32 v150, v150, v144
	v_cndmask_b32_e64 v112, v128, v150, s[26:27]
	v_sub_f32_e32 v129, v79, v129
	v_sub_f32_e32 v150, v129, v95
	v_add_f32_e32 v150, v150, v145
	v_cndmask_b32_e64 v113, v129, v150, s[26:27]
	v_sub_f32_e32 v130, v80, v130
	v_sub_f32_e32 v150, v130, v96
	v_add_f32_e32 v150, v150, v146
	v_cndmask_b32_e64 v114, v130, v150, s[26:27]
	v_sub_f32_e32 v131, v81, v131
	v_sub_f32_e32 v150, v131, v97
	v_add_f32_e32 v150, v150, v147
	v_cndmask_b32_e64 v115, v131, v150, s[26:27]
	v_sub_f32_e32 v132, v82, v132
	v_sub_f32_e32 v150, v132, v98
	v_add_f32_e32 v150, v150, v148
	v_cndmask_b32_e64 v116, v132, v150, s[26:27]
	v_sub_f32_e32 v133, v83, v133
	v_sub_f32_e32 v150, v133, v99
	v_add_f32_e32 v150, v150, v149
	v_cndmask_b32_e64 v117, v133, v150, s[26:27]
	v_sub_f32_e32 v84, v68, v84
	v_cndmask_b32_e64 v84, v68, v84, s[26:27]
	v_sub_f32_e32 v85, v69, v85
	v_cndmask_b32_e64 v85, v69, v85, s[26:27]
	v_sub_f32_e32 v86, v70, v86
	v_cndmask_b32_e64 v86, v70, v86, s[26:27]
	v_sub_f32_e32 v87, v71, v87
	v_cndmask_b32_e64 v87, v71, v87, s[26:27]
	v_sub_f32_e32 v88, v72, v88
	v_cndmask_b32_e64 v88, v72, v88, s[26:27]
	v_sub_f32_e32 v89, v73, v89
	v_cndmask_b32_e64 v89, v73, v89, s[26:27]
	v_sub_f32_e32 v90, v74, v90
	v_cndmask_b32_e64 v90, v74, v90, s[26:27]
	v_sub_f32_e32 v91, v75, v91
	v_cndmask_b32_e64 v91, v75, v91, s[26:27]
	v_sub_f32_e32 v92, v76, v92
	v_cndmask_b32_e64 v92, v76, v92, s[26:27]
	v_sub_f32_e32 v93, v77, v93
	v_cndmask_b32_e64 v93, v77, v93, s[26:27]
	v_sub_f32_e32 v94, v78, v94
	v_cndmask_b32_e64 v94, v78, v94, s[26:27]
	v_sub_f32_e32 v95, v79, v95
	v_cndmask_b32_e64 v95, v79, v95, s[26:27]
	v_sub_f32_e32 v96, v80, v96
	v_cndmask_b32_e64 v96, v80, v96, s[26:27]
	v_sub_f32_e32 v97, v81, v97
	v_cndmask_b32_e64 v97, v81, v97, s[26:27]
	v_sub_f32_e32 v98, v82, v98
	v_cndmask_b32_e64 v98, v82, v98, s[26:27]
	v_sub_f32_e32 v99, v83, v99
	v_cndmask_b32_e64 v99, v83, v99, s[26:27]
	s_branch .Lc1e_store
.Lc1e_inner:
	s_waitcnt vmcnt(0)
	v_sub_f32_e32 v84, v68, v84
	v_cndmask_b32_e64 v84, v68, v84, s[26:27]
	v_mov_b32_e32 v102, v84
	v_sub_f32_e32 v85, v69, v85
	v_cndmask_b32_e64 v85, v69, v85, s[26:27]
	v_mov_b32_e32 v103, v85
	v_sub_f32_e32 v86, v70, v86
	v_cndmask_b32_e64 v86, v70, v86, s[26:27]
	v_mov_b32_e32 v104, v86
	v_sub_f32_e32 v87, v71, v87
	v_cndmask_b32_e64 v87, v71, v87, s[26:27]
	v_mov_b32_e32 v105, v87
	v_sub_f32_e32 v88, v72, v88
	v_cndmask_b32_e64 v88, v72, v88, s[26:27]
	v_mov_b32_e32 v106, v88
	v_sub_f32_e32 v89, v73, v89
	v_cndmask_b32_e64 v89, v73, v89, s[26:27]
	v_mov_b32_e32 v107, v89
	v_sub_f32_e32 v90, v74, v90
	v_cndmask_b32_e64 v90, v74, v90, s[26:27]
	v_mov_b32_e32 v108, v90
	v_sub_f32_e32 v91, v75, v91
	v_cndmask_b32_e64 v91, v75, v91, s[26:27]
	v_mov_b32_e32 v109, v91
	v_sub_f32_e32 v92, v76, v92
	v_cndmask_b32_e64 v92, v76, v92, s[26:27]
	v_mov_b32_e32 v110, v92
	v_sub_f32_e32 v93, v77, v93
	v_cndmask_b32_e64 v93, v77, v93, s[26:27]
	v_mov_b32_e32 v111, v93
	v_sub_f32_e32 v94, v78, v94
	v_cndmask_b32_e64 v94, v78, v94, s[26:27]
	v_mov_b32_e32 v112, v94
	v_sub_f32_e32 v95, v79, v95
	v_cndmask_b32_e64 v95, v79, v95, s[26:27]
	v_mov_b32_e32 v113, v95
	v_sub_f32_e32 v96, v80, v96
	v_cndmask_b32_e64 v96, v80, v96, s[26:27]
	v_mov_b32_e32 v114, v96
	v_sub_f32_e32 v97, v81, v97
	v_cndmask_b32_e64 v97, v81, v97, s[26:27]
	v_mov_b32_e32 v115, v97
	v_sub_f32_e32 v98, v82, v98
	v_cndmask_b32_e64 v98, v82, v98, s[26:27]
	v_mov_b32_e32 v116, v98
	v_sub_f32_e32 v99, v83, v99
	v_cndmask_b32_e64 v99, v83, v99, s[26:27]
	v_mov_b32_e32 v117, v99
.Lc1e_store:
	v_fmamk_f32 v50, v50, 0x3a800000, v102
	v_fmamk_f32 v51, v51, 0x3a800000, v103
	v_fmamk_f32 v52, v52, 0x3a800000, v104
	v_fmamk_f32 v53, v53, 0x3a800000, v105
	v_max_f32_e32 v50, 0, v50
	v_max_f32_e32 v51, 0, v51
	v_max_f32_e32 v52, 0, v52
	v_max_f32_e32 v53, 0, v53
	global_store_dwordx4 v100, v[50:53], s[22:23]
	s_add_u32 s22, s22, 0x1000
	s_addc_u32 s23, s23, 0
	v_fmamk_f32 v34, v34, 0x3a800000, v84
	v_fmamk_f32 v35, v35, 0x3a800000, v85
	v_fmamk_f32 v36, v36, 0x3a800000, v86
	v_fmamk_f32 v37, v37, 0x3a800000, v87
	v_max_f32_e32 v34, 0, v34
	v_max_f32_e32 v35, 0, v35
	v_max_f32_e32 v36, 0, v36
	v_max_f32_e32 v37, 0, v37
	global_store_dwordx4 v100, v[34:37], s[22:23]
	s_add_u32 s22, s22, 0x1000
	s_addc_u32 s23, s23, 0
	v_fmamk_f32 v18, v18, 0x3a800000, v84
	v_fmamk_f32 v19, v19, 0x3a800000, v85
	v_fmamk_f32 v20, v20, 0x3a800000, v86
	v_fmamk_f32 v21, v21, 0x3a800000, v87
	v_max_f32_e32 v18, 0, v18
	v_max_f32_e32 v19, 0, v19
	v_max_f32_e32 v20, 0, v20
	v_max_f32_e32 v21, 0, v21
	global_store_dwordx4 v100, v[18:21], s[22:23]
	s_add_u32 s22, s22, 0x1000
	s_addc_u32 s23, s23, 0
	v_fmamk_f32 v2, v2, 0x3a800000, v84
	v_fmamk_f32 v3, v3, 0x3a800000, v85
	v_fmamk_f32 v4, v4, 0x3a800000, v86
	v_fmamk_f32 v5, v5, 0x3a800000, v87
	v_max_f32_e32 v2, 0, v2
	v_max_f32_e32 v3, 0, v3
	v_max_f32_e32 v4, 0, v4
	v_max_f32_e32 v5, 0, v5
	global_store_dwordx4 v100, v[2:5], s[22:23]
	s_add_u32 s22, s22, 0x7d000
	s_addc_u32 s23, s23, 0
	v_fmamk_f32 v54, v54, 0x3a800000, v106
	v_fmamk_f32 v55, v55, 0x3a800000, v107
	v_fmamk_f32 v56, v56, 0x3a800000, v108
	v_fmamk_f32 v57, v57, 0x3a800000, v109
	v_max_f32_e32 v54, 0, v54
	v_max_f32_e32 v55, 0, v55
	v_max_f32_e32 v56, 0, v56
	v_max_f32_e32 v57, 0, v57
	global_store_dwordx4 v100, v[54:57], s[22:23]
	s_add_u32 s22, s22, 0x1000
	s_addc_u32 s23, s23, 0
	v_fmamk_f32 v38, v38, 0x3a800000, v88
	v_fmamk_f32 v39, v39, 0x3a800000, v89
	v_fmamk_f32 v40, v40, 0x3a800000, v90
	v_fmamk_f32 v41, v41, 0x3a800000, v91
	v_max_f32_e32 v38, 0, v38
	v_max_f32_e32 v39, 0, v39
	v_max_f32_e32 v40, 0, v40
	v_max_f32_e32 v41, 0, v41
	global_store_dwordx4 v100, v[38:41], s[22:23]
	s_add_u32 s22, s22, 0x1000
	s_addc_u32 s23, s23, 0
	v_fmamk_f32 v22, v22, 0x3a800000, v88
	v_fmamk_f32 v23, v23, 0x3a800000, v89
	v_fmamk_f32 v24, v24, 0x3a800000, v90
	v_fmamk_f32 v25, v25, 0x3a800000, v91
	v_max_f32_e32 v22, 0, v22
	v_max_f32_e32 v23, 0, v23
	v_max_f32_e32 v24, 0, v24
	v_max_f32_e32 v25, 0, v25
	global_store_dwordx4 v100, v[22:25], s[22:23]
	s_add_u32 s22, s22, 0x1000
	s_addc_u32 s23, s23, 0
	v_fmamk_f32 v6, v6, 0x3a800000, v88
	v_fmamk_f32 v7, v7, 0x3a800000, v89
	v_fmamk_f32 v8, v8, 0x3a800000, v90
	v_fmamk_f32 v9, v9, 0x3a800000, v91
	v_max_f32_e32 v6, 0, v6
	v_max_f32_e32 v7, 0, v7
	v_max_f32_e32 v8, 0, v8
	v_max_f32_e32 v9, 0, v9
	global_store_dwordx4 v100, v[6:9], s[22:23]
	s_add_u32 s22, s22, 0x7d000
	s_addc_u32 s23, s23, 0
	v_fmamk_f32 v58, v58, 0x3a800000, v110
	v_fmamk_f32 v59, v59, 0x3a800000, v111
	v_fmamk_f32 v60, v60, 0x3a800000, v112
	v_fmamk_f32 v61, v61, 0x3a800000, v113
	v_max_f32_e32 v58, 0, v58
	v_max_f32_e32 v59, 0, v59
	v_max_f32_e32 v60, 0, v60
	v_max_f32_e32 v61, 0, v61
	global_store_dwordx4 v100, v[58:61], s[22:23]
	s_add_u32 s22, s22, 0x1000
	s_addc_u32 s23, s23, 0
	v_fmamk_f32 v42, v42, 0x3a800000, v92
	v_fmamk_f32 v43, v43, 0x3a800000, v93
	v_fmamk_f32 v44, v44, 0x3a800000, v94
	v_fmamk_f32 v45, v45, 0x3a800000, v95
	v_max_f32_e32 v42, 0, v42
	v_max_f32_e32 v43, 0, v43
	v_max_f32_e32 v44, 0, v44
	v_max_f32_e32 v45, 0, v45
	global_store_dwordx4 v100, v[42:45], s[22:23]
	s_add_u32 s22, s22, 0x1000
	s_addc_u32 s23, s23, 0
	v_fmamk_f32 v26, v26, 0x3a800000, v92
	v_fmamk_f32 v27, v27, 0x3a800000, v93
	v_fmamk_f32 v28, v28, 0x3a800000, v94
	v_fmamk_f32 v29, v29, 0x3a800000, v95
	v_max_f32_e32 v26, 0, v26
	v_max_f32_e32 v27, 0, v27
	v_max_f32_e32 v28, 0, v28
	v_max_f32_e32 v29, 0, v29
	global_store_dwordx4 v100, v[26:29], s[22:23]
	s_add_u32 s22, s22, 0x1000
	s_addc_u32 s23, s23, 0
	v_fmamk_f32 v10, v10, 0x3a800000, v92
	v_fmamk_f32 v11, v11, 0x3a800000, v93
	v_fmamk_f32 v12, v12, 0x3a800000, v94
	v_fmamk_f32 v13, v13, 0x3a800000, v95
	v_max_f32_e32 v10, 0, v10
	v_max_f32_e32 v11, 0, v11
	v_max_f32_e32 v12, 0, v12
	v_max_f32_e32 v13, 0, v13
	global_store_dwordx4 v100, v[10:13], s[22:23]
	s_add_u32 s22, s22, 0x7d000
	s_addc_u32 s23, s23, 0
	v_fmamk_f32 v62, v62, 0x3a800000, v114
	v_fmamk_f32 v63, v63, 0x3a800000, v115
	v_fmamk_f32 v64, v64, 0x3a800000, v116
	v_fmamk_f32 v65, v65, 0x3a800000, v117
	v_max_f32_e32 v62, 0, v62
	v_max_f32_e32 v63, 0, v63
	v_max_f32_e32 v64, 0, v64
	v_max_f32_e32 v65, 0, v65
	global_store_dwordx4 v100, v[62:65], s[22:23]
	s_add_u32 s22, s22, 0x1000
	s_addc_u32 s23, s23, 0
	v_fmamk_f32 v46, v46, 0x3a800000, v96
	v_fmamk_f32 v47, v47, 0x3a800000, v97
	v_fmamk_f32 v48, v48, 0x3a800000, v98
	v_fmamk_f32 v49, v49, 0x3a800000, v99
	v_max_f32_e32 v46, 0, v46
	v_max_f32_e32 v47, 0, v47
	v_max_f32_e32 v48, 0, v48
	v_max_f32_e32 v49, 0, v49
	global_store_dwordx4 v100, v[46:49], s[22:23]
	s_add_u32 s22, s22, 0x1000
	s_addc_u32 s23, s23, 0
	v_fmamk_f32 v30, v30, 0x3a800000, v96
	v_fmamk_f32 v31, v31, 0x3a800000, v97
	v_fmamk_f32 v32, v32, 0x3a800000, v98
	v_fmamk_f32 v33, v33, 0x3a800000, v99
	v_max_f32_e32 v30, 0, v30
	v_max_f32_e32 v31, 0, v31
	v_max_f32_e32 v32, 0, v32
	v_max_f32_e32 v33, 0, v33
	global_store_dwordx4 v100, v[30:33], s[22:23]
	s_add_u32 s22, s22, 0x1000
	s_addc_u32 s23, s23, 0
	v_fmamk_f32 v14, v14, 0x3a800000, v96
	v_fmamk_f32 v15, v15, 0x3a800000, v97
	v_fmamk_f32 v16, v16, 0x3a800000, v98
	v_fmamk_f32 v17, v17, 0x3a800000, v99
	v_max_f32_e32 v14, 0, v14
	v_max_f32_e32 v15, 0, v15
	v_max_f32_e32 v16, 0, v16
	v_max_f32_e32 v17, 0, v17
	global_store_dwordx4 v100, v[14:17], s[22:23]
	s_endpgm
	.p2align	8

	.amdhsa_kernel _Z11k_conv1_t14I3GeoILi64ELi16ELi3ELi2EEEvPKfPKDv8_DF16_S3_Pfiiii
		.amdhsa_group_segment_fixed_size 46800
		.amdhsa_private_segment_fixed_size 0
		.amdhsa_kernarg_size 48
		.amdhsa_user_sgpr_count 2
		.amdhsa_user_sgpr_dispatch_ptr 0
		.amdhsa_user_sgpr_queue_ptr 0
		.amdhsa_user_sgpr_kernarg_segment_ptr 1
		.amdhsa_user_sgpr_dispatch_id 0
		.amdhsa_user_sgpr_kernarg_preload_length 0
		.amdhsa_user_sgpr_kernarg_preload_offset 0
		.amdhsa_user_sgpr_private_segment_size 0
		.amdhsa_uses_dynamic_stack 0
		.amdhsa_enable_private_segment 0
		.amdhsa_system_sgpr_workgroup_id_x 1
		.amdhsa_system_sgpr_workgroup_id_y 1
		.amdhsa_system_sgpr_workgroup_id_z 1
		.amdhsa_system_sgpr_workgroup_info 0
		.amdhsa_system_vgpr_workitem_id 0
		.amdhsa_next_free_vgpr 168
		.amdhsa_next_free_sgpr 96
		.amdhsa_accum_offset 168
		.amdhsa_reserve_vcc 1
		.amdhsa_float_round_mode_32 0
		.amdhsa_float_round_mode_16_64 0
		.amdhsa_float_denorm_mode_32 3
		.amdhsa_float_denorm_mode_16_64 3
		.amdhsa_dx10_clamp 1
		.amdhsa_ieee_mode 1
		.amdhsa_fp16_overflow 0
		.amdhsa_tg_split 0
		.amdhsa_exception_fp_ieee_invalid_op 0
		.amdhsa_exception_fp_denorm_src 0
		.amdhsa_exception_fp_ieee_div_zero 0
		.amdhsa_exception_fp_ieee_overflow 0
		.amdhsa_exception_fp_ieee_underflow 0
		.amdhsa_exception_fp_ieee_inexact 0
		.amdhsa_exception_int_div_zero 0
	.end_amdhsa_kernel

amdhsa.kernels:
  - .agpr_count:     0
    .args:
      - .offset:         0
        .size:           200
        .value_kind:     by_value
      - .actual_access:  read_only
        .address_space:  global
        .offset:         200
        .size:           8
        .value_kind:     global_buffer
      - .actual_access:  read_only
        .address_space:  global
        .offset:         208
        .size:           8
        .value_kind:     global_buffer
      - .actual_access:  read_only
        .address_space:  global
        .offset:         216
        .size:           8
        .value_kind:     global_buffer
      - .actual_access:  read_only
        .address_space:  global
        .offset:         224
        .size:           8
        .value_kind:     global_buffer
      - .actual_access:  write_only
        .address_space:  global
        .offset:         232
        .size:           8
        .value_kind:     global_buffer
      - .actual_access:  write_only
        .address_space:  global
        .offset:         240
        .size:           8
        .value_kind:     global_buffer
      - .actual_access:  read_only
        .address_space:  global
        .offset:         248
        .size:           8
        .value_kind:     global_buffer
      - .actual_access:  write_only
        .address_space:  global
        .offset:         256
        .size:           8
        .value_kind:     global_buffer
    .group_segment_fixed_size: 37412
    .kernarg_segment_align: 8
    .kernarg_segment_size: 264
    .language:       OpenCL C
    .language_version:
      - 2
      - 0
    .max_flat_workgroup_size: 256
    .name:           _Z6k_prep8PrepArgsPKfS1_S1_S1_PDv8_DF16_PfS1_S4_
    .private_segment_fixed_size: 0
    .sgpr_count:     36
    .sgpr_spill_count: 0
    .symbol:         _Z6k_prep8PrepArgsPKfS1_S1_S1_PDv8_DF16_PfS1_S4_.kd
    .uniform_work_group_size: 1
    .uses_dynamic_stack: false
    .vgpr_count:     44
    .vgpr_spill_count: 0
    .wavefront_size: 64
  - .agpr_count:     0
    .args:
      - .actual_access:  read_only
        .address_space:  global
        .offset:         0
        .size:           8
        .value_kind:     global_buffer
      - .actual_access:  read_only
        .address_space:  global
        .offset:         8
        .size:           8
        .value_kind:     global_buffer
      - .actual_access:  read_only
        .address_space:  global
        .offset:         16
        .size:           8
        .value_kind:     global_buffer
      - .actual_access:  read_only
        .address_space:  global
        .offset:         24
        .size:           8
        .value_kind:     global_buffer
      - .actual_access:  read_only
        .address_space:  global
        .offset:         32
        .size:           8
        .value_kind:     global_buffer
      - .actual_access:  read_only
        .address_space:  global
        .offset:         40
        .size:           8
        .value_kind:     global_buffer
      - .actual_access:  write_only
        .address_space:  global
        .offset:         48
        .size:           8
        .value_kind:     global_buffer
      - .actual_access:  write_only
        .address_space:  global
        .offset:         56
        .size:           8
        .value_kind:     global_buffer
      - .actual_access:  write_only
        .address_space:  global
        .offset:         64
        .size:           8
        .value_kind:     global_buffer
      - .actual_access:  write_only
        .address_space:  global
        .offset:         72
        .size:           8
        .value_kind:     global_buffer
      - .offset:         80
        .size:           4
        .value_kind:     hidden_block_count_x
      - .offset:         84
        .size:           4
        .value_kind:     hidden_block_count_y
      - .offset:         88
        .size:           4
        .value_kind:     hidden_block_count_z
      - .offset:         92
        .size:           2
        .value_kind:     hidden_group_size_x
      - .offset:         94
        .size:           2
        .value_kind:     hidden_group_size_y
      - .offset:         96
        .size:           2
        .value_kind:     hidden_group_size_z
      - .offset:         98
        .size:           2
        .value_kind:     hidden_remainder_x
      - .offset:         100
        .size:           2
        .value_kind:     hidden_remainder_y
      - .offset:         102
        .size:           2
        .value_kind:     hidden_remainder_z
      - .offset:         120
        .size:           8
        .value_kind:     hidden_global_offset_x
      - .offset:         128
        .size:           8
        .value_kind:     hidden_global_offset_y
      - .offset:         136
        .size:           8
        .value_kind:     hidden_global_offset_z
      - .offset:         144
        .size:           2
        .value_kind:     hidden_grid_dims
    .group_segment_fixed_size: 72208
    .kernarg_segment_align: 8
    .kernarg_segment_size: 336
    .language:       OpenCL C
    .language_version:
      - 2
      - 0
    .max_flat_workgroup_size: 256
    .name:           _Z8k_projvqPKfPKDv8_DF16_S0_S3_S0_S0_PfS4_PiS4_
    .private_segment_fixed_size: 0
    .sgpr_count:     49
    .sgpr_spill_count: 0
    .symbol:         _Z8k_projvqPKfPKDv8_DF16_S0_S3_S0_S0_PfS4_PiS4_.kd
    .uniform_work_group_size: 1
    .uses_dynamic_stack: false
    .vgpr_count:     174
    .vgpr_spill_count: 0
    .wavefront_size: 64
  - .agpr_count:     0
    .args:
      - .actual_access:  read_only
        .address_space:  global
        .offset:         0
        .size:           8
        .value_kind:     global_buffer
      - .actual_access:  read_only
        .address_space:  global
        .offset:         8
        .size:           8
        .value_kind:     global_buffer
      - .actual_access:  write_only
        .address_space:  global
        .offset:         16
        .size:           8
        .value_kind:     global_buffer
      - .actual_access:  write_only
        .address_space:  global
        .offset:         24
        .size:           8
        .value_kind:     global_buffer
      - .offset:         32
        .size:           4
        .value_kind:     hidden_block_count_x
      - .offset:         36
        .size:           4
        .value_kind:     hidden_block_count_y
      - .offset:         40
        .size:           4
        .value_kind:     hidden_block_count_z
      - .offset:         44
        .size:           2
        .value_kind:     hidden_group_size_x
      - .offset:         46
        .size:           2
        .value_kind:     hidden_group_size_y
      - .offset:         48
        .size:           2
        .value_kind:     hidden_group_size_z
      - .offset:         50
        .size:           2
        .value_kind:     hidden_remainder_x
      - .offset:         52
        .size:           2
        .value_kind:     hidden_remainder_y
      - .offset:         54
        .size:           2
        .value_kind:     hidden_remainder_z
      - .offset:         72
        .size:           8
        .value_kind:     hidden_global_offset_x
      - .offset:         80
        .size:           8
        .value_kind:     hidden_global_offset_y
      - .offset:         88
        .size:           8
        .value_kind:     hidden_global_offset_z
      - .offset:         96
        .size:           2
        .value_kind:     hidden_grid_dims
    .group_segment_fixed_size: 16
    .kernarg_segment_align: 8
    .kernarg_segment_size: 288
    .language:       OpenCL C
    .language_version:
      - 2
      - 0
    .max_flat_workgroup_size: 256
    .name:           _Z10k_upsamplePKfS0_PfS1_
    .private_segment_fixed_size: 0
    .sgpr_count:     22
    .sgpr_spill_count: 0
    .symbol:         _Z10k_upsamplePKfS0_PfS1_.kd
    .uniform_work_group_size: 1
    .uses_dynamic_stack: false
    .vgpr_count:     44
    .vgpr_spill_count: 0
    .wavefront_size: 64
  - .agpr_count:     0
    .args:
      - .actual_access:  read_only
        .address_space:  global
        .offset:         0
        .size:           8
        .value_kind:     global_buffer
      - .offset:         8
        .size:           4
        .value_kind:     by_value
      - .actual_access:  read_only
        .address_space:  global
        .offset:         16
        .size:           8
        .value_kind:     global_buffer
      - .offset:         24
        .size:           4
        .value_kind:     by_value
      - .actual_access:  write_only
        .address_space:  global
        .offset:         32
        .size:           8
        .value_kind:     global_buffer
    .group_segment_fixed_size: 16384
    .kernarg_segment_align: 8
    .kernarg_segment_size: 40
    .language:       OpenCL C
    .language_version:
      - 2
      - 0
    .max_flat_workgroup_size: 1024
    .name:           _Z10k_finalizePKfiS0_iPf
    .private_segment_fixed_size: 0
    .sgpr_count:     21
    .sgpr_spill_count: 0
    .symbol:         _Z10k_finalizePKfiS0_iPf.kd
    .uniform_work_group_size: 1
    .uses_dynamic_stack: false
    .vgpr_count:     44
    .vgpr_spill_count: 0
    .wavefront_size: 64
  - .agpr_count:     0
    .args:
      - .actual_access:  read_only
        .address_space:  global
        .offset:         0
        .size:           8
        .value_kind:     global_buffer
      - .actual_access:  read_only
        .address_space:  global
        .offset:         8
        .size:           8
        .value_kind:     global_buffer
      - .actual_access:  read_only
        .address_space:  global
        .offset:         16
        .size:           8
        .value_kind:     global_buffer
      - .actual_access:  write_only
        .address_space:  global
        .offset:         24
        .size:           8
        .value_kind:     global_buffer
      - .offset:         32
        .size:           4
        .value_kind:     by_value
      - .offset:         36
        .size:           4
        .value_kind:     by_value
      - .offset:         40
        .size:           4
        .value_kind:     by_value
      - .offset:         44
        .size:           4
        .value_kind:     by_value
    .group_segment_fixed_size: 46800
    .kernarg_segment_align: 8
    .kernarg_segment_size: 48
    .language:       OpenCL C
    .language_version:
      - 2
      - 0
    .max_flat_workgroup_size: 256
    .name:           _Z11k_conv1_t14I3GeoILi64ELi16ELi3ELi2EEEvPKfPKDv8_DF16_S3_Pfiiii
    .private_segment_fixed_size: 0
    .sgpr_count:     66
    .sgpr_spill_count: 0
    .symbol:         _Z11k_conv1_t14I3GeoILi64ELi16ELi3ELi2EEEvPKfPKDv8_DF16_S3_Pfiiii.kd
    .uniform_work_group_size: 1
    .uses_dynamic_stack: false
    .vgpr_count:     168
    .vgpr_spill_count: 0
    .wavefront_size: 64
  - .agpr_count:     0
    .args:
      - .actual_access:  read_only
        .address_space:  global
        .offset:         0
        .size:           8
        .value_kind:     global_buffer
      - .actual_access:  read_only
        .address_space:  global
        .offset:         8
        .size:           8
        .value_kind:     global_buffer
      - .actual_access:  read_only
        .address_space:  global
        .offset:         16
        .size:           8
        .value_kind:     global_buffer
      - .actual_access:  read_only
        .address_space:  global
        .offset:         24
        .size:           8
        .value_kind:     global_buffer
      - .actual_access:  read_only
        .address_space:  global
        .offset:         32
        .size:           8
        .value_kind:     global_buffer
      - .actual_access:  read_only
        .address_space:  global
        .offset:         40
        .size:           8
        .value_kind:     global_buffer
      - .actual_access:  read_only
        .address_space:  global
        .offset:         48
        .size:           8
        .value_kind:     global_buffer
      - .actual_access:  read_only
        .address_space:  global
        .offset:         56
        .size:           8
        .value_kind:     global_buffer
      - .actual_access:  write_only
        .address_space:  global
        .offset:         64
        .size:           8
        .value_kind:     global_buffer
      - .actual_access:  write_only
        .address_space:  global
        .offset:         72
        .size:           8
        .value_kind:     global_buffer
      - .actual_access:  write_only
        .address_space:  global
        .offset:         80
        .size:           8
        .value_kind:     global_buffer
      - .actual_access:  write_only
        .address_space:  global
        .offset:         88
        .size:           8
        .value_kind:     global_buffer
      - .offset:         96
        .size:           4
        .value_kind:     by_value
      - .offset:         100
        .size:           4
        .value_kind:     by_value
      - .offset:         104
        .size:           4
        .value_kind:     hidden_block_count_x
      - .offset:         108
        .size:           4
        .value_kind:     hidden_block_count_y
      - .offset:         112
        .size:           4
        .value_kind:     hidden_block_count_z
      - .offset:         116
        .size:           2
        .value_kind:     hidden_group_size_x
      - .offset:         118
        .size:           2
        .value_kind:     hidden_group_size_y
      - .offset:         120
        .size:           2
        .value_kind:     hidden_group_size_z
      - .offset:         122
        .size:           2
        .value_kind:     hidden_remainder_x
      - .offset:         124
        .size:           2
        .value_kind:     hidden_remainder_y
      - .offset:         126
        .size:           2
        .value_kind:     hidden_remainder_z
      - .offset:         144
        .size:           8
        .value_kind:     hidden_global_offset_x
      - .offset:         152
        .size:           8
        .value_kind:     hidden_global_offset_y
      - .offset:         160
        .size:           8
        .value_kind:     hidden_global_offset_z
      - .offset:         168
        .size:           2
        .value_kind:     hidden_grid_dims
    .group_segment_fixed_size: 139264
    .kernarg_segment_align: 8
    .kernarg_segment_size: 360
    .language:       OpenCL C
    .language_version:
      - 2
      - 0
    .max_flat_workgroup_size: 512
    .name:           _Z7k_c2pvqI3GeoILi128ELi16ELi3ELi2EEEvPKfPKDv8_DF16_S3_S6_S3_S6_S3_S3_PfS7_PiS7_ii
    .private_segment_fixed_size: 0
    .sgpr_count:     64
    .sgpr_spill_count: 0
    .symbol:         _Z7k_c2pvqI3GeoILi128ELi16ELi3ELi2EEEvPKfPKDv8_DF16_S3_S6_S3_S6_S3_S3_PfS7_PiS7_ii.kd
    .uniform_work_group_size: 1
    .uses_dynamic_stack: false
    .vgpr_count:     256
    .vgpr_spill_count: 0
    .wavefront_size: 64
  - .agpr_count:     0
    .args:
      - .actual_access:  read_only
        .address_space:  global
        .offset:         0
        .size:           8
        .value_kind:     global_buffer
      - .actual_access:  read_only
        .address_space:  global
        .offset:         8
        .size:           8
        .value_kind:     global_buffer
      - .actual_access:  read_only
        .address_space:  global
        .offset:         16
        .size:           8
        .value_kind:     global_buffer
      - .actual_access:  read_only
        .address_space:  global
        .offset:         24
        .size:           8
        .value_kind:     global_buffer
      - .actual_access:  read_only
        .address_space:  global
        .offset:         32
        .size:           8
        .value_kind:     global_buffer
      - .actual_access:  read_only
        .address_space:  global
        .offset:         40
        .size:           8
        .value_kind:     global_buffer
      - .actual_access:  write_only
        .address_space:  global
        .offset:         48
        .size:           8
        .value_kind:     global_buffer
      - .offset:         56
        .size:           4
        .value_kind:     by_value
      - .offset:         60
        .size:           4
        .value_kind:     by_value
      - .offset:         64
        .size:           4
        .value_kind:     by_value
      - .offset:         68
        .size:           4
        .value_kind:     by_value
    .group_segment_fixed_size: 67584
    .kernarg_segment_align: 8
    .kernarg_segment_size: 72
    .language:       OpenCL C
    .language_version:
      - 2
      - 0
    .max_flat_workgroup_size: 256
    .name:           _Z12k_recfin_t14I3GeoILi128ELi32ELi3ELi1EEEvPKfPKiPKDv8_DF16_S3_S8_S3_Pfiiii
    .private_segment_fixed_size: 0
    .sgpr_count:     49
    .sgpr_spill_count: 0
    .symbol:         _Z12k_recfin_t14I3GeoILi128ELi32ELi3ELi1EEEvPKfPKiPKDv8_DF16_S3_S8_S3_Pfiiii.kd
    .uniform_work_group_size: 1
    .uses_dynamic_stack: false
    .vgpr_count:     194
    .vgpr_spill_count: 0
    .wavefront_size: 64
